# speedup vs baseline: 1.0151x; 1.0022x over previous
.LBB7_27:
	ds_read_b128 v[128:131], v170
	ds_read_b128 v[132:135], v170 offset:1024
	ds_read_b128 v[136:139], v170 offset:2048
	ds_read_b128 v[140:143], v170 offset:3072
	s_add_u32 s30, s28, 0xfffd0080
	s_addc_u32 s31, s29, -1
	s_cmp_eq_u32 s73, 8
	s_cselect_b32 s35, s9, s31
	s_cselect_b32 s34, s8, s30
	s_cselect_b32 s31, s1, s72
	s_cselect_b32 s30, s0, s71
	s_add_i32 m0, s43, 0xc000
	ds_read_b128 v[158:161], v171
	ds_read_b128 v[176:179], v171 offset:1024
	ds_read_b128 v[180:183], v171 offset:2048
	ds_read_b128 v[184:187], v171 offset:3072
	ds_read_b128 v[188:191], v171 offset:4096
	ds_read_b128 v[192:195], v171 offset:5120
	ds_read_b128 v[196:199], v171 offset:6144
	ds_read_b128 v[200:203], v171 offset:7168
	global_load_lds_dwordx4 v152, s[28:29]
	s_add_i32 m0, s43, 0xe000
	s_nop 0
	global_load_lds_dwordx4 v154, s[28:29]
	s_waitcnt lgkmcnt(8)
	s_barrier
	s_waitcnt lgkmcnt(0)
	v_mfma_f32_16x16x32_f16 v[124:127], v[128:131], v[158:161], v[124:127]
	v_mfma_f32_16x16x32_f16 v[120:123], v[136:139], v[158:161], v[120:123]
	v_mfma_f32_16x16x32_f16 v[108:111], v[128:131], v[180:183], v[108:111]
	v_mfma_f32_16x16x32_f16 v[104:107], v[136:139], v[180:183], v[104:107]
	v_mfma_f32_16x16x32_f16 v[96:99], v[128:131], v[188:191], v[96:99]
	v_mfma_f32_16x16x32_f16 v[88:91], v[136:139], v[188:191], v[88:91]
	v_mfma_f32_16x16x32_f16 v[80:83], v[128:131], v[196:199], v[80:83]
	v_mfma_f32_16x16x32_f16 v[72:75], v[136:139], v[196:199], v[72:75]
	v_mfma_f32_16x16x32_f16 v[124:127], v[132:135], v[176:179], v[124:127]
	v_mfma_f32_16x16x32_f16 v[120:123], v[140:143], v[176:179], v[120:123]
	v_mfma_f32_16x16x32_f16 v[108:111], v[132:135], v[184:187], v[108:111]
	v_mfma_f32_16x16x32_f16 v[104:107], v[140:143], v[184:187], v[104:107]
	v_mfma_f32_16x16x32_f16 v[96:99], v[132:135], v[192:195], v[96:99]
	v_mfma_f32_16x16x32_f16 v[88:91], v[140:143], v[192:195], v[88:91]
	v_mfma_f32_16x16x32_f16 v[80:83], v[132:135], v[200:203], v[80:83]
	v_mfma_f32_16x16x32_f16 v[72:75], v[140:143], v[200:203], v[72:75]
	s_barrier
	s_add_i32 s74, s65, s42
	s_add_u32 s78, s30, 0x80
	s_addc_u32 s79, s31, 0
	s_mov_b32 m0, s74
	ds_read_b128 v[204:207], v172
	ds_read_b128 v[208:211], v172 offset:1024
	ds_read_b128 v[212:215], v172 offset:2048
	ds_read_b128 v[216:219], v172 offset:3072
	global_load_lds_dwordx4 v146, s[30:31]
	s_add_i32 m0, s74, 0x2000
	s_nop 0
	global_load_lds_dwordx4 v150, s[30:31]
	s_barrier
	s_waitcnt lgkmcnt(0)
	v_mfma_f32_16x16x32_f16 v[116:119], v[204:207], v[158:161], v[116:119]
	v_mfma_f32_16x16x32_f16 v[112:115], v[212:215], v[158:161], v[112:115]
	v_mfma_f32_16x16x32_f16 v[100:103], v[204:207], v[180:183], v[100:103]
	v_mfma_f32_16x16x32_f16 v[92:95], v[212:215], v[180:183], v[92:95]
	v_mfma_f32_16x16x32_f16 v[84:87], v[204:207], v[188:191], v[84:87]
	v_mfma_f32_16x16x32_f16 v[76:79], v[212:215], v[188:191], v[76:79]
	v_mfma_f32_16x16x32_f16 v[68:71], v[204:207], v[196:199], v[68:71]
	v_mfma_f32_16x16x32_f16 v[64:67], v[212:215], v[196:199], v[64:67]
	v_mfma_f32_16x16x32_f16 v[116:119], v[208:211], v[176:179], v[116:119]
	v_mfma_f32_16x16x32_f16 v[112:115], v[216:219], v[176:179], v[112:115]
	v_mfma_f32_16x16x32_f16 v[100:103], v[208:211], v[184:187], v[100:103]
	v_mfma_f32_16x16x32_f16 v[92:95], v[216:219], v[184:187], v[92:95]
	v_mfma_f32_16x16x32_f16 v[84:87], v[208:211], v[192:195], v[84:87]
	v_mfma_f32_16x16x32_f16 v[76:79], v[216:219], v[192:195], v[76:79]
	v_mfma_f32_16x16x32_f16 v[68:71], v[208:211], v[200:203], v[68:71]
	v_mfma_f32_16x16x32_f16 v[64:67], v[216:219], v[200:203], v[64:67]
	s_barrier
	s_mov_b32 m0, s43
	s_add_u32 s80, s34, 0x80
	s_addc_u32 s81, s35, 0
	ds_read_b128 v[158:161], v171 offset:16384
	ds_read_b128 v[176:179], v171 offset:17408
	ds_read_b128 v[180:183], v171 offset:18432
	ds_read_b128 v[184:187], v171 offset:19456
	ds_read_b128 v[188:191], v171 offset:20480
	ds_read_b128 v[192:195], v171 offset:21504
	ds_read_b128 v[196:199], v171 offset:22528
	ds_read_b128 v[200:203], v171 offset:23552
	global_load_lds_dwordx4 v144, s[34:35]
	s_mov_b32 m0, s44
	s_nop 0
	global_load_lds_dwordx4 v148, s[34:35]
	s_barrier
	s_waitcnt lgkmcnt(0)
	v_mfma_f32_16x16x32_f16 v[60:63], v[128:131], v[158:161], v[60:63]
	v_mfma_f32_16x16x32_f16 v[56:59], v[136:139], v[158:161], v[56:59]
	v_mfma_f32_16x16x32_f16 v[48:51], v[128:131], v[180:183], v[48:51]
	v_mfma_f32_16x16x32_f16 v[40:43], v[136:139], v[180:183], v[40:43]
	v_mfma_f32_16x16x32_f16 v[32:35], v[128:131], v[188:191], v[32:35]
	v_mfma_f32_16x16x32_f16 v[24:27], v[136:139], v[188:191], v[24:27]
	v_mfma_f32_16x16x32_f16 v[16:19], v[128:131], v[196:199], v[16:19]
	v_mfma_f32_16x16x32_f16 v[8:11], v[136:139], v[196:199], v[8:11]
	v_mfma_f32_16x16x32_f16 v[60:63], v[132:135], v[176:179], v[60:63]
	v_mfma_f32_16x16x32_f16 v[56:59], v[140:143], v[176:179], v[56:59]
	v_mfma_f32_16x16x32_f16 v[48:51], v[132:135], v[184:187], v[48:51]
	v_mfma_f32_16x16x32_f16 v[40:43], v[140:143], v[184:187], v[40:43]
	v_mfma_f32_16x16x32_f16 v[32:35], v[132:135], v[192:195], v[32:35]
	v_mfma_f32_16x16x32_f16 v[24:27], v[140:143], v[192:195], v[24:27]
	v_mfma_f32_16x16x32_f16 v[16:19], v[132:135], v[200:203], v[16:19]
	v_mfma_f32_16x16x32_f16 v[8:11], v[140:143], v[200:203], v[8:11]
	s_barrier
	s_add_u32 s74, s30, 0xc000
	s_addc_u32 s75, s31, 0
	s_add_i32 s76, s66, s42
	s_mov_b32 m0, s76
	s_nop 0
	global_load_lds_dwordx4 v146, s[74:75]
	s_add_i32 m0, s76, 0x2000
	s_nop 0
	global_load_lds_dwordx4 v150, s[74:75]
	s_waitcnt vmcnt(6)
	s_barrier
	v_mfma_f32_16x16x32_f16 v[52:55], v[204:207], v[158:161], v[52:55]
	v_mfma_f32_16x16x32_f16 v[44:47], v[212:215], v[158:161], v[44:47]
	v_mfma_f32_16x16x32_f16 v[36:39], v[204:207], v[180:183], v[36:39]
	v_mfma_f32_16x16x32_f16 v[28:31], v[212:215], v[180:183], v[28:31]
	v_mfma_f32_16x16x32_f16 v[20:23], v[204:207], v[188:191], v[20:23]
	v_mfma_f32_16x16x32_f16 v[12:15], v[212:215], v[188:191], v[12:15]
	v_mfma_f32_16x16x32_f16 v[4:7], v[204:207], v[196:199], v[4:7]
	v_mfma_f32_16x16x32_f16 v[0:3], v[212:215], v[196:199], v[0:3]
	v_mfma_f32_16x16x32_f16 v[52:55], v[208:211], v[176:179], v[52:55]
	v_mfma_f32_16x16x32_f16 v[44:47], v[216:219], v[176:179], v[44:47]
	v_mfma_f32_16x16x32_f16 v[36:39], v[208:211], v[184:187], v[36:39]
	v_mfma_f32_16x16x32_f16 v[28:31], v[216:219], v[184:187], v[28:31]
	v_mfma_f32_16x16x32_f16 v[20:23], v[208:211], v[192:195], v[20:23]
	v_mfma_f32_16x16x32_f16 v[12:15], v[216:219], v[192:195], v[12:15]
	v_mfma_f32_16x16x32_f16 v[4:7], v[208:211], v[200:203], v[4:7]
	v_mfma_f32_16x16x32_f16 v[0:3], v[216:219], v[200:203], v[0:3]
	s_barrier
	s_add_i32 s74, 0, 0x18000
	v_add_u32_e32 v140, s74, v166
	ds_read_b128 v[128:131], v140
	ds_read_b128 v[132:135], v140 offset:1024
	ds_read_b128 v[136:139], v140 offset:2048
	ds_read_b128 v[140:143], v140 offset:3072
	s_add_u32 s34, s34, 0x30000
	s_addc_u32 s35, s35, 0
	s_mov_b32 m0, s45
	ds_read_b128 v[158:161], v171 offset:32768
	ds_read_b128 v[176:179], v171 offset:33792
	ds_read_b128 v[180:183], v171 offset:34816
	ds_read_b128 v[184:187], v171 offset:35840
	ds_read_b128 v[188:191], v171 offset:36864
	ds_read_b128 v[192:195], v171 offset:37888
	ds_read_b128 v[196:199], v171 offset:38912
	ds_read_b128 v[200:203], v171 offset:39936
	global_load_lds_dwordx4 v144, s[34:35]
	s_mov_b32 m0, s46
	s_nop 0
	global_load_lds_dwordx4 v148, s[34:35]
	s_waitcnt lgkmcnt(8)
	s_barrier
	s_waitcnt lgkmcnt(0)
	v_mfma_f32_16x16x32_f16 v[124:127], v[128:131], v[158:161], v[124:127]
	v_mfma_f32_16x16x32_f16 v[120:123], v[136:139], v[158:161], v[120:123]
	v_mfma_f32_16x16x32_f16 v[108:111], v[128:131], v[180:183], v[108:111]
	v_mfma_f32_16x16x32_f16 v[104:107], v[136:139], v[180:183], v[104:107]
	v_mfma_f32_16x16x32_f16 v[96:99], v[128:131], v[188:191], v[96:99]
	v_mfma_f32_16x16x32_f16 v[88:91], v[136:139], v[188:191], v[88:91]
	v_mfma_f32_16x16x32_f16 v[80:83], v[128:131], v[196:199], v[80:83]
	v_mfma_f32_16x16x32_f16 v[72:75], v[136:139], v[196:199], v[72:75]
	v_mfma_f32_16x16x32_f16 v[124:127], v[132:135], v[176:179], v[124:127]
	v_mfma_f32_16x16x32_f16 v[120:123], v[140:143], v[176:179], v[120:123]
	v_mfma_f32_16x16x32_f16 v[108:111], v[132:135], v[184:187], v[108:111]
	v_mfma_f32_16x16x32_f16 v[104:107], v[140:143], v[184:187], v[104:107]
	v_mfma_f32_16x16x32_f16 v[96:99], v[132:135], v[192:195], v[96:99]
	v_mfma_f32_16x16x32_f16 v[88:91], v[140:143], v[192:195], v[88:91]
	v_mfma_f32_16x16x32_f16 v[80:83], v[132:135], v[200:203], v[80:83]
	v_mfma_f32_16x16x32_f16 v[72:75], v[140:143], v[200:203], v[72:75]
	s_barrier
	s_add_i32 s34, 0, 0x1c000
	s_add_i32 s35, s74, s42
	v_add_u32_e32 v175, s34, v166
	s_mov_b32 m0, s35
	ds_read_b128 v[204:207], v175
	ds_read_b128 v[208:211], v175 offset:1024
	ds_read_b128 v[212:215], v175 offset:2048
	ds_read_b128 v[216:219], v175 offset:3072
	global_load_lds_dwordx4 v146, s[78:79]
	s_add_i32 m0, s35, 0x2000
	s_nop 0
	global_load_lds_dwordx4 v150, s[78:79]
	s_barrier
	s_waitcnt lgkmcnt(0)
	v_mfma_f32_16x16x32_f16 v[116:119], v[204:207], v[158:161], v[116:119]
	v_mfma_f32_16x16x32_f16 v[112:115], v[212:215], v[158:161], v[112:115]
	v_mfma_f32_16x16x32_f16 v[100:103], v[204:207], v[180:183], v[100:103]
	v_mfma_f32_16x16x32_f16 v[92:95], v[212:215], v[180:183], v[92:95]
	v_mfma_f32_16x16x32_f16 v[84:87], v[204:207], v[188:191], v[84:87]
	v_mfma_f32_16x16x32_f16 v[76:79], v[212:215], v[188:191], v[76:79]
	v_mfma_f32_16x16x32_f16 v[68:71], v[204:207], v[196:199], v[68:71]
	v_mfma_f32_16x16x32_f16 v[64:67], v[212:215], v[196:199], v[64:67]
	v_mfma_f32_16x16x32_f16 v[116:119], v[208:211], v[176:179], v[116:119]
	v_mfma_f32_16x16x32_f16 v[112:115], v[216:219], v[176:179], v[112:115]
	v_mfma_f32_16x16x32_f16 v[100:103], v[208:211], v[184:187], v[100:103]
	v_mfma_f32_16x16x32_f16 v[92:95], v[216:219], v[184:187], v[92:95]
	v_mfma_f32_16x16x32_f16 v[84:87], v[208:211], v[192:195], v[84:87]
	v_mfma_f32_16x16x32_f16 v[76:79], v[216:219], v[192:195], v[76:79]
	v_mfma_f32_16x16x32_f16 v[68:71], v[208:211], v[200:203], v[68:71]
	v_mfma_f32_16x16x32_f16 v[64:67], v[216:219], v[200:203], v[64:67]
	s_barrier
	s_mov_b32 m0, s49
	ds_read_b128 v[158:161], v171 offset:49152
	ds_read_b128 v[176:179], v171 offset:50176
	ds_read_b128 v[180:183], v171 offset:51200
	ds_read_b128 v[184:187], v171 offset:52224
	ds_read_b128 v[188:191], v171 offset:53248
	ds_read_b128 v[192:195], v171 offset:54272
	ds_read_b128 v[196:199], v171 offset:55296
	ds_read_b128 v[200:203], v171 offset:56320
	global_load_lds_dwordx4 v144, s[80:81]
	s_mov_b32 m0, s50
	s_nop 0
	global_load_lds_dwordx4 v148, s[80:81]
	s_barrier
	s_waitcnt lgkmcnt(0)
	v_mfma_f32_16x16x32_f16 v[60:63], v[128:131], v[158:161], v[60:63]
	v_mfma_f32_16x16x32_f16 v[56:59], v[136:139], v[158:161], v[56:59]
	v_mfma_f32_16x16x32_f16 v[48:51], v[128:131], v[180:183], v[48:51]
	v_mfma_f32_16x16x32_f16 v[40:43], v[136:139], v[180:183], v[40:43]
	v_mfma_f32_16x16x32_f16 v[32:35], v[128:131], v[188:191], v[32:35]
	v_mfma_f32_16x16x32_f16 v[24:27], v[136:139], v[188:191], v[24:27]
	v_mfma_f32_16x16x32_f16 v[16:19], v[128:131], v[196:199], v[16:19]
	v_mfma_f32_16x16x32_f16 v[8:11], v[136:139], v[196:199], v[8:11]
	v_mfma_f32_16x16x32_f16 v[60:63], v[132:135], v[176:179], v[60:63]
	v_mfma_f32_16x16x32_f16 v[56:59], v[140:143], v[176:179], v[56:59]
	v_mfma_f32_16x16x32_f16 v[48:51], v[132:135], v[184:187], v[48:51]
	v_mfma_f32_16x16x32_f16 v[40:43], v[140:143], v[184:187], v[40:43]
	v_mfma_f32_16x16x32_f16 v[32:35], v[132:135], v[192:195], v[32:35]
	v_mfma_f32_16x16x32_f16 v[24:27], v[140:143], v[192:195], v[24:27]
	v_mfma_f32_16x16x32_f16 v[16:19], v[132:135], v[200:203], v[16:19]
	v_mfma_f32_16x16x32_f16 v[8:11], v[140:143], v[200:203], v[8:11]
	s_barrier
	s_add_u32 s30, s30, 0xc080
	s_addc_u32 s31, s31, 0
	s_add_i32 s34, s34, s42
	s_mov_b32 m0, s34
	s_nop 0
	global_load_lds_dwordx4 v146, s[30:31]
	s_add_i32 m0, s34, 0x2000
	s_nop 0
	global_load_lds_dwordx4 v150, s[30:31]
	s_waitcnt vmcnt(6)
	s_barrier
	v_mfma_f32_16x16x32_f16 v[52:55], v[204:207], v[158:161], v[52:55]
	v_mfma_f32_16x16x32_f16 v[44:47], v[212:215], v[158:161], v[44:47]
	v_mfma_f32_16x16x32_f16 v[36:39], v[204:207], v[180:183], v[36:39]
	v_mfma_f32_16x16x32_f16 v[28:31], v[212:215], v[180:183], v[28:31]
	v_mfma_f32_16x16x32_f16 v[20:23], v[204:207], v[188:191], v[20:23]
	v_mfma_f32_16x16x32_f16 v[12:15], v[212:215], v[188:191], v[12:15]
	v_mfma_f32_16x16x32_f16 v[4:7], v[204:207], v[196:199], v[4:7]
	v_mfma_f32_16x16x32_f16 v[0:3], v[212:215], v[196:199], v[0:3]
	v_mfma_f32_16x16x32_f16 v[52:55], v[208:211], v[176:179], v[52:55]
	v_mfma_f32_16x16x32_f16 v[44:47], v[216:219], v[176:179], v[44:47]
	v_mfma_f32_16x16x32_f16 v[36:39], v[208:211], v[184:187], v[36:39]
	v_mfma_f32_16x16x32_f16 v[28:31], v[216:219], v[184:187], v[28:31]
	v_mfma_f32_16x16x32_f16 v[20:23], v[208:211], v[192:195], v[20:23]
	v_mfma_f32_16x16x32_f16 v[12:15], v[216:219], v[192:195], v[12:15]
	v_mfma_f32_16x16x32_f16 v[4:7], v[208:211], v[200:203], v[4:7]
	v_mfma_f32_16x16x32_f16 v[0:3], v[216:219], v[200:203], v[0:3]
	s_barrier
	s_add_i32 s73, s73, 2
	s_add_u32 s28, s28, 0x100
	s_addc_u32 s29, s29, 0
	s_add_u32 s71, s71, 0x100
	s_addc_u32 s72, s72, 0
	s_cmp_gt_u32 s73, 9
	s_cbranch_scc0 .LBB7_27
	s_lshl_b32 s28, s70, 8
	s_add_i32 s28, s28, s48
	s_lshl_b32 s29, s67, 8
	s_or_b32 s29, s29, s51
	s_waitcnt vmcnt(6)
	v_pk_fma_f32 v[126:127], v[126:127], v[226:227], v[236:237] op_sel_hi:[1,0,1]
	v_pk_fma_f32 v[124:125], v[124:125], v[226:227], v[234:235] op_sel_hi:[1,0,1]
	v_pk_fma_f32 v[186:187], v[122:123], v[226:227], v[240:241] op_sel_hi:[1,0,1]
	v_pk_fma_f32 v[122:123], v[120:121], v[226:227], v[238:239] op_sel_hi:[1,0,1]
	v_cvt_pk_f16_f32 v120, v124, v125
	v_cvt_pk_f16_f32 v121, v126, v127
	v_cvt_pk_f16_f32 v122, v122, v123
	v_cvt_pk_f16_f32 v123, v186, v187
	ds_write_b128 v173, v[120:123]
	v_pk_fma_f32 v[118:119], v[118:119], v[226:227], v[244:245] op_sel_hi:[1,0,1]
	v_pk_fma_f32 v[116:117], v[116:117], v[226:227], v[242:243] op_sel_hi:[1,0,1]
	v_pk_fma_f32 v[120:121], v[114:115], v[226:227], v[248:249] op_sel_hi:[1,0,1]
	v_pk_fma_f32 v[114:115], v[112:113], v[226:227], v[246:247] op_sel_hi:[1,0,1]
	v_cvt_pk_f16_f32 v112, v116, v117
	v_cvt_pk_f16_f32 v113, v118, v119
	v_cvt_pk_f16_f32 v114, v114, v115
	v_cvt_pk_f16_f32 v115, v120, v121
	ds_write_b128 v173, v[112:115] offset:64
	v_or_b32_e32 v116, s28, v167
	ds_read_b128 v[112:115], v174
	v_mul_lo_u32 v116, v116, s10
	v_add_u32_e32 v120, s29, v116
	v_lshlrev_b32_e32 v121, 1, v120
	v_add_u32_e32 v122, v121, v168
	ds_read_b128 v[116:119], v174 offset:1152
	s_waitcnt lgkmcnt(0)
	buffer_store_dwordx4 v[112:115], v122, s[20:23], 0 offen nt
	v_pk_fma_f32 v[110:111], v[110:111], v[226:227], v[236:237] op_sel:[0,1,0]
	v_pk_fma_f32 v[108:109], v[108:109], v[226:227], v[234:235] op_sel:[0,1,0]
	v_pk_fma_f32 v[112:113], v[106:107], v[226:227], v[240:241] op_sel:[0,1,0]
	v_pk_fma_f32 v[106:107], v[104:105], v[226:227], v[238:239] op_sel:[0,1,0]
	v_cvt_pk_f16_f32 v104, v108, v109
	v_cvt_pk_f16_f32 v105, v110, v111
	v_cvt_pk_f16_f32 v106, v106, v107
	v_cvt_pk_f16_f32 v107, v112, v113
	ds_write_b128 v173, v[104:107]
	v_pk_fma_f32 v[102:103], v[102:103], v[226:227], v[244:245] op_sel:[0,1,0]
	v_pk_fma_f32 v[100:101], v[100:101], v[226:227], v[242:243] op_sel:[0,1,0]
	v_pk_fma_f32 v[104:105], v[94:95], v[226:227], v[248:249] op_sel:[0,1,0]
	v_pk_fma_f32 v[94:95], v[92:93], v[226:227], v[246:247] op_sel:[0,1,0]
	v_cvt_pk_f16_f32 v92, v100, v101
	v_cvt_pk_f16_f32 v93, v102, v103
	v_cvt_pk_f16_f32 v94, v94, v95
	v_cvt_pk_f16_f32 v95, v104, v105
	ds_write_b128 v173, v[92:95] offset:64
	ds_read_b128 v[92:95], v174
	ds_read_b128 v[100:103], v174 offset:1152
	v_add_u32_e32 v104, s55, v121
	v_add_u32_e32 v114, v121, v169
	v_add_u32_e32 v105, v104, v168
	buffer_store_dwordx4 v[116:119], v114, s[20:23], 0 offen nt
	s_waitcnt lgkmcnt(1)
	buffer_store_dwordx4 v[92:95], v105, s[20:23], 0 offen nt
	v_pk_fma_f32 v[86:87], v[86:87], v[228:229], v[244:245] op_sel_hi:[1,0,1]
	v_pk_fma_f32 v[84:85], v[84:85], v[228:229], v[242:243] op_sel_hi:[1,0,1]
	v_pk_fma_f32 v[92:93], v[98:99], v[228:229], v[236:237] op_sel_hi:[1,0,1]
	v_pk_fma_f32 v[94:95], v[96:97], v[228:229], v[234:235] op_sel_hi:[1,0,1]
	v_pk_fma_f32 v[96:97], v[90:91], v[228:229], v[240:241] op_sel_hi:[1,0,1]
	v_pk_fma_f32 v[90:91], v[88:89], v[228:229], v[238:239] op_sel_hi:[1,0,1]
	v_cvt_pk_f16_f32 v88, v94, v95
	v_cvt_pk_f16_f32 v89, v92, v93
	v_cvt_pk_f16_f32 v90, v90, v91
	v_cvt_pk_f16_f32 v91, v96, v97
	ds_write_b128 v173, v[88:91]
	v_pk_fma_f32 v[88:89], v[78:79], v[228:229], v[248:249] op_sel_hi:[1,0,1]
	v_pk_fma_f32 v[78:79], v[76:77], v[228:229], v[246:247] op_sel_hi:[1,0,1]
	v_cvt_pk_f16_f32 v76, v84, v85
	v_cvt_pk_f16_f32 v77, v86, v87
	v_cvt_pk_f16_f32 v78, v78, v79
	v_cvt_pk_f16_f32 v79, v88, v89
	ds_write_b128 v173, v[76:79] offset:64
	ds_read_b128 v[76:79], v174
	ds_read_b128 v[84:87], v174 offset:1152
	v_add_u32_e32 v88, s55, v104
	v_add_u32_e32 v105, v104, v169
	v_add_u32_e32 v89, v88, v168
	s_waitcnt lgkmcnt(4)
	buffer_store_dwordx4 v[100:103], v105, s[20:23], 0 offen nt
	s_waitcnt lgkmcnt(1)
	buffer_store_dwordx4 v[76:79], v89, s[20:23], 0 offen nt
	v_pk_fma_f32 v[70:71], v[70:71], v[228:229], v[244:245] op_sel:[0,1,0]
	v_pk_fma_f32 v[68:69], v[68:69], v[228:229], v[242:243] op_sel:[0,1,0]
	v_add_u32_e32 v76, v88, v169
	s_waitcnt lgkmcnt(0)
	buffer_store_dwordx4 v[84:87], v76, s[20:23], 0 offen nt
	v_pk_fma_f32 v[76:77], v[82:83], v[228:229], v[236:237] op_sel:[0,1,0]
	v_pk_fma_f32 v[78:79], v[80:81], v[228:229], v[234:235] op_sel:[0,1,0]
	v_pk_fma_f32 v[80:81], v[74:75], v[228:229], v[240:241] op_sel:[0,1,0]
	v_pk_fma_f32 v[74:75], v[72:73], v[228:229], v[238:239] op_sel:[0,1,0]
	v_cvt_pk_f16_f32 v72, v78, v79
	v_cvt_pk_f16_f32 v73, v76, v77
	v_cvt_pk_f16_f32 v74, v74, v75
	v_cvt_pk_f16_f32 v75, v80, v81
	ds_write_b128 v173, v[72:75]
	v_pk_fma_f32 v[72:73], v[66:67], v[228:229], v[248:249] op_sel:[0,1,0]
	v_pk_fma_f32 v[66:67], v[64:65], v[228:229], v[246:247] op_sel:[0,1,0]
	v_cvt_pk_f16_f32 v64, v68, v69
	v_cvt_pk_f16_f32 v65, v70, v71
	v_cvt_pk_f16_f32 v66, v66, v67
	v_cvt_pk_f16_f32 v67, v72, v73
	ds_write_b128 v173, v[64:67] offset:64
	ds_read_b128 v[64:67], v174
	ds_read_b128 v[68:71], v174 offset:1152
	v_add_u32_e32 v72, s56, v120
	v_lshlrev_b32_e32 v73, 1, v72
	v_add_u32_e32 v74, v73, v168
	s_waitcnt lgkmcnt(1)
	buffer_store_dwordx4 v[64:67], v74, s[20:23], 0 offen nt
	v_pk_fma_f32 v[62:63], v[62:63], v[230:231], v[236:237] op_sel_hi:[1,0,1]
	v_pk_fma_f32 v[60:61], v[60:61], v[230:231], v[234:235] op_sel_hi:[1,0,1]
	v_pk_fma_f32 v[64:65], v[58:59], v[230:231], v[240:241] op_sel_hi:[1,0,1]
	v_pk_fma_f32 v[58:59], v[56:57], v[230:231], v[238:239] op_sel_hi:[1,0,1]
	v_cvt_pk_f16_f32 v56, v60, v61
	v_cvt_pk_f16_f32 v57, v62, v63
	v_cvt_pk_f16_f32 v58, v58, v59
	v_cvt_pk_f16_f32 v59, v64, v65
	ds_write_b128 v173, v[56:59]
	v_pk_fma_f32 v[54:55], v[54:55], v[230:231], v[244:245] op_sel_hi:[1,0,1]
	v_pk_fma_f32 v[52:53], v[52:53], v[230:231], v[242:243] op_sel_hi:[1,0,1]
	v_pk_fma_f32 v[56:57], v[46:47], v[230:231], v[248:249] op_sel_hi:[1,0,1]
	v_pk_fma_f32 v[46:47], v[44:45], v[230:231], v[246:247] op_sel_hi:[1,0,1]
	v_cvt_pk_f16_f32 v44, v52, v53
	v_cvt_pk_f16_f32 v45, v54, v55
	v_cvt_pk_f16_f32 v46, v46, v47
	v_cvt_pk_f16_f32 v47, v56, v57
	ds_write_b128 v173, v[44:47] offset:64
	ds_read_b128 v[44:47], v174
	ds_read_b128 v[52:55], v174 offset:1152
	v_add_u32_e32 v56, s62, v88
	v_add_u32_e32 v66, v73, v169
	v_add_u32_e32 v57, v56, v168
	s_waitcnt lgkmcnt(4)
	buffer_store_dwordx4 v[68:71], v66, s[20:23], 0 offen nt
	s_waitcnt lgkmcnt(1)
	buffer_store_dwordx4 v[44:47], v57, s[20:23], 0 offen nt
	v_pk_fma_f32 v[38:39], v[38:39], v[230:231], v[244:245] op_sel:[0,1,0]
	v_pk_fma_f32 v[36:37], v[36:37], v[230:231], v[242:243] op_sel:[0,1,0]
	v_add_u32_e32 v44, v56, v169
	s_waitcnt lgkmcnt(0)
	buffer_store_dwordx4 v[52:55], v44, s[20:23], 0 offen nt
	v_pk_fma_f32 v[44:45], v[50:51], v[230:231], v[236:237] op_sel:[0,1,0]
	v_pk_fma_f32 v[46:47], v[48:49], v[230:231], v[234:235] op_sel:[0,1,0]
	v_pk_fma_f32 v[48:49], v[42:43], v[230:231], v[240:241] op_sel:[0,1,0]
	v_pk_fma_f32 v[42:43], v[40:41], v[230:231], v[238:239] op_sel:[0,1,0]
	v_cvt_pk_f16_f32 v40, v46, v47
	v_cvt_pk_f16_f32 v41, v44, v45
	v_cvt_pk_f16_f32 v42, v42, v43
	v_cvt_pk_f16_f32 v43, v48, v49
	ds_write_b128 v173, v[40:43]
	v_pk_fma_f32 v[40:41], v[30:31], v[230:231], v[248:249] op_sel:[0,1,0]
	v_pk_fma_f32 v[30:31], v[28:29], v[230:231], v[246:247] op_sel:[0,1,0]
	v_cvt_pk_f16_f32 v28, v36, v37
	v_cvt_pk_f16_f32 v29, v38, v39
	v_cvt_pk_f16_f32 v30, v30, v31
	v_cvt_pk_f16_f32 v31, v40, v41
	ds_write_b128 v173, v[28:31] offset:64
	ds_read_b128 v[28:31], v174
	ds_read_b128 v[36:39], v174 offset:1152
	v_add_u32_e32 v40, s63, v72
	v_lshlrev_b32_e32 v41, 1, v40
	v_add_u32_e32 v42, v41, v168
	s_waitcnt lgkmcnt(1)
	buffer_store_dwordx4 v[28:31], v42, s[20:23], 0 offen nt
	v_pk_fma_f32 v[22:23], v[22:23], v[232:233], v[244:245] op_sel_hi:[1,0,1]
	v_pk_fma_f32 v[20:21], v[20:21], v[232:233], v[242:243] op_sel_hi:[1,0,1]
	v_add_u32_e32 v28, v41, v169
	s_waitcnt lgkmcnt(0)
	buffer_store_dwordx4 v[36:39], v28, s[20:23], 0 offen nt
	v_pk_fma_f32 v[28:29], v[34:35], v[232:233], v[236:237] op_sel_hi:[1,0,1]
	v_pk_fma_f32 v[30:31], v[32:33], v[232:233], v[234:235] op_sel_hi:[1,0,1]
	v_pk_fma_f32 v[32:33], v[26:27], v[232:233], v[240:241] op_sel_hi:[1,0,1]
	v_pk_fma_f32 v[26:27], v[24:25], v[232:233], v[238:239] op_sel_hi:[1,0,1]
	v_cvt_pk_f16_f32 v24, v30, v31
	v_cvt_pk_f16_f32 v25, v28, v29
	v_cvt_pk_f16_f32 v26, v26, v27
	v_cvt_pk_f16_f32 v27, v32, v33
	ds_write_b128 v173, v[24:27]
	v_pk_fma_f32 v[24:25], v[14:15], v[232:233], v[248:249] op_sel_hi:[1,0,1]
	v_pk_fma_f32 v[14:15], v[12:13], v[232:233], v[246:247] op_sel_hi:[1,0,1]
	v_cvt_pk_f16_f32 v12, v20, v21
	v_cvt_pk_f16_f32 v13, v22, v23
	v_cvt_pk_f16_f32 v14, v14, v15
	v_cvt_pk_f16_f32 v15, v24, v25
	ds_write_b128 v173, v[12:15] offset:64
	ds_read_b128 v[12:15], v174
	ds_read_b128 v[20:23], v174 offset:1152
	v_add_u32_e32 v24, s64, v40
	v_lshlrev_b32_e32 v25, 1, v24
	v_add_u32_e32 v26, v25, v168
	s_waitcnt lgkmcnt(1)
	buffer_store_dwordx4 v[12:15], v26, s[20:23], 0 offen nt
	v_pk_fma_f32 v[6:7], v[6:7], v[232:233], v[244:245] op_sel:[0,1,0]
	v_pk_fma_f32 v[4:5], v[4:5], v[232:233], v[242:243] op_sel:[0,1,0]
	v_pk_fma_f32 v[12:13], v[18:19], v[232:233], v[236:237] op_sel:[0,1,0]
	v_pk_fma_f32 v[14:15], v[16:17], v[232:233], v[234:235] op_sel:[0,1,0]
	v_pk_fma_f32 v[16:17], v[10:11], v[232:233], v[240:241] op_sel:[0,1,0]
	v_pk_fma_f32 v[10:11], v[8:9], v[232:233], v[238:239] op_sel:[0,1,0]
	v_cvt_pk_f16_f32 v8, v14, v15
	v_cvt_pk_f16_f32 v9, v12, v13
	v_cvt_pk_f16_f32 v10, v10, v11
	v_cvt_pk_f16_f32 v11, v16, v17
	ds_write_b128 v173, v[8:11]
	v_pk_fma_f32 v[8:9], v[2:3], v[232:233], v[248:249] op_sel:[0,1,0]
	v_pk_fma_f32 v[2:3], v[0:1], v[232:233], v[246:247] op_sel:[0,1,0]
	v_cvt_pk_f16_f32 v0, v4, v5
	v_cvt_pk_f16_f32 v1, v6, v7
	v_cvt_pk_f16_f32 v2, v2, v3
	v_cvt_pk_f16_f32 v3, v8, v9
	ds_write_b128 v173, v[0:3] offset:64
	ds_read_b128 v[0:3], v174
	ds_read_b128 v[4:7], v174 offset:1152
	v_add_lshl_u32 v8, v24, s64, 1
	v_add_u32_e32 v25, v25, v169
	v_add_u32_e32 v9, v8, v168
	s_waitcnt lgkmcnt(4)
	buffer_store_dwordx4 v[20:23], v25, s[20:23], 0 offen nt
	s_waitcnt lgkmcnt(1)
	buffer_store_dwordx4 v[0:3], v9, s[20:23], 0 offen nt
	s_mov_b32 s67, s68
	s_mov_b32 s70, s69
	v_add_u32_e32 v0, v8, v169
	s_mov_b64 s[30:31], s[0:1]
	s_mov_b64 s[28:29], s[8:9]
	s_mov_b64 vcc, s[6:7]
	s_waitcnt lgkmcnt(0)
	buffer_store_dwordx4 v[4:7], v0, s[20:23], 0 offen nt
	s_cbranch_vccz .LBB7_12
	s_waitcnt vmcnt(0)
	s_cmpk_gt_u32 s36, 0xff
	s_cbranch_scc1 .LBB7_31
	s_barrier

.LBB7_32:
	s_endpgm
	s_endpgm
	s_endpgm
	s_endpgm
	s_endpgm
	s_endpgm
	s_endpgm
	s_endpgm
	s_endpgm
	s_endpgm
	s_endpgm
	s_endpgm
	s_endpgm
	s_endpgm
	s_endpgm
	s_endpgm
	s_endpgm
	s_endpgm
	s_endpgm
	s_endpgm
	s_endpgm
	s_endpgm
	s_endpgm
	s_endpgm
	s_endpgm
	s_endpgm
	s_endpgm
	s_endpgm
	s_endpgm
	s_endpgm
	s_endpgm
	s_endpgm
	s_endpgm
	s_endpgm
	s_endpgm
	s_endpgm
	s_endpgm

.LBB8_27:
	ds_read_b128 v[72:75], v231
	ds_read_b128 v[80:83], v231 offset:1024
	ds_read_b128 v[88:91], v231 offset:2048
	ds_read_b128 v[92:95], v231 offset:3072
	s_add_u32 s40, s38, 0xfffd0080
	s_addc_u32 s41, s39, -1
	s_cmp_eq_u32 s87, 8
	s_cselect_b32 s43, s9, s41
	s_cselect_b32 s42, s8, s40
	s_cselect_b32 s41, s1, s86
	s_cselect_b32 s40, s0, s85
	s_add_i32 m0, s51, 0xc000
	ds_read_b128 v[136:139], v232
	ds_read_b128 v[148:151], v232 offset:1024
	ds_read_b128 v[152:155], v232 offset:2048
	ds_read_b128 v[156:159], v232 offset:3072
	ds_read_b128 v[160:163], v232 offset:4096
	ds_read_b128 v[164:167], v232 offset:5120
	ds_read_b128 v[168:171], v232 offset:6144
	ds_read_b128 v[172:175], v232 offset:7168
	global_load_lds_dwordx4 v184, s[38:39]
	s_add_i32 m0, s51, 0xe000
	s_nop 0
	global_load_lds_dwordx4 v186, s[38:39]
	s_waitcnt lgkmcnt(8)
	s_barrier
	s_waitcnt lgkmcnt(0)
	v_mfma_f32_16x16x32_f16 v[144:147], v[72:75], v[136:139], v[144:147]
	v_mfma_f32_16x16x32_f16 v[140:143], v[88:91], v[136:139], v[140:143]
	v_mfma_f32_16x16x32_f16 v[124:127], v[72:75], v[152:155], v[124:127]
	v_mfma_f32_16x16x32_f16 v[120:123], v[88:91], v[152:155], v[120:123]
	v_mfma_f32_16x16x32_f16 v[108:111], v[72:75], v[160:163], v[108:111]
	v_mfma_f32_16x16x32_f16 v[104:107], v[88:91], v[160:163], v[104:107]
	v_mfma_f32_16x16x32_f16 v[84:87], v[72:75], v[168:171], v[84:87]
	v_mfma_f32_16x16x32_f16 v[76:79], v[88:91], v[168:171], v[76:79]
	v_mfma_f32_16x16x32_f16 v[144:147], v[80:83], v[148:151], v[144:147]
	v_mfma_f32_16x16x32_f16 v[140:143], v[92:95], v[148:151], v[140:143]
	v_mfma_f32_16x16x32_f16 v[124:127], v[80:83], v[156:159], v[124:127]
	v_mfma_f32_16x16x32_f16 v[120:123], v[92:95], v[156:159], v[120:123]
	v_mfma_f32_16x16x32_f16 v[108:111], v[80:83], v[164:167], v[108:111]
	v_mfma_f32_16x16x32_f16 v[104:107], v[92:95], v[164:167], v[104:107]
	v_mfma_f32_16x16x32_f16 v[84:87], v[80:83], v[172:175], v[84:87]
	v_mfma_f32_16x16x32_f16 v[76:79], v[92:95], v[172:175], v[76:79]
	s_barrier
	s_add_i32 s88, s70, s50
	s_add_u32 s92, s40, 0x80
	s_addc_u32 s93, s41, 0
	s_mov_b32 m0, s88
	ds_read_b128 v[190:193], v233
	ds_read_b128 v[194:197], v233 offset:1024
	ds_read_b128 v[198:201], v233 offset:2048
	ds_read_b128 v[202:205], v233 offset:3072
	global_load_lds_dwordx4 v178, s[40:41]
	s_add_i32 m0, s88, 0x2000
	s_nop 0
	global_load_lds_dwordx4 v182, s[40:41]
	s_barrier
	s_waitcnt lgkmcnt(0)
	v_mfma_f32_16x16x32_f16 v[132:135], v[190:193], v[136:139], v[132:135]
	v_mfma_f32_16x16x32_f16 v[128:131], v[198:201], v[136:139], v[128:131]
	v_mfma_f32_16x16x32_f16 v[116:119], v[190:193], v[152:155], v[116:119]
	v_mfma_f32_16x16x32_f16 v[112:115], v[198:201], v[152:155], v[112:115]
	v_mfma_f32_16x16x32_f16 v[100:103], v[190:193], v[160:163], v[100:103]
	v_mfma_f32_16x16x32_f16 v[96:99], v[198:201], v[160:163], v[96:99]
	v_mfma_f32_16x16x32_f16 v[68:71], v[190:193], v[168:171], v[68:71]
	v_mfma_f32_16x16x32_f16 v[64:67], v[198:201], v[168:171], v[64:67]
	v_mfma_f32_16x16x32_f16 v[132:135], v[194:197], v[148:151], v[132:135]
	v_mfma_f32_16x16x32_f16 v[128:131], v[202:205], v[148:151], v[128:131]
	v_mfma_f32_16x16x32_f16 v[116:119], v[194:197], v[156:159], v[116:119]
	v_mfma_f32_16x16x32_f16 v[112:115], v[202:205], v[156:159], v[112:115]
	v_mfma_f32_16x16x32_f16 v[100:103], v[194:197], v[164:167], v[100:103]
	v_mfma_f32_16x16x32_f16 v[96:99], v[202:205], v[164:167], v[96:99]
	v_mfma_f32_16x16x32_f16 v[68:71], v[194:197], v[172:175], v[68:71]
	v_mfma_f32_16x16x32_f16 v[64:67], v[202:205], v[172:175], v[64:67]
	s_barrier
	s_mov_b32 m0, s51
	s_add_u32 s94, s42, 0x80
	s_addc_u32 s95, s43, 0
	ds_read_b128 v[136:139], v232 offset:16384
	ds_read_b128 v[148:151], v232 offset:17408
	ds_read_b128 v[152:155], v232 offset:18432
	ds_read_b128 v[156:159], v232 offset:19456
	ds_read_b128 v[160:163], v232 offset:20480
	ds_read_b128 v[164:167], v232 offset:21504
	ds_read_b128 v[168:171], v232 offset:22528
	ds_read_b128 v[172:175], v232 offset:23552
	global_load_lds_dwordx4 v176, s[42:43]
	s_mov_b32 m0, s52
	s_nop 0
	global_load_lds_dwordx4 v180, s[42:43]
	s_barrier
	s_waitcnt lgkmcnt(0)
	v_mfma_f32_16x16x32_f16 v[60:63], v[72:75], v[136:139], v[60:63]
	v_mfma_f32_16x16x32_f16 v[56:59], v[88:91], v[136:139], v[56:59]
	v_mfma_f32_16x16x32_f16 v[44:47], v[72:75], v[152:155], v[44:47]
	v_mfma_f32_16x16x32_f16 v[40:43], v[88:91], v[152:155], v[40:43]
	v_mfma_f32_16x16x32_f16 v[28:31], v[72:75], v[160:163], v[28:31]
	v_mfma_f32_16x16x32_f16 v[24:27], v[88:91], v[160:163], v[24:27]
	v_mfma_f32_16x16x32_f16 v[12:15], v[72:75], v[168:171], v[12:15]
	v_mfma_f32_16x16x32_f16 v[8:11], v[88:91], v[168:171], v[8:11]
	v_mfma_f32_16x16x32_f16 v[60:63], v[80:83], v[148:151], v[60:63]
	v_mfma_f32_16x16x32_f16 v[56:59], v[92:95], v[148:151], v[56:59]
	v_mfma_f32_16x16x32_f16 v[44:47], v[80:83], v[156:159], v[44:47]
	v_mfma_f32_16x16x32_f16 v[40:43], v[92:95], v[156:159], v[40:43]
	v_mfma_f32_16x16x32_f16 v[28:31], v[80:83], v[164:167], v[28:31]
	v_mfma_f32_16x16x32_f16 v[24:27], v[92:95], v[164:167], v[24:27]
	v_mfma_f32_16x16x32_f16 v[12:15], v[80:83], v[172:175], v[12:15]
	v_mfma_f32_16x16x32_f16 v[8:11], v[92:95], v[172:175], v[8:11]
	s_barrier
	s_add_u32 s88, s40, 0xc000
	s_addc_u32 s89, s41, 0
	s_add_i32 s90, s71, s50
	s_mov_b32 m0, s90
	s_nop 0
	global_load_lds_dwordx4 v178, s[88:89]
	s_add_i32 m0, s90, 0x2000
	s_nop 0
	global_load_lds_dwordx4 v182, s[88:89]
	s_waitcnt vmcnt(6)
	s_barrier
	v_mfma_f32_16x16x32_f16 v[52:55], v[190:193], v[136:139], v[52:55]
	v_mfma_f32_16x16x32_f16 v[48:51], v[198:201], v[136:139], v[48:51]
	v_mfma_f32_16x16x32_f16 v[36:39], v[190:193], v[152:155], v[36:39]
	v_mfma_f32_16x16x32_f16 v[32:35], v[198:201], v[152:155], v[32:35]
	v_mfma_f32_16x16x32_f16 v[20:23], v[190:193], v[160:163], v[20:23]
	v_mfma_f32_16x16x32_f16 v[16:19], v[198:201], v[160:163], v[16:19]
	v_mfma_f32_16x16x32_f16 v[4:7], v[190:193], v[168:171], v[4:7]
	v_mfma_f32_16x16x32_f16 v[0:3], v[198:201], v[168:171], v[0:3]
	v_mfma_f32_16x16x32_f16 v[52:55], v[194:197], v[148:151], v[52:55]
	v_mfma_f32_16x16x32_f16 v[48:51], v[202:205], v[148:151], v[48:51]
	v_mfma_f32_16x16x32_f16 v[36:39], v[194:197], v[156:159], v[36:39]
	v_mfma_f32_16x16x32_f16 v[32:35], v[202:205], v[156:159], v[32:35]
	v_mfma_f32_16x16x32_f16 v[20:23], v[194:197], v[164:167], v[20:23]
	v_mfma_f32_16x16x32_f16 v[16:19], v[202:205], v[164:167], v[16:19]
	v_mfma_f32_16x16x32_f16 v[4:7], v[194:197], v[172:175], v[4:7]
	v_mfma_f32_16x16x32_f16 v[0:3], v[202:205], v[172:175], v[0:3]
	s_barrier
	s_add_i32 s88, 0, 0x18000
	v_add_u32_e32 v92, s88, v228
	ds_read_b128 v[72:75], v92
	ds_read_b128 v[80:83], v92 offset:1024
	ds_read_b128 v[88:91], v92 offset:2048
	ds_read_b128 v[92:95], v92 offset:3072
	s_add_u32 s42, s42, 0x30000
	s_addc_u32 s43, s43, 0
	s_mov_b32 m0, s53
	ds_read_b128 v[136:139], v232 offset:32768
	ds_read_b128 v[148:151], v232 offset:33792
	ds_read_b128 v[152:155], v232 offset:34816
	ds_read_b128 v[156:159], v232 offset:35840
	ds_read_b128 v[160:163], v232 offset:36864
	ds_read_b128 v[164:167], v232 offset:37888
	ds_read_b128 v[168:171], v232 offset:38912
	ds_read_b128 v[172:175], v232 offset:39936
	global_load_lds_dwordx4 v176, s[42:43]
	s_mov_b32 m0, s54
	s_nop 0
	global_load_lds_dwordx4 v180, s[42:43]
	s_waitcnt lgkmcnt(8)
	s_barrier
	s_waitcnt lgkmcnt(0)
	v_mfma_f32_16x16x32_f16 v[144:147], v[72:75], v[136:139], v[144:147]
	v_mfma_f32_16x16x32_f16 v[140:143], v[88:91], v[136:139], v[140:143]
	v_mfma_f32_16x16x32_f16 v[124:127], v[72:75], v[152:155], v[124:127]
	v_mfma_f32_16x16x32_f16 v[120:123], v[88:91], v[152:155], v[120:123]
	v_mfma_f32_16x16x32_f16 v[108:111], v[72:75], v[160:163], v[108:111]
	v_mfma_f32_16x16x32_f16 v[104:107], v[88:91], v[160:163], v[104:107]
	v_mfma_f32_16x16x32_f16 v[84:87], v[72:75], v[168:171], v[84:87]
	v_mfma_f32_16x16x32_f16 v[76:79], v[88:91], v[168:171], v[76:79]
	v_mfma_f32_16x16x32_f16 v[144:147], v[80:83], v[148:151], v[144:147]
	v_mfma_f32_16x16x32_f16 v[140:143], v[92:95], v[148:151], v[140:143]
	v_mfma_f32_16x16x32_f16 v[124:127], v[80:83], v[156:159], v[124:127]
	v_mfma_f32_16x16x32_f16 v[120:123], v[92:95], v[156:159], v[120:123]
	v_mfma_f32_16x16x32_f16 v[108:111], v[80:83], v[164:167], v[108:111]
	v_mfma_f32_16x16x32_f16 v[104:107], v[92:95], v[164:167], v[104:107]
	v_mfma_f32_16x16x32_f16 v[84:87], v[80:83], v[172:175], v[84:87]
	v_mfma_f32_16x16x32_f16 v[76:79], v[92:95], v[172:175], v[76:79]
	s_barrier
	s_add_i32 s42, 0, 0x1c000
	s_add_i32 s43, s88, s50
	v_add_u32_e32 v202, s42, v228
	s_mov_b32 m0, s43
	ds_read_b128 v[190:193], v202
	ds_read_b128 v[194:197], v202 offset:1024
	ds_read_b128 v[198:201], v202 offset:2048
	ds_read_b128 v[202:205], v202 offset:3072
	global_load_lds_dwordx4 v178, s[92:93]
	s_add_i32 m0, s43, 0x2000
	s_nop 0
	global_load_lds_dwordx4 v182, s[92:93]
	s_barrier
	s_waitcnt lgkmcnt(0)
	v_mfma_f32_16x16x32_f16 v[132:135], v[190:193], v[136:139], v[132:135]
	v_mfma_f32_16x16x32_f16 v[128:131], v[198:201], v[136:139], v[128:131]
	v_mfma_f32_16x16x32_f16 v[116:119], v[190:193], v[152:155], v[116:119]
	v_mfma_f32_16x16x32_f16 v[112:115], v[198:201], v[152:155], v[112:115]
	v_mfma_f32_16x16x32_f16 v[100:103], v[190:193], v[160:163], v[100:103]
	v_mfma_f32_16x16x32_f16 v[96:99], v[198:201], v[160:163], v[96:99]
	v_mfma_f32_16x16x32_f16 v[68:71], v[190:193], v[168:171], v[68:71]
	v_mfma_f32_16x16x32_f16 v[64:67], v[198:201], v[168:171], v[64:67]
	v_mfma_f32_16x16x32_f16 v[132:135], v[194:197], v[148:151], v[132:135]
	v_mfma_f32_16x16x32_f16 v[128:131], v[202:205], v[148:151], v[128:131]
	v_mfma_f32_16x16x32_f16 v[116:119], v[194:197], v[156:159], v[116:119]
	v_mfma_f32_16x16x32_f16 v[112:115], v[202:205], v[156:159], v[112:115]
	v_mfma_f32_16x16x32_f16 v[100:103], v[194:197], v[164:167], v[100:103]
	v_mfma_f32_16x16x32_f16 v[96:99], v[202:205], v[164:167], v[96:99]
	v_mfma_f32_16x16x32_f16 v[68:71], v[194:197], v[172:175], v[68:71]
	v_mfma_f32_16x16x32_f16 v[64:67], v[202:205], v[172:175], v[64:67]
	s_barrier
	s_mov_b32 m0, s59
	ds_read_b128 v[136:139], v232 offset:49152
	ds_read_b128 v[148:151], v232 offset:50176
	ds_read_b128 v[152:155], v232 offset:51200
	ds_read_b128 v[156:159], v232 offset:52224
	ds_read_b128 v[160:163], v232 offset:53248
	ds_read_b128 v[164:167], v232 offset:54272
	ds_read_b128 v[168:171], v232 offset:55296
	ds_read_b128 v[172:175], v232 offset:56320
	global_load_lds_dwordx4 v176, s[94:95]
	s_mov_b32 m0, s60
	s_nop 0
	global_load_lds_dwordx4 v180, s[94:95]
	s_barrier
	s_waitcnt lgkmcnt(0)
	v_mfma_f32_16x16x32_f16 v[60:63], v[72:75], v[136:139], v[60:63]
	v_mfma_f32_16x16x32_f16 v[56:59], v[88:91], v[136:139], v[56:59]
	v_mfma_f32_16x16x32_f16 v[44:47], v[72:75], v[152:155], v[44:47]
	v_mfma_f32_16x16x32_f16 v[40:43], v[88:91], v[152:155], v[40:43]
	v_mfma_f32_16x16x32_f16 v[28:31], v[72:75], v[160:163], v[28:31]
	v_mfma_f32_16x16x32_f16 v[24:27], v[88:91], v[160:163], v[24:27]
	v_mfma_f32_16x16x32_f16 v[12:15], v[72:75], v[168:171], v[12:15]
	v_mfma_f32_16x16x32_f16 v[8:11], v[88:91], v[168:171], v[8:11]
	v_mfma_f32_16x16x32_f16 v[60:63], v[80:83], v[148:151], v[60:63]
	v_mfma_f32_16x16x32_f16 v[56:59], v[92:95], v[148:151], v[56:59]
	v_mfma_f32_16x16x32_f16 v[44:47], v[80:83], v[156:159], v[44:47]
	v_mfma_f32_16x16x32_f16 v[40:43], v[92:95], v[156:159], v[40:43]
	v_mfma_f32_16x16x32_f16 v[28:31], v[80:83], v[164:167], v[28:31]
	v_mfma_f32_16x16x32_f16 v[24:27], v[92:95], v[164:167], v[24:27]
	v_mfma_f32_16x16x32_f16 v[12:15], v[80:83], v[172:175], v[12:15]
	v_mfma_f32_16x16x32_f16 v[8:11], v[92:95], v[172:175], v[8:11]
	s_barrier
	s_add_u32 s40, s40, 0xc080
	s_addc_u32 s41, s41, 0
	s_add_i32 s42, s42, s50
	s_mov_b32 m0, s42
	s_nop 0
	global_load_lds_dwordx4 v178, s[40:41]
	s_add_i32 m0, s42, 0x2000
	s_nop 0
	global_load_lds_dwordx4 v182, s[40:41]
	s_waitcnt vmcnt(6)
	s_barrier
	v_mfma_f32_16x16x32_f16 v[52:55], v[190:193], v[136:139], v[52:55]
	v_mfma_f32_16x16x32_f16 v[48:51], v[198:201], v[136:139], v[48:51]
	v_mfma_f32_16x16x32_f16 v[36:39], v[190:193], v[152:155], v[36:39]
	v_mfma_f32_16x16x32_f16 v[32:35], v[198:201], v[152:155], v[32:35]
	v_mfma_f32_16x16x32_f16 v[20:23], v[190:193], v[160:163], v[20:23]
	v_mfma_f32_16x16x32_f16 v[16:19], v[198:201], v[160:163], v[16:19]
	v_mfma_f32_16x16x32_f16 v[4:7], v[190:193], v[168:171], v[4:7]
	v_mfma_f32_16x16x32_f16 v[0:3], v[198:201], v[168:171], v[0:3]
	v_mfma_f32_16x16x32_f16 v[52:55], v[194:197], v[148:151], v[52:55]
	v_mfma_f32_16x16x32_f16 v[48:51], v[202:205], v[148:151], v[48:51]
	v_mfma_f32_16x16x32_f16 v[36:39], v[194:197], v[156:159], v[36:39]
	v_mfma_f32_16x16x32_f16 v[32:35], v[202:205], v[156:159], v[32:35]
	v_mfma_f32_16x16x32_f16 v[20:23], v[194:197], v[164:167], v[20:23]
	v_mfma_f32_16x16x32_f16 v[16:19], v[202:205], v[164:167], v[16:19]
	v_mfma_f32_16x16x32_f16 v[4:7], v[194:197], v[172:175], v[4:7]
	v_mfma_f32_16x16x32_f16 v[0:3], v[202:205], v[172:175], v[0:3]
	s_barrier
	s_add_i32 s87, s87, 2
	s_add_u32 s38, s38, 0x100
	s_addc_u32 s39, s39, 0
	s_add_u32 s85, s85, 0x100
	s_addc_u32 s86, s86, 0
	s_cmp_gt_u32 s87, 9
	s_cbranch_scc0 .LBB8_27
	s_lshl_b32 s92, s84, 8
	s_add_i32 s92, s92, s58
	s_lshl_b32 s93, s83, 8
	s_or_b32 s93, s93, s61
	v_lshlrev_b32_e32 v237, 2, v226
	s_lshl_b32 s96, s93, 2
	s_add_u32 s94, s16, s96
	s_addc_u32 s95, s17, 0
	global_load_dwordx4 v[72:75], v237, s[94:95] offset:0
	global_load_dwordx4 v[80:83], v237, s[94:95] offset:16
	global_load_dwordx4 v[88:91], v237, s[94:95] offset:128
	global_load_dwordx4 v[92:95], v237, s[94:95] offset:144
	s_add_u32 s94, s18, s96
	s_addc_u32 s95, s19, 0
	global_load_dwordx4 v[136:139], v237, s[94:95] offset:0
	global_load_dwordx4 v[148:151], v237, s[94:95] offset:16
	global_load_dwordx4 v[152:155], v237, s[94:95] offset:128
	global_load_dwordx4 v[156:159], v237, s[94:95] offset:144
	s_add_u32 s94, s14, s96
	s_addc_u32 s95, s15, 0
	global_load_dwordx4 v[160:163], v237, s[94:95] offset:0
	global_load_dwordx4 v[164:167], v237, s[94:95] offset:16
	global_load_dwordx4 v[168:171], v237, s[94:95] offset:128
	global_load_dwordx4 v[172:175], v237, s[94:95] offset:144
	v_lshlrev_b32_e32 v190, 3, v227
	s_lshl_b32 s96, s92, 3
	s_add_u32 s94, s12, s96
	s_addc_u32 s95, s13, 0
	global_load_dwordx2 v[238:239], v190, s[94:95] offset:0
	global_load_dwordx2 v[192:193], v190, s[94:95] offset:128
	global_load_dwordx2 v[194:195], v190, s[94:95] offset:256
	global_load_dwordx2 v[196:197], v190, s[94:95] offset:384
	global_load_dwordx2 v[198:199], v190, s[94:95] offset:1024
	global_load_dwordx2 v[200:201], v190, s[94:95] offset:1152
	global_load_dwordx2 v[202:203], v190, s[94:95] offset:1280
	global_load_dwordx2 v[204:205], v190, s[94:95] offset:1408
	v_mul_u32_u24_e32 v191, 0x600, v227
	v_lshl_add_u32 v191, v226, 1, v191
	s_mul_i32 s96, s92, 0x600
	s_lshl_b32 s97, s93, 1
	s_add_u32 s96, s96, s97
	s_add_u32 s98, s10, s96
	s_addc_u32 s99, s11, 0
	s_add_u32 s94, s98, 0x0
	s_addc_u32 s95, s99, 0
	global_load_dwordx4 v[208:211], v191, s[94:95] offset:0 nt
	global_load_dwordx4 v[212:215], v191, s[94:95] offset:64 nt
	s_add_u32 s94, s98, 0x6000
	s_addc_u32 s95, s99, 0
	global_load_dwordx4 v[216:219], v191, s[94:95] offset:0 nt
	global_load_dwordx4 v[220:223], v191, s[94:95] offset:64 nt
	v_add_u32_e32 v224, s92, v229
	v_mul_u32_u24_e32 v224, 0x600, v224
	s_lshl_b32 s97, s93, 1
	v_add3_u32 v224, v224, v230, s97
	s_lshl_b32 s96, s83, 2
	s_lshr_b32 s97, s61, 6
	s_add_u32 s96, s96, s97
	s_lshl_b32 s96, s96, 19
	s_lshl_b32 s97, s92, 3
	s_add_u32 s96, s96, s97
	s_add_u32 s100, s28, s96
	s_addc_u32 s101, s29, 0
	s_waitcnt vmcnt(19)
	v_pk_add_f32 v[72:73], v[72:73], v[136:137]
	v_pk_add_f32 v[74:75], v[74:75], v[138:139]
	s_waitcnt vmcnt(18)
	v_pk_add_f32 v[80:81], v[80:81], v[148:149]
	v_pk_add_f32 v[82:83], v[82:83], v[150:151]
	s_waitcnt vmcnt(17)
	v_pk_add_f32 v[88:89], v[88:89], v[152:153]
	v_pk_add_f32 v[90:91], v[90:91], v[154:155]
	s_waitcnt vmcnt(16)
	v_pk_add_f32 v[92:93], v[92:93], v[156:157]
	v_pk_add_f32 v[94:95], v[94:95], v[158:159]
	v_pk_add_f32 v[144:145], v[144:145], v[72:73]
	v_pk_add_f32 v[146:147], v[146:147], v[74:75]
	v_pk_add_f32 v[124:125], v[124:125], v[72:73]
	v_pk_add_f32 v[126:127], v[126:127], v[74:75]
	v_pk_add_f32 v[108:109], v[108:109], v[72:73]
	v_pk_add_f32 v[110:111], v[110:111], v[74:75]
	v_pk_add_f32 v[84:85], v[84:85], v[72:73]
	v_pk_add_f32 v[86:87], v[86:87], v[74:75]
	v_pk_add_f32 v[60:61], v[60:61], v[72:73]
	v_pk_add_f32 v[62:63], v[62:63], v[74:75]
	v_pk_add_f32 v[44:45], v[44:45], v[72:73]
	v_pk_add_f32 v[46:47], v[46:47], v[74:75]
	v_pk_add_f32 v[28:29], v[28:29], v[72:73]
	v_pk_add_f32 v[30:31], v[30:31], v[74:75]
	v_pk_add_f32 v[12:13], v[12:13], v[72:73]
	v_pk_add_f32 v[14:15], v[14:15], v[74:75]
	v_pk_add_f32 v[140:141], v[140:141], v[80:81]
	v_pk_add_f32 v[142:143], v[142:143], v[82:83]
	v_pk_add_f32 v[120:121], v[120:121], v[80:81]
	v_pk_add_f32 v[122:123], v[122:123], v[82:83]
	v_pk_add_f32 v[104:105], v[104:105], v[80:81]
	v_pk_add_f32 v[106:107], v[106:107], v[82:83]
	v_pk_add_f32 v[76:77], v[76:77], v[80:81]
	v_pk_add_f32 v[78:79], v[78:79], v[82:83]
	v_pk_add_f32 v[56:57], v[56:57], v[80:81]
	v_pk_add_f32 v[58:59], v[58:59], v[82:83]
	v_pk_add_f32 v[40:41], v[40:41], v[80:81]
	v_pk_add_f32 v[42:43], v[42:43], v[82:83]
	v_pk_add_f32 v[24:25], v[24:25], v[80:81]
	v_pk_add_f32 v[26:27], v[26:27], v[82:83]
	v_pk_add_f32 v[8:9], v[8:9], v[80:81]
	v_pk_add_f32 v[10:11], v[10:11], v[82:83]
	v_pk_add_f32 v[132:133], v[132:133], v[88:89]
	v_pk_add_f32 v[134:135], v[134:135], v[90:91]
	v_pk_add_f32 v[116:117], v[116:117], v[88:89]
	v_pk_add_f32 v[118:119], v[118:119], v[90:91]
	v_pk_add_f32 v[100:101], v[100:101], v[88:89]
	v_pk_add_f32 v[102:103], v[102:103], v[90:91]
	v_pk_add_f32 v[68:69], v[68:69], v[88:89]
	v_pk_add_f32 v[70:71], v[70:71], v[90:91]
	v_pk_add_f32 v[52:53], v[52:53], v[88:89]
	v_pk_add_f32 v[54:55], v[54:55], v[90:91]
	v_pk_add_f32 v[36:37], v[36:37], v[88:89]
	v_pk_add_f32 v[38:39], v[38:39], v[90:91]
	v_pk_add_f32 v[20:21], v[20:21], v[88:89]
	v_pk_add_f32 v[22:23], v[22:23], v[90:91]
	v_pk_add_f32 v[4:5], v[4:5], v[88:89]
	v_pk_add_f32 v[6:7], v[6:7], v[90:91]
	v_pk_add_f32 v[128:129], v[128:129], v[92:93]
	v_pk_add_f32 v[130:131], v[130:131], v[94:95]
	v_pk_add_f32 v[112:113], v[112:113], v[92:93]
	v_pk_add_f32 v[114:115], v[114:115], v[94:95]
	v_pk_add_f32 v[96:97], v[96:97], v[92:93]
	v_pk_add_f32 v[98:99], v[98:99], v[94:95]
	v_pk_add_f32 v[64:65], v[64:65], v[92:93]
	v_pk_add_f32 v[66:67], v[66:67], v[94:95]
	v_pk_add_f32 v[48:49], v[48:49], v[92:93]
	v_pk_add_f32 v[50:51], v[50:51], v[94:95]
	v_pk_add_f32 v[32:33], v[32:33], v[92:93]
	v_pk_add_f32 v[34:35], v[34:35], v[94:95]
	v_pk_add_f32 v[16:17], v[16:17], v[92:93]
	v_pk_add_f32 v[18:19], v[18:19], v[94:95]
	v_pk_add_f32 v[0:1], v[0:1], v[92:93]
	v_pk_add_f32 v[2:3], v[2:3], v[94:95]
	s_add_u32 s94, s98, 0xc000
	s_addc_u32 s95, s99, 0
	global_load_dwordx4 v[240:243], v191, s[94:95] offset:0 nt
	global_load_dwordx4 v[244:247], v191, s[94:95] offset:64 nt
	s_add_u32 s94, s98, 0x12000
	s_addc_u32 s95, s99, 0
	global_load_dwordx4 v[248:251], v191, s[94:95] offset:0 nt
	global_load_dwordx4 v[252:255], v191, s[94:95] offset:64 nt
	s_add_u32 s94, s98, 0x30000
	s_addc_u32 s95, s99, 0
	global_load_dwordx4 v[136:139], v191, s[94:95] offset:0 nt
	global_load_dwordx4 v[148:151], v191, s[94:95] offset:64 nt
	s_add_u32 s94, s98, 0x36000
	s_addc_u32 s95, s99, 0
	global_load_dwordx4 v[152:155], v191, s[94:95] offset:0 nt
	global_load_dwordx4 v[156:159], v191, s[94:95] offset:64 nt
	s_waitcnt vmcnt(19)
	s_waitcnt vmcnt(11)
	v_cvt_f32_f16_e32 v72, v208
	v_cvt_f32_f16_sdwa v73, v208 dst_sel:DWORD dst_unused:UNUSED_PAD src0_sel:WORD_1
	v_cvt_f32_f16_e32 v74, v209
	v_cvt_f32_f16_sdwa v75, v209 dst_sel:DWORD dst_unused:UNUSED_PAD src0_sel:WORD_1
	v_cvt_f32_f16_e32 v80, v210
	v_cvt_f32_f16_sdwa v81, v210 dst_sel:DWORD dst_unused:UNUSED_PAD src0_sel:WORD_1
	v_cvt_f32_f16_e32 v82, v211
	v_cvt_f32_f16_sdwa v83, v211 dst_sel:DWORD dst_unused:UNUSED_PAD src0_sel:WORD_1
	v_sub_f32_e32 v72, v72, v238
	v_sub_f32_e32 v73, v73, v238
	v_sub_f32_e32 v74, v74, v238
	v_sub_f32_e32 v75, v75, v238
	v_sub_f32_e32 v80, v80, v238
	v_sub_f32_e32 v81, v81, v238
	v_sub_f32_e32 v82, v82, v238
	v_sub_f32_e32 v83, v83, v238
	v_pk_mul_f32 v[72:73], v[238:239], v[72:73] op_sel:[1,0]
	v_pk_mul_f32 v[74:75], v[238:239], v[74:75] op_sel:[1,0]
	v_pk_mul_f32 v[80:81], v[238:239], v[80:81] op_sel:[1,0]
	v_pk_mul_f32 v[82:83], v[238:239], v[82:83] op_sel:[1,0]
	v_pk_fma_f32 v[144:145], v[72:73], v[160:161], v[144:145]
	v_pk_fma_f32 v[146:147], v[74:75], v[162:163], v[146:147]
	v_pk_fma_f32 v[140:141], v[80:81], v[164:165], v[140:141]
	v_pk_fma_f32 v[142:143], v[82:83], v[166:167], v[142:143]
	v_cvt_pk_f16_f32 v144, v144, v145
	v_cvt_pk_f16_f32 v145, v146, v147
	v_cvt_pk_f16_f32 v146, v140, v141
	v_cvt_pk_f16_f32 v147, v142, v143
	ds_write_b128 v235, v[144:147]
	v_fma_mix_f32 v206, v144, 1.0, 0 op_sel_hi:[1,0,0]
	v_fma_mix_f32 v207, v144, v144, 0 op_sel_hi:[1,1,0]
	v_fma_mix_f32 v206, v144, 1.0, v206 op_sel:[1,0,0] op_sel_hi:[1,0,0]
	v_fma_mix_f32 v207, v144, v144, v207 op_sel:[1,1,0] op_sel_hi:[1,1,0]
	v_fma_mix_f32 v206, v145, 1.0, v206 op_sel_hi:[1,0,0]
	v_fma_mix_f32 v207, v145, v145, v207 op_sel_hi:[1,1,0]
	v_fma_mix_f32 v206, v145, 1.0, v206 op_sel:[1,0,0] op_sel_hi:[1,0,0]
	v_fma_mix_f32 v207, v145, v145, v207 op_sel:[1,1,0] op_sel_hi:[1,1,0]
	v_fma_mix_f32 v206, v146, 1.0, v206 op_sel_hi:[1,0,0]
	v_fma_mix_f32 v207, v146, v146, v207 op_sel_hi:[1,1,0]
	v_fma_mix_f32 v206, v146, 1.0, v206 op_sel:[1,0,0] op_sel_hi:[1,0,0]
	v_fma_mix_f32 v207, v146, v146, v207 op_sel:[1,1,0] op_sel_hi:[1,1,0]
	v_fma_mix_f32 v206, v147, 1.0, v206 op_sel_hi:[1,0,0]
	v_fma_mix_f32 v207, v147, v147, v207 op_sel_hi:[1,1,0]
	v_fma_mix_f32 v206, v147, 1.0, v206 op_sel:[1,0,0] op_sel_hi:[1,0,0]
	v_fma_mix_f32 v207, v147, v147, v207 op_sel:[1,1,0] op_sel_hi:[1,1,0]
	s_waitcnt vmcnt(10)
	v_cvt_f32_f16_e32 v72, v212
	v_cvt_f32_f16_sdwa v73, v212 dst_sel:DWORD dst_unused:UNUSED_PAD src0_sel:WORD_1
	v_cvt_f32_f16_e32 v74, v213
	v_cvt_f32_f16_sdwa v75, v213 dst_sel:DWORD dst_unused:UNUSED_PAD src0_sel:WORD_1
	v_cvt_f32_f16_e32 v80, v214
	v_cvt_f32_f16_sdwa v81, v214 dst_sel:DWORD dst_unused:UNUSED_PAD src0_sel:WORD_1
	v_cvt_f32_f16_e32 v82, v215
	v_cvt_f32_f16_sdwa v83, v215 dst_sel:DWORD dst_unused:UNUSED_PAD src0_sel:WORD_1
	v_sub_f32_e32 v72, v72, v238
	v_sub_f32_e32 v73, v73, v238
	v_sub_f32_e32 v74, v74, v238
	v_sub_f32_e32 v75, v75, v238
	v_sub_f32_e32 v80, v80, v238
	v_sub_f32_e32 v81, v81, v238
	v_sub_f32_e32 v82, v82, v238
	v_sub_f32_e32 v83, v83, v238
	v_pk_mul_f32 v[72:73], v[238:239], v[72:73] op_sel:[1,0]
	v_pk_mul_f32 v[74:75], v[238:239], v[74:75] op_sel:[1,0]
	v_pk_mul_f32 v[80:81], v[238:239], v[80:81] op_sel:[1,0]
	v_pk_mul_f32 v[82:83], v[238:239], v[82:83] op_sel:[1,0]
	v_pk_fma_f32 v[132:133], v[72:73], v[168:169], v[132:133]
	v_pk_fma_f32 v[134:135], v[74:75], v[170:171], v[134:135]
	v_pk_fma_f32 v[128:129], v[80:81], v[172:173], v[128:129]
	v_pk_fma_f32 v[130:131], v[82:83], v[174:175], v[130:131]
	v_cvt_pk_f16_f32 v132, v132, v133
	v_cvt_pk_f16_f32 v133, v134, v135
	v_cvt_pk_f16_f32 v134, v128, v129
	v_cvt_pk_f16_f32 v135, v130, v131
	ds_write_b128 v235, v[132:135] offset:64
	v_fma_mix_f32 v206, v132, 1.0, v206 op_sel_hi:[1,0,0]
	v_fma_mix_f32 v207, v132, v132, v207 op_sel_hi:[1,1,0]
	v_fma_mix_f32 v206, v132, 1.0, v206 op_sel:[1,0,0] op_sel_hi:[1,0,0]
	v_fma_mix_f32 v207, v132, v132, v207 op_sel:[1,1,0] op_sel_hi:[1,1,0]
	v_fma_mix_f32 v206, v133, 1.0, v206 op_sel_hi:[1,0,0]
	v_fma_mix_f32 v207, v133, v133, v207 op_sel_hi:[1,1,0]
	v_fma_mix_f32 v206, v133, 1.0, v206 op_sel:[1,0,0] op_sel_hi:[1,0,0]
	v_fma_mix_f32 v207, v133, v133, v207 op_sel:[1,1,0] op_sel_hi:[1,1,0]
	v_fma_mix_f32 v206, v134, 1.0, v206 op_sel_hi:[1,0,0]
	v_fma_mix_f32 v207, v134, v134, v207 op_sel_hi:[1,1,0]
	v_fma_mix_f32 v206, v134, 1.0, v206 op_sel:[1,0,0] op_sel_hi:[1,0,0]
	v_fma_mix_f32 v207, v134, v134, v207 op_sel:[1,1,0] op_sel_hi:[1,1,0]
	v_fma_mix_f32 v206, v135, 1.0, v206 op_sel_hi:[1,0,0]
	v_fma_mix_f32 v207, v135, v135, v207 op_sel_hi:[1,1,0]
	v_fma_mix_f32 v206, v135, 1.0, v206 op_sel:[1,0,0] op_sel_hi:[1,0,0]
	v_fma_mix_f32 v207, v135, v135, v207 op_sel:[1,1,0] op_sel_hi:[1,1,0]
	ds_read_b128 v[88:91], v236
	ds_read_b128 v[92:95], v236 offset:1152
	s_waitcnt vmcnt(9)
	v_cvt_f32_f16_e32 v72, v216
	v_cvt_f32_f16_sdwa v73, v216 dst_sel:DWORD dst_unused:UNUSED_PAD src0_sel:WORD_1
	v_cvt_f32_f16_e32 v74, v217
	v_cvt_f32_f16_sdwa v75, v217 dst_sel:DWORD dst_unused:UNUSED_PAD src0_sel:WORD_1
	v_cvt_f32_f16_e32 v80, v218
	v_cvt_f32_f16_sdwa v81, v218 dst_sel:DWORD dst_unused:UNUSED_PAD src0_sel:WORD_1
	v_cvt_f32_f16_e32 v82, v219
	v_cvt_f32_f16_sdwa v83, v219 dst_sel:DWORD dst_unused:UNUSED_PAD src0_sel:WORD_1
	v_sub_f32_e32 v72, v72, v192
	v_sub_f32_e32 v73, v73, v192
	v_sub_f32_e32 v74, v74, v192
	v_sub_f32_e32 v75, v75, v192
	v_sub_f32_e32 v80, v80, v192
	v_sub_f32_e32 v81, v81, v192
	v_sub_f32_e32 v82, v82, v192
	v_sub_f32_e32 v83, v83, v192
	v_pk_mul_f32 v[72:73], v[192:193], v[72:73] op_sel:[1,0]
	v_pk_mul_f32 v[74:75], v[192:193], v[74:75] op_sel:[1,0]
	v_pk_mul_f32 v[80:81], v[192:193], v[80:81] op_sel:[1,0]
	v_pk_mul_f32 v[82:83], v[192:193], v[82:83] op_sel:[1,0]
	v_pk_fma_f32 v[124:125], v[72:73], v[160:161], v[124:125]
	v_pk_fma_f32 v[126:127], v[74:75], v[162:163], v[126:127]
	v_pk_fma_f32 v[120:121], v[80:81], v[164:165], v[120:121]
	v_pk_fma_f32 v[122:123], v[82:83], v[166:167], v[122:123]
	v_cvt_pk_f16_f32 v124, v124, v125
	v_cvt_pk_f16_f32 v125, v126, v127
	v_cvt_pk_f16_f32 v126, v120, v121
	v_cvt_pk_f16_f32 v127, v122, v123
	s_waitcnt lgkmcnt(0)
	buffer_store_dwordx4 v[88:91], v224, s[24:27], 0 offen nt
	v_add_u32_e32 v82, 0x3000, v224
	buffer_store_dwordx4 v[92:95], v82, s[24:27], 0 offen nt
	ds_write_b128 v235, v[124:127]
	v_fma_mix_f32 v140, v124, 1.0, 0 op_sel_hi:[1,0,0]
	v_fma_mix_f32 v141, v124, v124, 0 op_sel_hi:[1,1,0]
	v_fma_mix_f32 v140, v124, 1.0, v140 op_sel:[1,0,0] op_sel_hi:[1,0,0]
	v_fma_mix_f32 v141, v124, v124, v141 op_sel:[1,1,0] op_sel_hi:[1,1,0]
	v_fma_mix_f32 v140, v125, 1.0, v140 op_sel_hi:[1,0,0]
	v_fma_mix_f32 v141, v125, v125, v141 op_sel_hi:[1,1,0]
	v_fma_mix_f32 v140, v125, 1.0, v140 op_sel:[1,0,0] op_sel_hi:[1,0,0]
	v_fma_mix_f32 v141, v125, v125, v141 op_sel:[1,1,0] op_sel_hi:[1,1,0]
	v_fma_mix_f32 v140, v126, 1.0, v140 op_sel_hi:[1,0,0]
	v_fma_mix_f32 v141, v126, v126, v141 op_sel_hi:[1,1,0]
	v_fma_mix_f32 v140, v126, 1.0, v140 op_sel:[1,0,0] op_sel_hi:[1,0,0]
	v_fma_mix_f32 v141, v126, v126, v141 op_sel:[1,1,0] op_sel_hi:[1,1,0]
	v_fma_mix_f32 v140, v127, 1.0, v140 op_sel_hi:[1,0,0]
	v_fma_mix_f32 v141, v127, v127, v141 op_sel_hi:[1,1,0]
	v_fma_mix_f32 v140, v127, 1.0, v140 op_sel:[1,0,0] op_sel_hi:[1,0,0]
	v_fma_mix_f32 v141, v127, v127, v141 op_sel:[1,1,0] op_sel_hi:[1,1,0]
	s_waitcnt vmcnt(10)
	v_cvt_f32_f16_e32 v72, v220
	v_cvt_f32_f16_sdwa v73, v220 dst_sel:DWORD dst_unused:UNUSED_PAD src0_sel:WORD_1
	v_cvt_f32_f16_e32 v74, v221
	v_cvt_f32_f16_sdwa v75, v221 dst_sel:DWORD dst_unused:UNUSED_PAD src0_sel:WORD_1
	v_cvt_f32_f16_e32 v80, v222
	v_cvt_f32_f16_sdwa v81, v222 dst_sel:DWORD dst_unused:UNUSED_PAD src0_sel:WORD_1
	v_cvt_f32_f16_e32 v82, v223
	v_cvt_f32_f16_sdwa v83, v223 dst_sel:DWORD dst_unused:UNUSED_PAD src0_sel:WORD_1
	v_sub_f32_e32 v72, v72, v192
	v_sub_f32_e32 v73, v73, v192
	v_sub_f32_e32 v74, v74, v192
	v_sub_f32_e32 v75, v75, v192
	v_sub_f32_e32 v80, v80, v192
	v_sub_f32_e32 v81, v81, v192
	v_sub_f32_e32 v82, v82, v192
	v_sub_f32_e32 v83, v83, v192
	v_pk_mul_f32 v[72:73], v[192:193], v[72:73] op_sel:[1,0]
	v_pk_mul_f32 v[74:75], v[192:193], v[74:75] op_sel:[1,0]
	v_pk_mul_f32 v[80:81], v[192:193], v[80:81] op_sel:[1,0]
	v_pk_mul_f32 v[82:83], v[192:193], v[82:83] op_sel:[1,0]
	v_pk_fma_f32 v[116:117], v[72:73], v[168:169], v[116:117]
	v_pk_fma_f32 v[118:119], v[74:75], v[170:171], v[118:119]
	v_pk_fma_f32 v[112:113], v[80:81], v[172:173], v[112:113]
	v_pk_fma_f32 v[114:115], v[82:83], v[174:175], v[114:115]
	v_cvt_pk_f16_f32 v116, v116, v117
	v_cvt_pk_f16_f32 v117, v118, v119
	v_cvt_pk_f16_f32 v118, v112, v113
	v_cvt_pk_f16_f32 v119, v114, v115
	ds_write_b128 v235, v[116:119] offset:64
	v_fma_mix_f32 v140, v116, 1.0, v140 op_sel_hi:[1,0,0]
	v_fma_mix_f32 v141, v116, v116, v141 op_sel_hi:[1,1,0]
	v_fma_mix_f32 v140, v116, 1.0, v140 op_sel:[1,0,0] op_sel_hi:[1,0,0]
	v_fma_mix_f32 v141, v116, v116, v141 op_sel:[1,1,0] op_sel_hi:[1,1,0]
	v_fma_mix_f32 v140, v117, 1.0, v140 op_sel_hi:[1,0,0]
	v_fma_mix_f32 v141, v117, v117, v141 op_sel_hi:[1,1,0]
	v_fma_mix_f32 v140, v117, 1.0, v140 op_sel:[1,0,0] op_sel_hi:[1,0,0]
	v_fma_mix_f32 v141, v117, v117, v141 op_sel:[1,1,0] op_sel_hi:[1,1,0]
	v_fma_mix_f32 v140, v118, 1.0, v140 op_sel_hi:[1,0,0]
	v_fma_mix_f32 v141, v118, v118, v141 op_sel_hi:[1,1,0]
	v_fma_mix_f32 v140, v118, 1.0, v140 op_sel:[1,0,0] op_sel_hi:[1,0,0]
	v_fma_mix_f32 v141, v118, v118, v141 op_sel:[1,1,0] op_sel_hi:[1,1,0]
	v_fma_mix_f32 v140, v119, 1.0, v140 op_sel_hi:[1,0,0]
	v_fma_mix_f32 v141, v119, v119, v141 op_sel_hi:[1,1,0]
	v_fma_mix_f32 v140, v119, 1.0, v140 op_sel:[1,0,0] op_sel_hi:[1,0,0]
	v_fma_mix_f32 v141, v119, v119, v141 op_sel:[1,1,0] op_sel_hi:[1,1,0]
	ds_read_b128 v[208:211], v236
	ds_read_b128 v[128:131], v236 offset:1152
	s_add_u32 s94, s98, 0x3c000
	s_addc_u32 s95, s99, 0
	global_load_dwordx4 v[212:215], v191, s[94:95] offset:0 nt
	global_load_dwordx4 v[144:147], v191, s[94:95] offset:64 nt
	s_add_u32 s94, s98, 0x42000
	s_addc_u32 s95, s99, 0
	global_load_dwordx4 v[132:135], v191, s[94:95] offset:0 nt
	global_load_dwordx4 v[88:91], v191, s[94:95] offset:64 nt
	s_waitcnt vmcnt(13)
	v_cvt_f32_f16_e32 v72, v240
	v_cvt_f32_f16_sdwa v73, v240 dst_sel:DWORD dst_unused:UNUSED_PAD src0_sel:WORD_1
	v_cvt_f32_f16_e32 v74, v241
	v_cvt_f32_f16_sdwa v75, v241 dst_sel:DWORD dst_unused:UNUSED_PAD src0_sel:WORD_1
	v_cvt_f32_f16_e32 v80, v242
	v_cvt_f32_f16_sdwa v81, v242 dst_sel:DWORD dst_unused:UNUSED_PAD src0_sel:WORD_1
	v_cvt_f32_f16_e32 v82, v243
	v_cvt_f32_f16_sdwa v83, v243 dst_sel:DWORD dst_unused:UNUSED_PAD src0_sel:WORD_1
	v_sub_f32_e32 v72, v72, v194
	v_sub_f32_e32 v73, v73, v194
	v_sub_f32_e32 v74, v74, v194
	v_sub_f32_e32 v75, v75, v194
	v_sub_f32_e32 v80, v80, v194
	v_sub_f32_e32 v81, v81, v194
	v_sub_f32_e32 v82, v82, v194
	v_sub_f32_e32 v83, v83, v194
	v_pk_mul_f32 v[72:73], v[194:195], v[72:73] op_sel:[1,0]
	v_pk_mul_f32 v[74:75], v[194:195], v[74:75] op_sel:[1,0]
	v_pk_mul_f32 v[80:81], v[194:195], v[80:81] op_sel:[1,0]
	v_pk_mul_f32 v[82:83], v[194:195], v[82:83] op_sel:[1,0]
	v_pk_fma_f32 v[108:109], v[72:73], v[160:161], v[108:109]
	v_pk_fma_f32 v[110:111], v[74:75], v[162:163], v[110:111]
	v_pk_fma_f32 v[104:105], v[80:81], v[164:165], v[104:105]
	v_pk_fma_f32 v[106:107], v[82:83], v[166:167], v[106:107]
	v_cvt_pk_f16_f32 v108, v108, v109
	v_cvt_pk_f16_f32 v109, v110, v111
	v_cvt_pk_f16_f32 v110, v104, v105
	v_cvt_pk_f16_f32 v111, v106, v107
	s_waitcnt lgkmcnt(0)
	v_add_u32_e32 v83, 0x6000, v224
	buffer_store_dwordx4 v[208:211], v83, s[24:27], 0 offen nt
	v_add_u32_e32 v82, 0x9000, v224
	buffer_store_dwordx4 v[128:131], v82, s[24:27], 0 offen nt
	ds_write_b128 v235, v[108:111]
	v_fma_mix_f32 v142, v108, 1.0, 0 op_sel_hi:[1,0,0]
	v_fma_mix_f32 v143, v108, v108, 0 op_sel_hi:[1,1,0]
	v_fma_mix_f32 v142, v108, 1.0, v142 op_sel:[1,0,0] op_sel_hi:[1,0,0]
	v_fma_mix_f32 v143, v108, v108, v143 op_sel:[1,1,0] op_sel_hi:[1,1,0]
	v_fma_mix_f32 v142, v109, 1.0, v142 op_sel_hi:[1,0,0]
	v_fma_mix_f32 v143, v109, v109, v143 op_sel_hi:[1,1,0]
	v_fma_mix_f32 v142, v109, 1.0, v142 op_sel:[1,0,0] op_sel_hi:[1,0,0]
	v_fma_mix_f32 v143, v109, v109, v143 op_sel:[1,1,0] op_sel_hi:[1,1,0]
	v_fma_mix_f32 v142, v110, 1.0, v142 op_sel_hi:[1,0,0]
	v_fma_mix_f32 v143, v110, v110, v143 op_sel_hi:[1,1,0]
	v_fma_mix_f32 v142, v110, 1.0, v142 op_sel:[1,0,0] op_sel_hi:[1,0,0]
	v_fma_mix_f32 v143, v110, v110, v143 op_sel:[1,1,0] op_sel_hi:[1,1,0]
	v_fma_mix_f32 v142, v111, 1.0, v142 op_sel_hi:[1,0,0]
	v_fma_mix_f32 v143, v111, v111, v143 op_sel_hi:[1,1,0]
	v_fma_mix_f32 v142, v111, 1.0, v142 op_sel:[1,0,0] op_sel_hi:[1,0,0]
	v_fma_mix_f32 v143, v111, v111, v143 op_sel:[1,1,0] op_sel_hi:[1,1,0]
	s_waitcnt vmcnt(14)
	v_cvt_f32_f16_e32 v72, v244
	v_cvt_f32_f16_sdwa v73, v244 dst_sel:DWORD dst_unused:UNUSED_PAD src0_sel:WORD_1
	v_cvt_f32_f16_e32 v74, v245
	v_cvt_f32_f16_sdwa v75, v245 dst_sel:DWORD dst_unused:UNUSED_PAD src0_sel:WORD_1
	v_cvt_f32_f16_e32 v80, v246
	v_cvt_f32_f16_sdwa v81, v246 dst_sel:DWORD dst_unused:UNUSED_PAD src0_sel:WORD_1
	v_cvt_f32_f16_e32 v82, v247
	v_cvt_f32_f16_sdwa v83, v247 dst_sel:DWORD dst_unused:UNUSED_PAD src0_sel:WORD_1
	v_sub_f32_e32 v72, v72, v194
	v_sub_f32_e32 v73, v73, v194
	v_sub_f32_e32 v74, v74, v194
	v_sub_f32_e32 v75, v75, v194
	v_sub_f32_e32 v80, v80, v194
	v_sub_f32_e32 v81, v81, v194
	v_sub_f32_e32 v82, v82, v194
	v_sub_f32_e32 v83, v83, v194
	v_pk_mul_f32 v[72:73], v[194:195], v[72:73] op_sel:[1,0]
	v_pk_mul_f32 v[74:75], v[194:195], v[74:75] op_sel:[1,0]
	v_pk_mul_f32 v[80:81], v[194:195], v[80:81] op_sel:[1,0]
	v_pk_mul_f32 v[82:83], v[194:195], v[82:83] op_sel:[1,0]
	v_pk_fma_f32 v[100:101], v[72:73], v[168:169], v[100:101]
	v_pk_fma_f32 v[102:103], v[74:75], v[170:171], v[102:103]
	v_pk_fma_f32 v[96:97], v[80:81], v[172:173], v[96:97]
	v_pk_fma_f32 v[98:99], v[82:83], v[174:175], v[98:99]
	v_cvt_pk_f16_f32 v100, v100, v101
	v_cvt_pk_f16_f32 v101, v102, v103
	v_cvt_pk_f16_f32 v102, v96, v97
	v_cvt_pk_f16_f32 v103, v98, v99
	ds_write_b128 v235, v[100:103] offset:64
	v_fma_mix_f32 v142, v100, 1.0, v142 op_sel_hi:[1,0,0]
	v_fma_mix_f32 v143, v100, v100, v143 op_sel_hi:[1,1,0]
	v_fma_mix_f32 v142, v100, 1.0, v142 op_sel:[1,0,0] op_sel_hi:[1,0,0]
	v_fma_mix_f32 v143, v100, v100, v143 op_sel:[1,1,0] op_sel_hi:[1,1,0]
	v_fma_mix_f32 v142, v101, 1.0, v142 op_sel_hi:[1,0,0]
	v_fma_mix_f32 v143, v101, v101, v143 op_sel_hi:[1,1,0]
	v_fma_mix_f32 v142, v101, 1.0, v142 op_sel:[1,0,0] op_sel_hi:[1,0,0]
	v_fma_mix_f32 v143, v101, v101, v143 op_sel:[1,1,0] op_sel_hi:[1,1,0]
	v_fma_mix_f32 v142, v102, 1.0, v142 op_sel_hi:[1,0,0]
	v_fma_mix_f32 v143, v102, v102, v143 op_sel_hi:[1,1,0]
	v_fma_mix_f32 v142, v102, 1.0, v142 op_sel:[1,0,0] op_sel_hi:[1,0,0]
	v_fma_mix_f32 v143, v102, v102, v143 op_sel:[1,1,0] op_sel_hi:[1,1,0]
	v_fma_mix_f32 v142, v103, 1.0, v142 op_sel_hi:[1,0,0]
	v_fma_mix_f32 v143, v103, v103, v143 op_sel_hi:[1,1,0]
	v_fma_mix_f32 v142, v103, 1.0, v142 op_sel:[1,0,0] op_sel_hi:[1,0,0]
	v_fma_mix_f32 v143, v103, v103, v143 op_sel:[1,1,0] op_sel_hi:[1,1,0]
	ds_read_b128 v[92:95], v236
	ds_read_b128 v[120:123], v236 offset:1152
	s_waitcnt vmcnt(13)
	v_cvt_f32_f16_e32 v72, v248
	v_cvt_f32_f16_sdwa v73, v248 dst_sel:DWORD dst_unused:UNUSED_PAD src0_sel:WORD_1
	v_cvt_f32_f16_e32 v74, v249
	v_cvt_f32_f16_sdwa v75, v249 dst_sel:DWORD dst_unused:UNUSED_PAD src0_sel:WORD_1
	v_cvt_f32_f16_e32 v80, v250
	v_cvt_f32_f16_sdwa v81, v250 dst_sel:DWORD dst_unused:UNUSED_PAD src0_sel:WORD_1
	v_cvt_f32_f16_e32 v82, v251
	v_cvt_f32_f16_sdwa v83, v251 dst_sel:DWORD dst_unused:UNUSED_PAD src0_sel:WORD_1
	v_sub_f32_e32 v72, v72, v196
	v_sub_f32_e32 v73, v73, v196
	v_sub_f32_e32 v74, v74, v196
	v_sub_f32_e32 v75, v75, v196
	v_sub_f32_e32 v80, v80, v196
	v_sub_f32_e32 v81, v81, v196
	v_sub_f32_e32 v82, v82, v196
	v_sub_f32_e32 v83, v83, v196
	v_pk_mul_f32 v[72:73], v[196:197], v[72:73] op_sel:[1,0]
	v_pk_mul_f32 v[74:75], v[196:197], v[74:75] op_sel:[1,0]
	v_pk_mul_f32 v[80:81], v[196:197], v[80:81] op_sel:[1,0]
	v_pk_mul_f32 v[82:83], v[196:197], v[82:83] op_sel:[1,0]
	v_pk_fma_f32 v[84:85], v[72:73], v[160:161], v[84:85]
	v_pk_fma_f32 v[86:87], v[74:75], v[162:163], v[86:87]
	v_pk_fma_f32 v[76:77], v[80:81], v[164:165], v[76:77]
	v_pk_fma_f32 v[78:79], v[82:83], v[166:167], v[78:79]
	v_cvt_pk_f16_f32 v84, v84, v85
	v_cvt_pk_f16_f32 v85, v86, v87
	v_cvt_pk_f16_f32 v86, v76, v77
	v_cvt_pk_f16_f32 v87, v78, v79
	s_waitcnt lgkmcnt(0)
	v_add_u32_e32 v83, 0xc000, v224
	buffer_store_dwordx4 v[92:95], v83, s[24:27], 0 offen nt
	v_add_u32_e32 v82, 0xf000, v224
	buffer_store_dwordx4 v[120:123], v82, s[24:27], 0 offen nt
	ds_write_b128 v235, v[84:87]
	v_fma_mix_f32 v216, v84, 1.0, 0 op_sel_hi:[1,0,0]
	v_fma_mix_f32 v217, v84, v84, 0 op_sel_hi:[1,1,0]
	v_fma_mix_f32 v216, v84, 1.0, v216 op_sel:[1,0,0] op_sel_hi:[1,0,0]
	v_fma_mix_f32 v217, v84, v84, v217 op_sel:[1,1,0] op_sel_hi:[1,1,0]
	v_fma_mix_f32 v216, v85, 1.0, v216 op_sel_hi:[1,0,0]
	v_fma_mix_f32 v217, v85, v85, v217 op_sel_hi:[1,1,0]
	v_fma_mix_f32 v216, v85, 1.0, v216 op_sel:[1,0,0] op_sel_hi:[1,0,0]
	v_fma_mix_f32 v217, v85, v85, v217 op_sel:[1,1,0] op_sel_hi:[1,1,0]
	v_fma_mix_f32 v216, v86, 1.0, v216 op_sel_hi:[1,0,0]
	v_fma_mix_f32 v217, v86, v86, v217 op_sel_hi:[1,1,0]
	v_fma_mix_f32 v216, v86, 1.0, v216 op_sel:[1,0,0] op_sel_hi:[1,0,0]
	v_fma_mix_f32 v217, v86, v86, v217 op_sel:[1,1,0] op_sel_hi:[1,1,0]
	v_fma_mix_f32 v216, v87, 1.0, v216 op_sel_hi:[1,0,0]
	v_fma_mix_f32 v217, v87, v87, v217 op_sel_hi:[1,1,0]
	v_fma_mix_f32 v216, v87, 1.0, v216 op_sel:[1,0,0] op_sel_hi:[1,0,0]
	v_fma_mix_f32 v217, v87, v87, v217 op_sel:[1,1,0] op_sel_hi:[1,1,0]
	s_waitcnt vmcnt(14)
	v_cvt_f32_f16_e32 v72, v252
	v_cvt_f32_f16_sdwa v73, v252 dst_sel:DWORD dst_unused:UNUSED_PAD src0_sel:WORD_1
	v_cvt_f32_f16_e32 v74, v253
	v_cvt_f32_f16_sdwa v75, v253 dst_sel:DWORD dst_unused:UNUSED_PAD src0_sel:WORD_1
	v_cvt_f32_f16_e32 v80, v254
	v_cvt_f32_f16_sdwa v81, v254 dst_sel:DWORD dst_unused:UNUSED_PAD src0_sel:WORD_1
	v_cvt_f32_f16_e32 v82, v255
	v_cvt_f32_f16_sdwa v83, v255 dst_sel:DWORD dst_unused:UNUSED_PAD src0_sel:WORD_1
	v_sub_f32_e32 v72, v72, v196
	v_sub_f32_e32 v73, v73, v196
	v_sub_f32_e32 v74, v74, v196
	v_sub_f32_e32 v75, v75, v196
	v_sub_f32_e32 v80, v80, v196
	v_sub_f32_e32 v81, v81, v196
	v_sub_f32_e32 v82, v82, v196
	v_sub_f32_e32 v83, v83, v196
	v_pk_mul_f32 v[72:73], v[196:197], v[72:73] op_sel:[1,0]
	v_pk_mul_f32 v[74:75], v[196:197], v[74:75] op_sel:[1,0]
	v_pk_mul_f32 v[80:81], v[196:197], v[80:81] op_sel:[1,0]
	v_pk_mul_f32 v[82:83], v[196:197], v[82:83] op_sel:[1,0]
	v_pk_fma_f32 v[68:69], v[72:73], v[168:169], v[68:69]
	v_pk_fma_f32 v[70:71], v[74:75], v[170:171], v[70:71]
	v_pk_fma_f32 v[64:65], v[80:81], v[172:173], v[64:65]
	v_pk_fma_f32 v[66:67], v[82:83], v[174:175], v[66:67]
	v_cvt_pk_f16_f32 v68, v68, v69
	v_cvt_pk_f16_f32 v69, v70, v71
	v_cvt_pk_f16_f32 v70, v64, v65
	v_cvt_pk_f16_f32 v71, v66, v67
	ds_write_b128 v235, v[68:71] offset:64
	v_fma_mix_f32 v216, v68, 1.0, v216 op_sel_hi:[1,0,0]
	v_fma_mix_f32 v217, v68, v68, v217 op_sel_hi:[1,1,0]
	v_fma_mix_f32 v216, v68, 1.0, v216 op_sel:[1,0,0] op_sel_hi:[1,0,0]
	v_fma_mix_f32 v217, v68, v68, v217 op_sel:[1,1,0] op_sel_hi:[1,1,0]
	v_fma_mix_f32 v216, v69, 1.0, v216 op_sel_hi:[1,0,0]
	v_fma_mix_f32 v217, v69, v69, v217 op_sel_hi:[1,1,0]
	v_fma_mix_f32 v216, v69, 1.0, v216 op_sel:[1,0,0] op_sel_hi:[1,0,0]
	v_fma_mix_f32 v217, v69, v69, v217 op_sel:[1,1,0] op_sel_hi:[1,1,0]
	v_fma_mix_f32 v216, v70, 1.0, v216 op_sel_hi:[1,0,0]
	v_fma_mix_f32 v217, v70, v70, v217 op_sel_hi:[1,1,0]
	v_fma_mix_f32 v216, v70, 1.0, v216 op_sel:[1,0,0] op_sel_hi:[1,0,0]
	v_fma_mix_f32 v217, v70, v70, v217 op_sel:[1,1,0] op_sel_hi:[1,1,0]
	v_fma_mix_f32 v216, v71, 1.0, v216 op_sel_hi:[1,0,0]
	v_fma_mix_f32 v217, v71, v71, v217 op_sel_hi:[1,1,0]
	v_fma_mix_f32 v216, v71, 1.0, v216 op_sel:[1,0,0] op_sel_hi:[1,0,0]
	v_fma_mix_f32 v217, v71, v71, v217 op_sel:[1,1,0] op_sel_hi:[1,1,0]
	ds_read_b128 v[112:115], v236
	ds_read_b128 v[220:223], v236 offset:1152
	s_waitcnt vmcnt(13)
	v_cvt_f32_f16_e32 v72, v136
	v_cvt_f32_f16_sdwa v73, v136 dst_sel:DWORD dst_unused:UNUSED_PAD src0_sel:WORD_1
	v_cvt_f32_f16_e32 v74, v137
	v_cvt_f32_f16_sdwa v75, v137 dst_sel:DWORD dst_unused:UNUSED_PAD src0_sel:WORD_1
	v_cvt_f32_f16_e32 v80, v138
	v_cvt_f32_f16_sdwa v81, v138 dst_sel:DWORD dst_unused:UNUSED_PAD src0_sel:WORD_1
	v_cvt_f32_f16_e32 v82, v139
	v_cvt_f32_f16_sdwa v83, v139 dst_sel:DWORD dst_unused:UNUSED_PAD src0_sel:WORD_1
	v_sub_f32_e32 v72, v72, v198
	v_sub_f32_e32 v73, v73, v198
	v_sub_f32_e32 v74, v74, v198
	v_sub_f32_e32 v75, v75, v198
	v_sub_f32_e32 v80, v80, v198
	v_sub_f32_e32 v81, v81, v198
	v_sub_f32_e32 v82, v82, v198
	v_sub_f32_e32 v83, v83, v198
	v_pk_mul_f32 v[72:73], v[198:199], v[72:73] op_sel:[1,0]
	v_pk_mul_f32 v[74:75], v[198:199], v[74:75] op_sel:[1,0]
	v_pk_mul_f32 v[80:81], v[198:199], v[80:81] op_sel:[1,0]
	v_pk_mul_f32 v[82:83], v[198:199], v[82:83] op_sel:[1,0]
	v_pk_fma_f32 v[60:61], v[72:73], v[160:161], v[60:61]
	v_pk_fma_f32 v[62:63], v[74:75], v[162:163], v[62:63]
	v_pk_fma_f32 v[56:57], v[80:81], v[164:165], v[56:57]
	v_pk_fma_f32 v[58:59], v[82:83], v[166:167], v[58:59]
	v_cvt_pk_f16_f32 v60, v60, v61
	v_cvt_pk_f16_f32 v61, v62, v63
	v_cvt_pk_f16_f32 v62, v56, v57
	v_cvt_pk_f16_f32 v63, v58, v59
	s_waitcnt lgkmcnt(0)
	v_add_u32_e32 v83, 0x12000, v224
	buffer_store_dwordx4 v[112:115], v83, s[24:27], 0 offen nt
	v_add_u32_e32 v82, 0x15000, v224
	buffer_store_dwordx4 v[220:223], v82, s[24:27], 0 offen nt
	ds_write_b128 v235, v[60:63]
	v_fma_mix_f32 v218, v60, 1.0, 0 op_sel_hi:[1,0,0]
	v_fma_mix_f32 v219, v60, v60, 0 op_sel_hi:[1,1,0]
	v_fma_mix_f32 v218, v60, 1.0, v218 op_sel:[1,0,0] op_sel_hi:[1,0,0]
	v_fma_mix_f32 v219, v60, v60, v219 op_sel:[1,1,0] op_sel_hi:[1,1,0]
	v_fma_mix_f32 v218, v61, 1.0, v218 op_sel_hi:[1,0,0]
	v_fma_mix_f32 v219, v61, v61, v219 op_sel_hi:[1,1,0]
	v_fma_mix_f32 v218, v61, 1.0, v218 op_sel:[1,0,0] op_sel_hi:[1,0,0]
	v_fma_mix_f32 v219, v61, v61, v219 op_sel:[1,1,0] op_sel_hi:[1,1,0]
	v_fma_mix_f32 v218, v62, 1.0, v218 op_sel_hi:[1,0,0]
	v_fma_mix_f32 v219, v62, v62, v219 op_sel_hi:[1,1,0]
	v_fma_mix_f32 v218, v62, 1.0, v218 op_sel:[1,0,0] op_sel_hi:[1,0,0]
	v_fma_mix_f32 v219, v62, v62, v219 op_sel:[1,1,0] op_sel_hi:[1,1,0]
	v_fma_mix_f32 v218, v63, 1.0, v218 op_sel_hi:[1,0,0]
	v_fma_mix_f32 v219, v63, v63, v219 op_sel_hi:[1,1,0]
	v_fma_mix_f32 v218, v63, 1.0, v218 op_sel:[1,0,0] op_sel_hi:[1,0,0]
	v_fma_mix_f32 v219, v63, v63, v219 op_sel:[1,1,0] op_sel_hi:[1,1,0]
	s_waitcnt vmcnt(14)
	v_cvt_f32_f16_e32 v72, v148
	v_cvt_f32_f16_sdwa v73, v148 dst_sel:DWORD dst_unused:UNUSED_PAD src0_sel:WORD_1
	v_cvt_f32_f16_e32 v74, v149
	v_cvt_f32_f16_sdwa v75, v149 dst_sel:DWORD dst_unused:UNUSED_PAD src0_sel:WORD_1
	v_cvt_f32_f16_e32 v80, v150
	v_cvt_f32_f16_sdwa v81, v150 dst_sel:DWORD dst_unused:UNUSED_PAD src0_sel:WORD_1
	v_cvt_f32_f16_e32 v82, v151
	v_cvt_f32_f16_sdwa v83, v151 dst_sel:DWORD dst_unused:UNUSED_PAD src0_sel:WORD_1
	v_sub_f32_e32 v72, v72, v198
	v_sub_f32_e32 v73, v73, v198
	v_sub_f32_e32 v74, v74, v198
	v_sub_f32_e32 v75, v75, v198
	v_sub_f32_e32 v80, v80, v198
	v_sub_f32_e32 v81, v81, v198
	v_sub_f32_e32 v82, v82, v198
	v_sub_f32_e32 v83, v83, v198
	v_pk_mul_f32 v[72:73], v[198:199], v[72:73] op_sel:[1,0]
	v_pk_mul_f32 v[74:75], v[198:199], v[74:75] op_sel:[1,0]
	v_pk_mul_f32 v[80:81], v[198:199], v[80:81] op_sel:[1,0]
	v_pk_mul_f32 v[82:83], v[198:199], v[82:83] op_sel:[1,0]
	v_pk_fma_f32 v[52:53], v[72:73], v[168:169], v[52:53]
	v_pk_fma_f32 v[54:55], v[74:75], v[170:171], v[54:55]
	v_pk_fma_f32 v[48:49], v[80:81], v[172:173], v[48:49]
	v_pk_fma_f32 v[50:51], v[82:83], v[174:175], v[50:51]
	v_cvt_pk_f16_f32 v52, v52, v53
	v_cvt_pk_f16_f32 v53, v54, v55
	v_cvt_pk_f16_f32 v54, v48, v49
	v_cvt_pk_f16_f32 v55, v50, v51
	ds_write_b128 v235, v[52:55] offset:64
	v_fma_mix_f32 v218, v52, 1.0, v218 op_sel_hi:[1,0,0]
	v_fma_mix_f32 v219, v52, v52, v219 op_sel_hi:[1,1,0]
	v_fma_mix_f32 v218, v52, 1.0, v218 op_sel:[1,0,0] op_sel_hi:[1,0,0]
	v_fma_mix_f32 v219, v52, v52, v219 op_sel:[1,1,0] op_sel_hi:[1,1,0]
	v_fma_mix_f32 v218, v53, 1.0, v218 op_sel_hi:[1,0,0]
	v_fma_mix_f32 v219, v53, v53, v219 op_sel_hi:[1,1,0]
	v_fma_mix_f32 v218, v53, 1.0, v218 op_sel:[1,0,0] op_sel_hi:[1,0,0]
	v_fma_mix_f32 v219, v53, v53, v219 op_sel:[1,1,0] op_sel_hi:[1,1,0]
	v_fma_mix_f32 v218, v54, 1.0, v218 op_sel_hi:[1,0,0]
	v_fma_mix_f32 v219, v54, v54, v219 op_sel_hi:[1,1,0]
	v_fma_mix_f32 v218, v54, 1.0, v218 op_sel:[1,0,0] op_sel_hi:[1,0,0]
	v_fma_mix_f32 v219, v54, v54, v219 op_sel:[1,1,0] op_sel_hi:[1,1,0]
	v_fma_mix_f32 v218, v55, 1.0, v218 op_sel_hi:[1,0,0]
	v_fma_mix_f32 v219, v55, v55, v219 op_sel_hi:[1,1,0]
	v_fma_mix_f32 v218, v55, 1.0, v218 op_sel:[1,0,0] op_sel_hi:[1,0,0]
	v_fma_mix_f32 v219, v55, v55, v219 op_sel:[1,1,0] op_sel_hi:[1,1,0]
	ds_read_b128 v[124:127], v236
	ds_read_b128 v[116:119], v236 offset:1152
	s_waitcnt vmcnt(13)
	v_cvt_f32_f16_e32 v72, v152
	v_cvt_f32_f16_sdwa v73, v152 dst_sel:DWORD dst_unused:UNUSED_PAD src0_sel:WORD_1
	v_cvt_f32_f16_e32 v74, v153
	v_cvt_f32_f16_sdwa v75, v153 dst_sel:DWORD dst_unused:UNUSED_PAD src0_sel:WORD_1
	v_cvt_f32_f16_e32 v80, v154
	v_cvt_f32_f16_sdwa v81, v154 dst_sel:DWORD dst_unused:UNUSED_PAD src0_sel:WORD_1
	v_cvt_f32_f16_e32 v82, v155
	v_cvt_f32_f16_sdwa v83, v155 dst_sel:DWORD dst_unused:UNUSED_PAD src0_sel:WORD_1
	v_sub_f32_e32 v72, v72, v200
	v_sub_f32_e32 v73, v73, v200
	v_sub_f32_e32 v74, v74, v200
	v_sub_f32_e32 v75, v75, v200
	v_sub_f32_e32 v80, v80, v200
	v_sub_f32_e32 v81, v81, v200
	v_sub_f32_e32 v82, v82, v200
	v_sub_f32_e32 v83, v83, v200
	v_pk_mul_f32 v[72:73], v[200:201], v[72:73] op_sel:[1,0]
	v_pk_mul_f32 v[74:75], v[200:201], v[74:75] op_sel:[1,0]
	v_pk_mul_f32 v[80:81], v[200:201], v[80:81] op_sel:[1,0]
	v_pk_mul_f32 v[82:83], v[200:201], v[82:83] op_sel:[1,0]
	v_pk_fma_f32 v[44:45], v[72:73], v[160:161], v[44:45]
	v_pk_fma_f32 v[46:47], v[74:75], v[162:163], v[46:47]
	v_pk_fma_f32 v[40:41], v[80:81], v[164:165], v[40:41]
	v_pk_fma_f32 v[42:43], v[82:83], v[166:167], v[42:43]
	v_cvt_pk_f16_f32 v44, v44, v45
	v_cvt_pk_f16_f32 v45, v46, v47
	v_cvt_pk_f16_f32 v46, v40, v41
	v_cvt_pk_f16_f32 v47, v42, v43
	s_waitcnt lgkmcnt(0)
	v_add_u32_e32 v83, 0x30000, v224
	buffer_store_dwordx4 v[124:127], v83, s[24:27], 0 offen nt
	v_add_u32_e32 v82, 0x33000, v224
	buffer_store_dwordx4 v[116:119], v82, s[24:27], 0 offen nt
	ds_write_b128 v235, v[44:47]
	v_fma_mix_f32 v208, v44, 1.0, 0 op_sel_hi:[1,0,0]
	v_fma_mix_f32 v209, v44, v44, 0 op_sel_hi:[1,1,0]
	v_fma_mix_f32 v208, v44, 1.0, v208 op_sel:[1,0,0] op_sel_hi:[1,0,0]
	v_fma_mix_f32 v209, v44, v44, v209 op_sel:[1,1,0] op_sel_hi:[1,1,0]
	v_fma_mix_f32 v208, v45, 1.0, v208 op_sel_hi:[1,0,0]
	v_fma_mix_f32 v209, v45, v45, v209 op_sel_hi:[1,1,0]
	v_fma_mix_f32 v208, v45, 1.0, v208 op_sel:[1,0,0] op_sel_hi:[1,0,0]
	v_fma_mix_f32 v209, v45, v45, v209 op_sel:[1,1,0] op_sel_hi:[1,1,0]
	v_fma_mix_f32 v208, v46, 1.0, v208 op_sel_hi:[1,0,0]
	v_fma_mix_f32 v209, v46, v46, v209 op_sel_hi:[1,1,0]
	v_fma_mix_f32 v208, v46, 1.0, v208 op_sel:[1,0,0] op_sel_hi:[1,0,0]
	v_fma_mix_f32 v209, v46, v46, v209 op_sel:[1,1,0] op_sel_hi:[1,1,0]
	v_fma_mix_f32 v208, v47, 1.0, v208 op_sel_hi:[1,0,0]
	v_fma_mix_f32 v209, v47, v47, v209 op_sel_hi:[1,1,0]
	v_fma_mix_f32 v208, v47, 1.0, v208 op_sel:[1,0,0] op_sel_hi:[1,0,0]
	v_fma_mix_f32 v209, v47, v47, v209 op_sel:[1,1,0] op_sel_hi:[1,1,0]
	s_waitcnt vmcnt(14)
	v_cvt_f32_f16_e32 v72, v156
	v_cvt_f32_f16_sdwa v73, v156 dst_sel:DWORD dst_unused:UNUSED_PAD src0_sel:WORD_1
	v_cvt_f32_f16_e32 v74, v157
	v_cvt_f32_f16_sdwa v75, v157 dst_sel:DWORD dst_unused:UNUSED_PAD src0_sel:WORD_1
	v_cvt_f32_f16_e32 v80, v158
	v_cvt_f32_f16_sdwa v81, v158 dst_sel:DWORD dst_unused:UNUSED_PAD src0_sel:WORD_1
	v_cvt_f32_f16_e32 v82, v159
	v_cvt_f32_f16_sdwa v83, v159 dst_sel:DWORD dst_unused:UNUSED_PAD src0_sel:WORD_1
	v_sub_f32_e32 v72, v72, v200
	v_sub_f32_e32 v73, v73, v200
	v_sub_f32_e32 v74, v74, v200
	v_sub_f32_e32 v75, v75, v200
	v_sub_f32_e32 v80, v80, v200
	v_sub_f32_e32 v81, v81, v200
	v_sub_f32_e32 v82, v82, v200
	v_sub_f32_e32 v83, v83, v200
	v_pk_mul_f32 v[72:73], v[200:201], v[72:73] op_sel:[1,0]
	v_pk_mul_f32 v[74:75], v[200:201], v[74:75] op_sel:[1,0]
	v_pk_mul_f32 v[80:81], v[200:201], v[80:81] op_sel:[1,0]
	v_pk_mul_f32 v[82:83], v[200:201], v[82:83] op_sel:[1,0]
	v_pk_fma_f32 v[36:37], v[72:73], v[168:169], v[36:37]
	v_pk_fma_f32 v[38:39], v[74:75], v[170:171], v[38:39]
	v_pk_fma_f32 v[32:33], v[80:81], v[172:173], v[32:33]
	v_pk_fma_f32 v[34:35], v[82:83], v[174:175], v[34:35]
	v_cvt_pk_f16_f32 v36, v36, v37
	v_cvt_pk_f16_f32 v37, v38, v39
	v_cvt_pk_f16_f32 v38, v32, v33
	v_cvt_pk_f16_f32 v39, v34, v35
	ds_write_b128 v235, v[36:39] offset:64
	v_fma_mix_f32 v208, v36, 1.0, v208 op_sel_hi:[1,0,0]
	v_fma_mix_f32 v209, v36, v36, v209 op_sel_hi:[1,1,0]
	v_fma_mix_f32 v208, v36, 1.0, v208 op_sel:[1,0,0] op_sel_hi:[1,0,0]
	v_fma_mix_f32 v209, v36, v36, v209 op_sel:[1,1,0] op_sel_hi:[1,1,0]
	v_fma_mix_f32 v208, v37, 1.0, v208 op_sel_hi:[1,0,0]
	v_fma_mix_f32 v209, v37, v37, v209 op_sel_hi:[1,1,0]
	v_fma_mix_f32 v208, v37, 1.0, v208 op_sel:[1,0,0] op_sel_hi:[1,0,0]
	v_fma_mix_f32 v209, v37, v37, v209 op_sel:[1,1,0] op_sel_hi:[1,1,0]
	v_fma_mix_f32 v208, v38, 1.0, v208 op_sel_hi:[1,0,0]
	v_fma_mix_f32 v209, v38, v38, v209 op_sel_hi:[1,1,0]
	v_fma_mix_f32 v208, v38, 1.0, v208 op_sel:[1,0,0] op_sel_hi:[1,0,0]
	v_fma_mix_f32 v209, v38, v38, v209 op_sel:[1,1,0] op_sel_hi:[1,1,0]
	v_fma_mix_f32 v208, v39, 1.0, v208 op_sel_hi:[1,0,0]
	v_fma_mix_f32 v209, v39, v39, v209 op_sel_hi:[1,1,0]
	v_fma_mix_f32 v208, v39, 1.0, v208 op_sel:[1,0,0] op_sel_hi:[1,0,0]
	v_fma_mix_f32 v209, v39, v39, v209 op_sel:[1,1,0] op_sel_hi:[1,1,0]
	ds_read_b128 v[128:131], v236
	ds_read_b128 v[104:107], v236 offset:1152
	s_waitcnt vmcnt(11)
	v_cvt_f32_f16_e32 v72, v212
	v_cvt_f32_f16_sdwa v73, v212 dst_sel:DWORD dst_unused:UNUSED_PAD src0_sel:WORD_1
	v_cvt_f32_f16_e32 v74, v213
	v_cvt_f32_f16_sdwa v75, v213 dst_sel:DWORD dst_unused:UNUSED_PAD src0_sel:WORD_1
	v_cvt_f32_f16_e32 v80, v214
	v_cvt_f32_f16_sdwa v81, v214 dst_sel:DWORD dst_unused:UNUSED_PAD src0_sel:WORD_1
	v_cvt_f32_f16_e32 v82, v215
	v_cvt_f32_f16_sdwa v83, v215 dst_sel:DWORD dst_unused:UNUSED_PAD src0_sel:WORD_1
	v_sub_f32_e32 v72, v72, v202
	v_sub_f32_e32 v73, v73, v202
	v_sub_f32_e32 v74, v74, v202
	v_sub_f32_e32 v75, v75, v202
	v_sub_f32_e32 v80, v80, v202
	v_sub_f32_e32 v81, v81, v202
	v_sub_f32_e32 v82, v82, v202
	v_sub_f32_e32 v83, v83, v202
	v_pk_mul_f32 v[72:73], v[202:203], v[72:73] op_sel:[1,0]
	v_pk_mul_f32 v[74:75], v[202:203], v[74:75] op_sel:[1,0]
	v_pk_mul_f32 v[80:81], v[202:203], v[80:81] op_sel:[1,0]
	v_pk_mul_f32 v[82:83], v[202:203], v[82:83] op_sel:[1,0]
	v_pk_fma_f32 v[28:29], v[72:73], v[160:161], v[28:29]
	v_pk_fma_f32 v[30:31], v[74:75], v[162:163], v[30:31]
	v_pk_fma_f32 v[24:25], v[80:81], v[164:165], v[24:25]
	v_pk_fma_f32 v[26:27], v[82:83], v[166:167], v[26:27]
	v_cvt_pk_f16_f32 v28, v28, v29
	v_cvt_pk_f16_f32 v29, v30, v31
	v_cvt_pk_f16_f32 v30, v24, v25
	v_cvt_pk_f16_f32 v31, v26, v27
	s_waitcnt lgkmcnt(0)
	v_add_u32_e32 v83, 0x36000, v224
	buffer_store_dwordx4 v[128:131], v83, s[24:27], 0 offen nt
	v_add_u32_e32 v82, 0x39000, v224
	buffer_store_dwordx4 v[104:107], v82, s[24:27], 0 offen nt
	ds_write_b128 v235, v[28:31]
	v_fma_mix_f32 v210, v28, 1.0, 0 op_sel_hi:[1,0,0]
	v_fma_mix_f32 v211, v28, v28, 0 op_sel_hi:[1,1,0]
	v_fma_mix_f32 v210, v28, 1.0, v210 op_sel:[1,0,0] op_sel_hi:[1,0,0]
	v_fma_mix_f32 v211, v28, v28, v211 op_sel:[1,1,0] op_sel_hi:[1,1,0]
	v_fma_mix_f32 v210, v29, 1.0, v210 op_sel_hi:[1,0,0]
	v_fma_mix_f32 v211, v29, v29, v211 op_sel_hi:[1,1,0]
	v_fma_mix_f32 v210, v29, 1.0, v210 op_sel:[1,0,0] op_sel_hi:[1,0,0]
	v_fma_mix_f32 v211, v29, v29, v211 op_sel:[1,1,0] op_sel_hi:[1,1,0]
	v_fma_mix_f32 v210, v30, 1.0, v210 op_sel_hi:[1,0,0]
	v_fma_mix_f32 v211, v30, v30, v211 op_sel_hi:[1,1,0]
	v_fma_mix_f32 v210, v30, 1.0, v210 op_sel:[1,0,0] op_sel_hi:[1,0,0]
	v_fma_mix_f32 v211, v30, v30, v211 op_sel:[1,1,0] op_sel_hi:[1,1,0]
	v_fma_mix_f32 v210, v31, 1.0, v210 op_sel_hi:[1,0,0]
	v_fma_mix_f32 v211, v31, v31, v211 op_sel_hi:[1,1,0]
	v_fma_mix_f32 v210, v31, 1.0, v210 op_sel:[1,0,0] op_sel_hi:[1,0,0]
	v_fma_mix_f32 v211, v31, v31, v211 op_sel:[1,1,0] op_sel_hi:[1,1,0]
	s_waitcnt vmcnt(12)
	v_cvt_f32_f16_e32 v72, v144
	v_cvt_f32_f16_sdwa v73, v144 dst_sel:DWORD dst_unused:UNUSED_PAD src0_sel:WORD_1
	v_cvt_f32_f16_e32 v74, v145
	v_cvt_f32_f16_sdwa v75, v145 dst_sel:DWORD dst_unused:UNUSED_PAD src0_sel:WORD_1
	v_cvt_f32_f16_e32 v80, v146
	v_cvt_f32_f16_sdwa v81, v146 dst_sel:DWORD dst_unused:UNUSED_PAD src0_sel:WORD_1
	v_cvt_f32_f16_e32 v82, v147
	v_cvt_f32_f16_sdwa v83, v147 dst_sel:DWORD dst_unused:UNUSED_PAD src0_sel:WORD_1
	v_sub_f32_e32 v72, v72, v202
	v_sub_f32_e32 v73, v73, v202
	v_sub_f32_e32 v74, v74, v202
	v_sub_f32_e32 v75, v75, v202
	v_sub_f32_e32 v80, v80, v202
	v_sub_f32_e32 v81, v81, v202
	v_sub_f32_e32 v82, v82, v202
	v_sub_f32_e32 v83, v83, v202
	v_pk_mul_f32 v[72:73], v[202:203], v[72:73] op_sel:[1,0]
	v_pk_mul_f32 v[74:75], v[202:203], v[74:75] op_sel:[1,0]
	v_pk_mul_f32 v[80:81], v[202:203], v[80:81] op_sel:[1,0]
	v_pk_mul_f32 v[82:83], v[202:203], v[82:83] op_sel:[1,0]
	v_pk_fma_f32 v[20:21], v[72:73], v[168:169], v[20:21]
	v_pk_fma_f32 v[22:23], v[74:75], v[170:171], v[22:23]
	v_pk_fma_f32 v[16:17], v[80:81], v[172:173], v[16:17]
	v_pk_fma_f32 v[18:19], v[82:83], v[174:175], v[18:19]
	v_cvt_pk_f16_f32 v20, v20, v21
	v_cvt_pk_f16_f32 v21, v22, v23
	v_cvt_pk_f16_f32 v22, v16, v17
	v_cvt_pk_f16_f32 v23, v18, v19
	ds_write_b128 v235, v[20:23] offset:64
	v_fma_mix_f32 v210, v20, 1.0, v210 op_sel_hi:[1,0,0]
	v_fma_mix_f32 v211, v20, v20, v211 op_sel_hi:[1,1,0]
	v_fma_mix_f32 v210, v20, 1.0, v210 op_sel:[1,0,0] op_sel_hi:[1,0,0]
	v_fma_mix_f32 v211, v20, v20, v211 op_sel:[1,1,0] op_sel_hi:[1,1,0]
	v_fma_mix_f32 v210, v21, 1.0, v210 op_sel_hi:[1,0,0]
	v_fma_mix_f32 v211, v21, v21, v211 op_sel_hi:[1,1,0]
	v_fma_mix_f32 v210, v21, 1.0, v210 op_sel:[1,0,0] op_sel_hi:[1,0,0]
	v_fma_mix_f32 v211, v21, v21, v211 op_sel:[1,1,0] op_sel_hi:[1,1,0]
	v_fma_mix_f32 v210, v22, 1.0, v210 op_sel_hi:[1,0,0]
	v_fma_mix_f32 v211, v22, v22, v211 op_sel_hi:[1,1,0]
	v_fma_mix_f32 v210, v22, 1.0, v210 op_sel:[1,0,0] op_sel_hi:[1,0,0]
	v_fma_mix_f32 v211, v22, v22, v211 op_sel:[1,1,0] op_sel_hi:[1,1,0]
	v_fma_mix_f32 v210, v23, 1.0, v210 op_sel_hi:[1,0,0]
	v_fma_mix_f32 v211, v23, v23, v211 op_sel_hi:[1,1,0]
	v_fma_mix_f32 v210, v23, 1.0, v210 op_sel:[1,0,0] op_sel_hi:[1,0,0]
	v_fma_mix_f32 v211, v23, v23, v211 op_sel:[1,1,0] op_sel_hi:[1,1,0]
	ds_read_b128 v[240:243], v236
	ds_read_b128 v[96:99], v236 offset:1152
	s_waitcnt vmcnt(11)
	v_cvt_f32_f16_e32 v72, v132
	v_cvt_f32_f16_sdwa v73, v132 dst_sel:DWORD dst_unused:UNUSED_PAD src0_sel:WORD_1
	v_cvt_f32_f16_e32 v74, v133
	v_cvt_f32_f16_sdwa v75, v133 dst_sel:DWORD dst_unused:UNUSED_PAD src0_sel:WORD_1
	v_cvt_f32_f16_e32 v80, v134
	v_cvt_f32_f16_sdwa v81, v134 dst_sel:DWORD dst_unused:UNUSED_PAD src0_sel:WORD_1
	v_cvt_f32_f16_e32 v82, v135
	v_cvt_f32_f16_sdwa v83, v135 dst_sel:DWORD dst_unused:UNUSED_PAD src0_sel:WORD_1
	v_sub_f32_e32 v72, v72, v204
	v_sub_f32_e32 v73, v73, v204
	v_sub_f32_e32 v74, v74, v204
	v_sub_f32_e32 v75, v75, v204
	v_sub_f32_e32 v80, v80, v204
	v_sub_f32_e32 v81, v81, v204
	v_sub_f32_e32 v82, v82, v204
	v_sub_f32_e32 v83, v83, v204
	v_pk_mul_f32 v[72:73], v[204:205], v[72:73] op_sel:[1,0]
	v_pk_mul_f32 v[74:75], v[204:205], v[74:75] op_sel:[1,0]
	v_pk_mul_f32 v[80:81], v[204:205], v[80:81] op_sel:[1,0]
	v_pk_mul_f32 v[82:83], v[204:205], v[82:83] op_sel:[1,0]
	v_pk_fma_f32 v[12:13], v[72:73], v[160:161], v[12:13]
	v_pk_fma_f32 v[14:15], v[74:75], v[162:163], v[14:15]
	v_pk_fma_f32 v[8:9], v[80:81], v[164:165], v[8:9]
	v_pk_fma_f32 v[10:11], v[82:83], v[166:167], v[10:11]
	v_cvt_pk_f16_f32 v12, v12, v13
	v_cvt_pk_f16_f32 v13, v14, v15
	v_cvt_pk_f16_f32 v14, v8, v9
	v_cvt_pk_f16_f32 v15, v10, v11
	s_waitcnt lgkmcnt(0)
	v_add_u32_e32 v83, 0x3c000, v224
	buffer_store_dwordx4 v[240:243], v83, s[24:27], 0 offen nt
	v_add_u32_e32 v82, 0x3f000, v224
	buffer_store_dwordx4 v[96:99], v82, s[24:27], 0 offen nt
	ds_write_b128 v235, v[12:15]
	v_fma_mix_f32 v244, v12, 1.0, 0 op_sel_hi:[1,0,0]
	v_fma_mix_f32 v245, v12, v12, 0 op_sel_hi:[1,1,0]
	v_fma_mix_f32 v244, v12, 1.0, v244 op_sel:[1,0,0] op_sel_hi:[1,0,0]
	v_fma_mix_f32 v245, v12, v12, v245 op_sel:[1,1,0] op_sel_hi:[1,1,0]
	v_fma_mix_f32 v244, v13, 1.0, v244 op_sel_hi:[1,0,0]
	v_fma_mix_f32 v245, v13, v13, v245 op_sel_hi:[1,1,0]
	v_fma_mix_f32 v244, v13, 1.0, v244 op_sel:[1,0,0] op_sel_hi:[1,0,0]
	v_fma_mix_f32 v245, v13, v13, v245 op_sel:[1,1,0] op_sel_hi:[1,1,0]
	v_fma_mix_f32 v244, v14, 1.0, v244 op_sel_hi:[1,0,0]
	v_fma_mix_f32 v245, v14, v14, v245 op_sel_hi:[1,1,0]
	v_fma_mix_f32 v244, v14, 1.0, v244 op_sel:[1,0,0] op_sel_hi:[1,0,0]
	v_fma_mix_f32 v245, v14, v14, v245 op_sel:[1,1,0] op_sel_hi:[1,1,0]
	v_fma_mix_f32 v244, v15, 1.0, v244 op_sel_hi:[1,0,0]
	v_fma_mix_f32 v245, v15, v15, v245 op_sel_hi:[1,1,0]
	v_fma_mix_f32 v244, v15, 1.0, v244 op_sel:[1,0,0] op_sel_hi:[1,0,0]
	v_fma_mix_f32 v245, v15, v15, v245 op_sel:[1,1,0] op_sel_hi:[1,1,0]
	s_waitcnt vmcnt(12)
	v_cvt_f32_f16_e32 v72, v88
	v_cvt_f32_f16_sdwa v73, v88 dst_sel:DWORD dst_unused:UNUSED_PAD src0_sel:WORD_1
	v_cvt_f32_f16_e32 v74, v89
	v_cvt_f32_f16_sdwa v75, v89 dst_sel:DWORD dst_unused:UNUSED_PAD src0_sel:WORD_1
	v_cvt_f32_f16_e32 v80, v90
	v_cvt_f32_f16_sdwa v81, v90 dst_sel:DWORD dst_unused:UNUSED_PAD src0_sel:WORD_1
	v_cvt_f32_f16_e32 v82, v91
	v_cvt_f32_f16_sdwa v83, v91 dst_sel:DWORD dst_unused:UNUSED_PAD src0_sel:WORD_1
	v_sub_f32_e32 v72, v72, v204
	v_sub_f32_e32 v73, v73, v204
	v_sub_f32_e32 v74, v74, v204
	v_sub_f32_e32 v75, v75, v204
	v_sub_f32_e32 v80, v80, v204
	v_sub_f32_e32 v81, v81, v204
	v_sub_f32_e32 v82, v82, v204
	v_sub_f32_e32 v83, v83, v204
	v_pk_mul_f32 v[72:73], v[204:205], v[72:73] op_sel:[1,0]
	v_pk_mul_f32 v[74:75], v[204:205], v[74:75] op_sel:[1,0]
	v_pk_mul_f32 v[80:81], v[204:205], v[80:81] op_sel:[1,0]
	v_pk_mul_f32 v[82:83], v[204:205], v[82:83] op_sel:[1,0]
	v_pk_fma_f32 v[4:5], v[72:73], v[168:169], v[4:5]
	v_pk_fma_f32 v[6:7], v[74:75], v[170:171], v[6:7]
	v_pk_fma_f32 v[0:1], v[80:81], v[172:173], v[0:1]
	v_pk_fma_f32 v[2:3], v[82:83], v[174:175], v[2:3]
	v_cvt_pk_f16_f32 v4, v4, v5
	v_cvt_pk_f16_f32 v5, v6, v7
	v_cvt_pk_f16_f32 v6, v0, v1
	v_cvt_pk_f16_f32 v7, v2, v3
	ds_write_b128 v235, v[4:7] offset:64
	v_fma_mix_f32 v244, v4, 1.0, v244 op_sel_hi:[1,0,0]
	v_fma_mix_f32 v245, v4, v4, v245 op_sel_hi:[1,1,0]
	v_fma_mix_f32 v244, v4, 1.0, v244 op_sel:[1,0,0] op_sel_hi:[1,0,0]
	v_fma_mix_f32 v245, v4, v4, v245 op_sel:[1,1,0] op_sel_hi:[1,1,0]
	v_fma_mix_f32 v244, v5, 1.0, v244 op_sel_hi:[1,0,0]
	v_fma_mix_f32 v245, v5, v5, v245 op_sel_hi:[1,1,0]
	v_fma_mix_f32 v244, v5, 1.0, v244 op_sel:[1,0,0] op_sel_hi:[1,0,0]
	v_fma_mix_f32 v245, v5, v5, v245 op_sel:[1,1,0] op_sel_hi:[1,1,0]
	v_fma_mix_f32 v244, v6, 1.0, v244 op_sel_hi:[1,0,0]
	v_fma_mix_f32 v245, v6, v6, v245 op_sel_hi:[1,1,0]
	v_fma_mix_f32 v244, v6, 1.0, v244 op_sel:[1,0,0] op_sel_hi:[1,0,0]
	v_fma_mix_f32 v245, v6, v6, v245 op_sel:[1,1,0] op_sel_hi:[1,1,0]
	v_fma_mix_f32 v244, v7, 1.0, v244 op_sel_hi:[1,0,0]
	v_fma_mix_f32 v245, v7, v7, v245 op_sel_hi:[1,1,0]
	v_fma_mix_f32 v244, v7, 1.0, v244 op_sel:[1,0,0] op_sel_hi:[1,0,0]
	v_fma_mix_f32 v245, v7, v7, v245 op_sel:[1,1,0] op_sel_hi:[1,1,0]
	ds_read_b128 v[108:111], v236
	ds_read_b128 v[100:103], v236 offset:1152
	s_waitcnt lgkmcnt(0)
	v_add_u32_e32 v83, 0x42000, v224
	buffer_store_dwordx4 v[108:111], v83, s[24:27], 0 offen nt
	v_add_u32_e32 v82, 0x45000, v224
	buffer_store_dwordx4 v[100:103], v82, s[24:27], 0 offen nt
	v_xor_b32_e32 v225, 16, v234
	v_lshlrev_b32_e32 v225, 2, v225
	v_xor_b32_e32 v246, 32, v234
	v_lshlrev_b32_e32 v246, 2, v246
	ds_bpermute_b32 v92, v225, v206
	ds_bpermute_b32 v93, v225, v207
	ds_bpermute_b32 v94, v225, v140
	ds_bpermute_b32 v95, v225, v141
	ds_bpermute_b32 v120, v225, v142
	ds_bpermute_b32 v121, v225, v143
	ds_bpermute_b32 v122, v225, v216
	ds_bpermute_b32 v123, v225, v217
	s_waitcnt lgkmcnt(0)
	v_pk_add_f32 v[206:207], v[206:207], v[92:93]
	v_pk_add_f32 v[140:141], v[140:141], v[94:95]
	v_pk_add_f32 v[142:143], v[142:143], v[120:121]
	v_pk_add_f32 v[216:217], v[216:217], v[122:123]
	ds_bpermute_b32 v92, v225, v218
	ds_bpermute_b32 v93, v225, v219
	ds_bpermute_b32 v94, v225, v208
	ds_bpermute_b32 v95, v225, v209
	ds_bpermute_b32 v120, v225, v210
	ds_bpermute_b32 v121, v225, v211
	ds_bpermute_b32 v122, v225, v244
	ds_bpermute_b32 v123, v225, v245
	s_waitcnt lgkmcnt(0)
	v_pk_add_f32 v[218:219], v[218:219], v[92:93]
	v_pk_add_f32 v[208:209], v[208:209], v[94:95]
	v_pk_add_f32 v[210:211], v[210:211], v[120:121]
	v_pk_add_f32 v[244:245], v[244:245], v[122:123]
	ds_bpermute_b32 v92, v246, v206
	ds_bpermute_b32 v93, v246, v207
	ds_bpermute_b32 v94, v246, v140
	ds_bpermute_b32 v95, v246, v141
	ds_bpermute_b32 v120, v246, v142
	ds_bpermute_b32 v121, v246, v143
	ds_bpermute_b32 v122, v246, v216
	ds_bpermute_b32 v123, v246, v217
	s_waitcnt lgkmcnt(0)
	v_pk_add_f32 v[206:207], v[206:207], v[92:93]
	v_pk_add_f32 v[140:141], v[140:141], v[94:95]
	v_pk_add_f32 v[142:143], v[142:143], v[120:121]
	v_pk_add_f32 v[216:217], v[216:217], v[122:123]
	ds_bpermute_b32 v92, v246, v218
	ds_bpermute_b32 v93, v246, v219
	ds_bpermute_b32 v94, v246, v208
	ds_bpermute_b32 v95, v246, v209
	ds_bpermute_b32 v120, v246, v210
	ds_bpermute_b32 v121, v246, v211
	ds_bpermute_b32 v122, v246, v244
	ds_bpermute_b32 v123, v246, v245
	s_waitcnt lgkmcnt(0)
	v_pk_add_f32 v[218:219], v[218:219], v[92:93]
	v_pk_add_f32 v[208:209], v[208:209], v[94:95]
	v_pk_add_f32 v[210:211], v[210:211], v[120:121]
	v_pk_add_f32 v[244:245], v[244:245], v[122:123]
	s_mov_b64 exec, 0xffff
	global_store_dwordx2 v190, v[206:207], s[100:101] offset:0
	global_store_dwordx2 v190, v[140:141], s[100:101] offset:128
	global_store_dwordx2 v190, v[142:143], s[100:101] offset:256
	global_store_dwordx2 v190, v[216:217], s[100:101] offset:384
	global_store_dwordx2 v190, v[218:219], s[100:101] offset:1024
	global_store_dwordx2 v190, v[208:209], s[100:101] offset:1152
	global_store_dwordx2 v190, v[210:211], s[100:101] offset:1280
	global_store_dwordx2 v190, v[244:245], s[100:101] offset:1408
	s_mov_b64 exec, -1
	s_mov_b32 s83, s81
	s_mov_b32 s84, s82
	s_mov_b64 s[40:41], s[0:1]
	s_mov_b64 s[38:39], s[8:9]
	s_mov_b64 vcc, s[6:7]
	s_cbranch_vccz .LBB8_12
	s_waitcnt vmcnt(0)
	s_cmpk_gt_u32 s44, 0xff
	s_cbranch_scc1 .LBB8_31
	s_barrier

.LBB9_27:
	ds_read_b128 v[128:131], v172
	ds_read_b128 v[132:135], v172 offset:1024
	ds_read_b128 v[136:139], v172 offset:2048
	ds_read_b128 v[140:143], v172 offset:3072
	s_add_u32 s30, s28, 0xfffd0080
	s_addc_u32 s31, s29, -1
	s_cmp_eq_u32 s73, 8
	s_cselect_b32 s35, s9, s31
	s_cselect_b32 s34, s8, s30
	s_cselect_b32 s31, s1, s72
	s_cselect_b32 s30, s0, s71
	s_add_i32 m0, s43, 0xc000
	ds_read_b128 v[158:161], v173
	ds_read_b128 v[162:165], v173 offset:1024
	ds_read_b128 v[178:181], v173 offset:2048
	ds_read_b128 v[182:185], v173 offset:3072
	ds_read_b128 v[186:189], v173 offset:4096
	ds_read_b128 v[190:193], v173 offset:5120
	ds_read_b128 v[194:197], v173 offset:6144
	ds_read_b128 v[198:201], v173 offset:7168
	global_load_lds_dwordx4 v152, s[28:29]
	s_add_i32 m0, s43, 0xe000
	s_nop 0
	global_load_lds_dwordx4 v154, s[28:29]
	s_waitcnt lgkmcnt(8)
	s_barrier
	s_waitcnt lgkmcnt(0)
	v_mfma_f32_16x16x32_f16 v[124:127], v[128:131], v[158:161], v[124:127]
	v_mfma_f32_16x16x32_f16 v[120:123], v[136:139], v[158:161], v[120:123]
	v_mfma_f32_16x16x32_f16 v[108:111], v[128:131], v[178:181], v[108:111]
	v_mfma_f32_16x16x32_f16 v[104:107], v[136:139], v[178:181], v[104:107]
	v_mfma_f32_16x16x32_f16 v[96:99], v[128:131], v[186:189], v[96:99]
	v_mfma_f32_16x16x32_f16 v[88:91], v[136:139], v[186:189], v[88:91]
	v_mfma_f32_16x16x32_f16 v[80:83], v[128:131], v[194:197], v[80:83]
	v_mfma_f32_16x16x32_f16 v[72:75], v[136:139], v[194:197], v[72:75]
	v_mfma_f32_16x16x32_f16 v[124:127], v[132:135], v[162:165], v[124:127]
	v_mfma_f32_16x16x32_f16 v[120:123], v[140:143], v[162:165], v[120:123]
	v_mfma_f32_16x16x32_f16 v[108:111], v[132:135], v[182:185], v[108:111]
	v_mfma_f32_16x16x32_f16 v[104:107], v[140:143], v[182:185], v[104:107]
	v_mfma_f32_16x16x32_f16 v[96:99], v[132:135], v[190:193], v[96:99]
	v_mfma_f32_16x16x32_f16 v[88:91], v[140:143], v[190:193], v[88:91]
	v_mfma_f32_16x16x32_f16 v[80:83], v[132:135], v[198:201], v[80:83]
	v_mfma_f32_16x16x32_f16 v[72:75], v[140:143], v[198:201], v[72:75]
	s_barrier
	s_add_i32 s74, s65, s42
	s_add_u32 s78, s30, 0x80
	s_addc_u32 s79, s31, 0
	s_mov_b32 m0, s74
	ds_read_b128 v[202:205], v174
	ds_read_b128 v[206:209], v174 offset:1024
	ds_read_b128 v[210:213], v174 offset:2048
	ds_read_b128 v[214:217], v174 offset:3072
	global_load_lds_dwordx4 v146, s[30:31]
	s_add_i32 m0, s74, 0x2000
	s_nop 0
	global_load_lds_dwordx4 v150, s[30:31]
	s_barrier
	s_waitcnt lgkmcnt(0)
	v_mfma_f32_16x16x32_f16 v[116:119], v[202:205], v[158:161], v[116:119]
	v_mfma_f32_16x16x32_f16 v[112:115], v[210:213], v[158:161], v[112:115]
	v_mfma_f32_16x16x32_f16 v[100:103], v[202:205], v[178:181], v[100:103]
	v_mfma_f32_16x16x32_f16 v[92:95], v[210:213], v[178:181], v[92:95]
	v_mfma_f32_16x16x32_f16 v[84:87], v[202:205], v[186:189], v[84:87]
	v_mfma_f32_16x16x32_f16 v[76:79], v[210:213], v[186:189], v[76:79]
	v_mfma_f32_16x16x32_f16 v[68:71], v[202:205], v[194:197], v[68:71]
	v_mfma_f32_16x16x32_f16 v[64:67], v[210:213], v[194:197], v[64:67]
	v_mfma_f32_16x16x32_f16 v[116:119], v[206:209], v[162:165], v[116:119]
	v_mfma_f32_16x16x32_f16 v[112:115], v[214:217], v[162:165], v[112:115]
	v_mfma_f32_16x16x32_f16 v[100:103], v[206:209], v[182:185], v[100:103]
	v_mfma_f32_16x16x32_f16 v[92:95], v[214:217], v[182:185], v[92:95]
	v_mfma_f32_16x16x32_f16 v[84:87], v[206:209], v[190:193], v[84:87]
	v_mfma_f32_16x16x32_f16 v[76:79], v[214:217], v[190:193], v[76:79]
	v_mfma_f32_16x16x32_f16 v[68:71], v[206:209], v[198:201], v[68:71]
	v_mfma_f32_16x16x32_f16 v[64:67], v[214:217], v[198:201], v[64:67]
	s_barrier
	s_mov_b32 m0, s43
	s_add_u32 s80, s34, 0x80
	s_addc_u32 s81, s35, 0
	ds_read_b128 v[158:161], v173 offset:16384
	ds_read_b128 v[162:165], v173 offset:17408
	ds_read_b128 v[178:181], v173 offset:18432
	ds_read_b128 v[182:185], v173 offset:19456
	ds_read_b128 v[186:189], v173 offset:20480
	ds_read_b128 v[190:193], v173 offset:21504
	ds_read_b128 v[194:197], v173 offset:22528
	ds_read_b128 v[198:201], v173 offset:23552
	global_load_lds_dwordx4 v144, s[34:35]
	s_mov_b32 m0, s44
	s_nop 0
	global_load_lds_dwordx4 v148, s[34:35]
	s_barrier
	s_waitcnt lgkmcnt(0)
	v_mfma_f32_16x16x32_f16 v[60:63], v[128:131], v[158:161], v[60:63]
	v_mfma_f32_16x16x32_f16 v[56:59], v[136:139], v[158:161], v[56:59]
	v_mfma_f32_16x16x32_f16 v[48:51], v[128:131], v[178:181], v[48:51]
	v_mfma_f32_16x16x32_f16 v[40:43], v[136:139], v[178:181], v[40:43]
	v_mfma_f32_16x16x32_f16 v[32:35], v[128:131], v[186:189], v[32:35]
	v_mfma_f32_16x16x32_f16 v[24:27], v[136:139], v[186:189], v[24:27]
	v_mfma_f32_16x16x32_f16 v[16:19], v[128:131], v[194:197], v[16:19]
	v_mfma_f32_16x16x32_f16 v[8:11], v[136:139], v[194:197], v[8:11]
	v_mfma_f32_16x16x32_f16 v[60:63], v[132:135], v[162:165], v[60:63]
	v_mfma_f32_16x16x32_f16 v[56:59], v[140:143], v[162:165], v[56:59]
	v_mfma_f32_16x16x32_f16 v[48:51], v[132:135], v[182:185], v[48:51]
	v_mfma_f32_16x16x32_f16 v[40:43], v[140:143], v[182:185], v[40:43]
	v_mfma_f32_16x16x32_f16 v[32:35], v[132:135], v[190:193], v[32:35]
	v_mfma_f32_16x16x32_f16 v[24:27], v[140:143], v[190:193], v[24:27]
	v_mfma_f32_16x16x32_f16 v[16:19], v[132:135], v[198:201], v[16:19]
	v_mfma_f32_16x16x32_f16 v[8:11], v[140:143], v[198:201], v[8:11]
	s_barrier
	s_add_u32 s74, s30, 0xc000
	s_addc_u32 s75, s31, 0
	s_add_i32 s76, s66, s42
	s_mov_b32 m0, s76
	s_nop 0
	global_load_lds_dwordx4 v146, s[74:75]
	s_add_i32 m0, s76, 0x2000
	s_nop 0
	global_load_lds_dwordx4 v150, s[74:75]
	s_waitcnt vmcnt(6)
	s_barrier
	v_mfma_f32_16x16x32_f16 v[52:55], v[202:205], v[158:161], v[52:55]
	v_mfma_f32_16x16x32_f16 v[44:47], v[210:213], v[158:161], v[44:47]
	v_mfma_f32_16x16x32_f16 v[36:39], v[202:205], v[178:181], v[36:39]
	v_mfma_f32_16x16x32_f16 v[28:31], v[210:213], v[178:181], v[28:31]
	v_mfma_f32_16x16x32_f16 v[20:23], v[202:205], v[186:189], v[20:23]
	v_mfma_f32_16x16x32_f16 v[12:15], v[210:213], v[186:189], v[12:15]
	v_mfma_f32_16x16x32_f16 v[4:7], v[202:205], v[194:197], v[4:7]
	v_mfma_f32_16x16x32_f16 v[0:3], v[210:213], v[194:197], v[0:3]
	v_mfma_f32_16x16x32_f16 v[52:55], v[206:209], v[162:165], v[52:55]
	v_mfma_f32_16x16x32_f16 v[44:47], v[214:217], v[162:165], v[44:47]
	v_mfma_f32_16x16x32_f16 v[36:39], v[206:209], v[182:185], v[36:39]
	v_mfma_f32_16x16x32_f16 v[28:31], v[214:217], v[182:185], v[28:31]
	v_mfma_f32_16x16x32_f16 v[20:23], v[206:209], v[190:193], v[20:23]
	v_mfma_f32_16x16x32_f16 v[12:15], v[214:217], v[190:193], v[12:15]
	v_mfma_f32_16x16x32_f16 v[4:7], v[206:209], v[198:201], v[4:7]
	v_mfma_f32_16x16x32_f16 v[0:3], v[214:217], v[198:201], v[0:3]
	s_barrier
	s_add_i32 s74, 0, 0x18000
	v_add_u32_e32 v140, s74, v168
	ds_read_b128 v[128:131], v140
	ds_read_b128 v[132:135], v140 offset:1024
	ds_read_b128 v[136:139], v140 offset:2048
	ds_read_b128 v[140:143], v140 offset:3072
	s_add_u32 s34, s34, 0x30000
	s_addc_u32 s35, s35, 0
	s_mov_b32 m0, s45
	ds_read_b128 v[158:161], v173 offset:32768
	ds_read_b128 v[162:165], v173 offset:33792
	ds_read_b128 v[178:181], v173 offset:34816
	ds_read_b128 v[182:185], v173 offset:35840
	ds_read_b128 v[186:189], v173 offset:36864
	ds_read_b128 v[190:193], v173 offset:37888
	ds_read_b128 v[194:197], v173 offset:38912
	ds_read_b128 v[198:201], v173 offset:39936
	global_load_lds_dwordx4 v144, s[34:35]
	s_mov_b32 m0, s46
	s_nop 0
	global_load_lds_dwordx4 v148, s[34:35]
	s_waitcnt lgkmcnt(8)
	s_barrier
	s_waitcnt lgkmcnt(0)
	v_mfma_f32_16x16x32_f16 v[124:127], v[128:131], v[158:161], v[124:127]
	v_mfma_f32_16x16x32_f16 v[120:123], v[136:139], v[158:161], v[120:123]
	v_mfma_f32_16x16x32_f16 v[108:111], v[128:131], v[178:181], v[108:111]
	v_mfma_f32_16x16x32_f16 v[104:107], v[136:139], v[178:181], v[104:107]
	v_mfma_f32_16x16x32_f16 v[96:99], v[128:131], v[186:189], v[96:99]
	v_mfma_f32_16x16x32_f16 v[88:91], v[136:139], v[186:189], v[88:91]
	v_mfma_f32_16x16x32_f16 v[80:83], v[128:131], v[194:197], v[80:83]
	v_mfma_f32_16x16x32_f16 v[72:75], v[136:139], v[194:197], v[72:75]
	v_mfma_f32_16x16x32_f16 v[124:127], v[132:135], v[162:165], v[124:127]
	v_mfma_f32_16x16x32_f16 v[120:123], v[140:143], v[162:165], v[120:123]
	v_mfma_f32_16x16x32_f16 v[108:111], v[132:135], v[182:185], v[108:111]
	v_mfma_f32_16x16x32_f16 v[104:107], v[140:143], v[182:185], v[104:107]
	v_mfma_f32_16x16x32_f16 v[96:99], v[132:135], v[190:193], v[96:99]
	v_mfma_f32_16x16x32_f16 v[88:91], v[140:143], v[190:193], v[88:91]
	v_mfma_f32_16x16x32_f16 v[80:83], v[132:135], v[198:201], v[80:83]
	v_mfma_f32_16x16x32_f16 v[72:75], v[140:143], v[198:201], v[72:75]
	s_barrier
	s_add_i32 s34, 0, 0x1c000
	s_add_i32 s35, s74, s42
	v_add_u32_e32 v177, s34, v168
	s_mov_b32 m0, s35
	ds_read_b128 v[202:205], v177
	ds_read_b128 v[206:209], v177 offset:1024
	ds_read_b128 v[210:213], v177 offset:2048
	ds_read_b128 v[214:217], v177 offset:3072
	global_load_lds_dwordx4 v146, s[78:79]
	s_add_i32 m0, s35, 0x2000
	s_nop 0
	global_load_lds_dwordx4 v150, s[78:79]
	s_barrier
	s_waitcnt lgkmcnt(0)
	v_mfma_f32_16x16x32_f16 v[116:119], v[202:205], v[158:161], v[116:119]
	v_mfma_f32_16x16x32_f16 v[112:115], v[210:213], v[158:161], v[112:115]
	v_mfma_f32_16x16x32_f16 v[100:103], v[202:205], v[178:181], v[100:103]
	v_mfma_f32_16x16x32_f16 v[92:95], v[210:213], v[178:181], v[92:95]
	v_mfma_f32_16x16x32_f16 v[84:87], v[202:205], v[186:189], v[84:87]
	v_mfma_f32_16x16x32_f16 v[76:79], v[210:213], v[186:189], v[76:79]
	v_mfma_f32_16x16x32_f16 v[68:71], v[202:205], v[194:197], v[68:71]
	v_mfma_f32_16x16x32_f16 v[64:67], v[210:213], v[194:197], v[64:67]
	v_mfma_f32_16x16x32_f16 v[116:119], v[206:209], v[162:165], v[116:119]
	v_mfma_f32_16x16x32_f16 v[112:115], v[214:217], v[162:165], v[112:115]
	v_mfma_f32_16x16x32_f16 v[100:103], v[206:209], v[182:185], v[100:103]
	v_mfma_f32_16x16x32_f16 v[92:95], v[214:217], v[182:185], v[92:95]
	v_mfma_f32_16x16x32_f16 v[84:87], v[206:209], v[190:193], v[84:87]
	v_mfma_f32_16x16x32_f16 v[76:79], v[214:217], v[190:193], v[76:79]
	v_mfma_f32_16x16x32_f16 v[68:71], v[206:209], v[198:201], v[68:71]
	v_mfma_f32_16x16x32_f16 v[64:67], v[214:217], v[198:201], v[64:67]
	s_barrier
	s_mov_b32 m0, s49
	ds_read_b128 v[158:161], v173 offset:49152
	ds_read_b128 v[162:165], v173 offset:50176
	ds_read_b128 v[178:181], v173 offset:51200
	ds_read_b128 v[182:185], v173 offset:52224
	ds_read_b128 v[186:189], v173 offset:53248
	ds_read_b128 v[190:193], v173 offset:54272
	ds_read_b128 v[194:197], v173 offset:55296
	ds_read_b128 v[198:201], v173 offset:56320
	global_load_lds_dwordx4 v144, s[80:81]
	s_mov_b32 m0, s50
	s_nop 0
	global_load_lds_dwordx4 v148, s[80:81]
	s_barrier
	s_waitcnt lgkmcnt(0)
	v_mfma_f32_16x16x32_f16 v[60:63], v[128:131], v[158:161], v[60:63]
	v_mfma_f32_16x16x32_f16 v[56:59], v[136:139], v[158:161], v[56:59]
	v_mfma_f32_16x16x32_f16 v[48:51], v[128:131], v[178:181], v[48:51]
	v_mfma_f32_16x16x32_f16 v[40:43], v[136:139], v[178:181], v[40:43]
	v_mfma_f32_16x16x32_f16 v[32:35], v[128:131], v[186:189], v[32:35]
	v_mfma_f32_16x16x32_f16 v[24:27], v[136:139], v[186:189], v[24:27]
	v_mfma_f32_16x16x32_f16 v[16:19], v[128:131], v[194:197], v[16:19]
	v_mfma_f32_16x16x32_f16 v[8:11], v[136:139], v[194:197], v[8:11]
	v_mfma_f32_16x16x32_f16 v[60:63], v[132:135], v[162:165], v[60:63]
	v_mfma_f32_16x16x32_f16 v[56:59], v[140:143], v[162:165], v[56:59]
	v_mfma_f32_16x16x32_f16 v[48:51], v[132:135], v[182:185], v[48:51]
	v_mfma_f32_16x16x32_f16 v[40:43], v[140:143], v[182:185], v[40:43]
	v_mfma_f32_16x16x32_f16 v[32:35], v[132:135], v[190:193], v[32:35]
	v_mfma_f32_16x16x32_f16 v[24:27], v[140:143], v[190:193], v[24:27]
	v_mfma_f32_16x16x32_f16 v[16:19], v[132:135], v[198:201], v[16:19]
	v_mfma_f32_16x16x32_f16 v[8:11], v[140:143], v[198:201], v[8:11]
	s_barrier
	s_add_u32 s30, s30, 0xc080
	s_addc_u32 s31, s31, 0
	s_add_i32 s34, s34, s42
	s_mov_b32 m0, s34
	s_nop 0
	global_load_lds_dwordx4 v146, s[30:31]
	s_add_i32 m0, s34, 0x2000
	s_nop 0
	global_load_lds_dwordx4 v150, s[30:31]
	s_waitcnt vmcnt(6)
	s_barrier
	v_mfma_f32_16x16x32_f16 v[52:55], v[202:205], v[158:161], v[52:55]
	v_mfma_f32_16x16x32_f16 v[44:47], v[210:213], v[158:161], v[44:47]
	v_mfma_f32_16x16x32_f16 v[36:39], v[202:205], v[178:181], v[36:39]
	v_mfma_f32_16x16x32_f16 v[28:31], v[210:213], v[178:181], v[28:31]
	v_mfma_f32_16x16x32_f16 v[20:23], v[202:205], v[186:189], v[20:23]
	v_mfma_f32_16x16x32_f16 v[12:15], v[210:213], v[186:189], v[12:15]
	v_mfma_f32_16x16x32_f16 v[4:7], v[202:205], v[194:197], v[4:7]
	v_mfma_f32_16x16x32_f16 v[0:3], v[210:213], v[194:197], v[0:3]
	v_mfma_f32_16x16x32_f16 v[52:55], v[206:209], v[162:165], v[52:55]
	v_mfma_f32_16x16x32_f16 v[44:47], v[214:217], v[162:165], v[44:47]
	v_mfma_f32_16x16x32_f16 v[36:39], v[206:209], v[182:185], v[36:39]
	v_mfma_f32_16x16x32_f16 v[28:31], v[214:217], v[182:185], v[28:31]
	v_mfma_f32_16x16x32_f16 v[20:23], v[206:209], v[190:193], v[20:23]
	v_mfma_f32_16x16x32_f16 v[12:15], v[214:217], v[190:193], v[12:15]
	v_mfma_f32_16x16x32_f16 v[4:7], v[206:209], v[198:201], v[4:7]
	v_mfma_f32_16x16x32_f16 v[0:3], v[214:217], v[198:201], v[0:3]
	s_barrier
	s_add_i32 s73, s73, 2
	s_add_u32 s28, s28, 0x100
	s_addc_u32 s29, s29, 0
	s_add_u32 s71, s71, 0x100
	s_addc_u32 s72, s72, 0
	s_cmp_gt_u32 s73, 9
	s_cbranch_scc0 .LBB9_27
	s_lshl_b32 s28, s70, 8
	s_add_i32 s28, s28, s48
	s_lshl_b32 s29, s68, 8
	s_or_b32 s29, s29, s51
	s_waitcnt vmcnt(6)
	v_pk_fma_f32 v[126:127], v[126:127], v[226:227], v[236:237] op_sel_hi:[1,0,1]
	v_pk_fma_f32 v[124:125], v[124:125], v[226:227], v[234:235] op_sel_hi:[1,0,1]
	v_pk_fma_f32 v[122:123], v[122:123], v[226:227], v[240:241] op_sel_hi:[1,0,1]
	v_pk_fma_f32 v[120:121], v[120:121], v[226:227], v[238:239] op_sel_hi:[1,0,1]
	v_cvt_pk_f16_f32 v124, v124, v125
	v_cvt_pk_f16_f32 v125, v126, v127
	v_cvt_pk_f16_f32 v126, v120, v121
	v_cvt_pk_f16_f32 v123, v122, v123
	v_pk_fma_f32 v[118:119], v[118:119], v[226:227], v[244:245] op_sel_hi:[1,0,1]
	v_pk_fma_f32 v[116:117], v[116:117], v[226:227], v[242:243] op_sel_hi:[1,0,1]
	v_pk_fma_f32 v[114:115], v[114:115], v[226:227], v[248:249] op_sel_hi:[1,0,1]
	v_pk_fma_f32 v[112:113], v[112:113], v[226:227], v[246:247] op_sel_hi:[1,0,1]
	v_pk_max_f16 v120, v124, 0
	v_pk_max_f16 v121, v125, 0
	v_pk_max_f16 v122, v126, 0
	v_pk_max_f16 v123, v123, 0
	v_cvt_pk_f16_f32 v116, v116, v117
	v_cvt_pk_f16_f32 v117, v118, v119
	v_cvt_pk_f16_f32 v118, v112, v113
	v_cvt_pk_f16_f32 v115, v114, v115
	v_pk_fma_f32 v[110:111], v[110:111], v[226:227], v[236:237] op_sel:[0,1,0]
	v_pk_fma_f32 v[108:109], v[108:109], v[226:227], v[234:235] op_sel:[0,1,0]
	v_pk_fma_f32 v[106:107], v[106:107], v[226:227], v[240:241] op_sel:[0,1,0]
	v_pk_fma_f32 v[104:105], v[104:105], v[226:227], v[238:239] op_sel:[0,1,0]
	v_pk_fma_f32 v[102:103], v[102:103], v[226:227], v[244:245] op_sel:[0,1,0]
	v_pk_fma_f32 v[100:101], v[100:101], v[226:227], v[242:243] op_sel:[0,1,0]
	v_pk_fma_f32 v[94:95], v[94:95], v[226:227], v[248:249] op_sel:[0,1,0]
	v_pk_fma_f32 v[92:93], v[92:93], v[226:227], v[246:247] op_sel:[0,1,0]
	ds_write_b128 v175, v[120:123]
	v_or_b32_e32 v120, s28, v169
	v_pk_max_f16 v112, v116, 0
	v_pk_max_f16 v113, v117, 0
	v_pk_max_f16 v114, v118, 0
	v_pk_max_f16 v115, v115, 0
	v_cvt_pk_f16_f32 v108, v108, v109
	v_cvt_pk_f16_f32 v109, v110, v111
	v_cvt_pk_f16_f32 v110, v104, v105
	v_cvt_pk_f16_f32 v107, v106, v107
	v_cvt_pk_f16_f32 v100, v100, v101
	v_cvt_pk_f16_f32 v101, v102, v103
	v_cvt_pk_f16_f32 v102, v92, v93
	v_cvt_pk_f16_f32 v95, v94, v95
	ds_write_b128 v175, v[112:115] offset:64
	v_mul_lo_u32 v116, v120, s10
	v_pk_max_f16 v104, v108, 0
	v_pk_max_f16 v105, v109, 0
	v_pk_max_f16 v106, v110, 0
	v_pk_max_f16 v107, v107, 0
	v_pk_max_f16 v92, v100, 0
	v_pk_max_f16 v93, v101, 0
	v_pk_max_f16 v94, v102, 0
	v_pk_max_f16 v95, v95, 0
	ds_read_b128 v[112:115], v176
	v_add_u32_e32 v120, s29, v116
	ds_read_b128 v[116:119], v176 offset:1152
	ds_write_b128 v175, v[104:107]
	ds_write_b128 v175, v[92:95] offset:64
	ds_read_b128 v[92:95], v176
	ds_read_b128 v[100:103], v176 offset:1152
	v_lshlrev_b32_e32 v121, 1, v120
	v_add_u32_e32 v122, v121, v170
	v_add_u32_e32 v104, s55, v121
	s_waitcnt lgkmcnt(0)
	buffer_store_dwordx4 v[112:115], v122, s[20:23], 0 offen nt
	v_add_u32_e32 v105, v104, v170
	v_pk_fma_f32 v[90:91], v[90:91], v[228:229], v[240:241] op_sel_hi:[1,0,1]
	v_add_u32_e32 v112, v121, v171
	buffer_store_dwordx4 v[116:119], v112, s[20:23], 0 offen nt
	buffer_store_dwordx4 v[92:95], v105, s[20:23], 0 offen nt
	v_pk_fma_f32 v[88:89], v[88:89], v[228:229], v[238:239] op_sel_hi:[1,0,1]
	v_pk_fma_f32 v[86:87], v[86:87], v[228:229], v[244:245] op_sel_hi:[1,0,1]
	v_pk_fma_f32 v[92:93], v[98:99], v[228:229], v[236:237] op_sel_hi:[1,0,1]
	v_pk_fma_f32 v[94:95], v[96:97], v[228:229], v[234:235] op_sel_hi:[1,0,1]
	v_pk_fma_f32 v[84:85], v[84:85], v[228:229], v[242:243] op_sel_hi:[1,0,1]
	v_pk_fma_f32 v[78:79], v[78:79], v[228:229], v[248:249] op_sel_hi:[1,0,1]
	v_pk_fma_f32 v[76:77], v[76:77], v[228:229], v[246:247] op_sel_hi:[1,0,1]
	v_cvt_pk_f16_f32 v94, v94, v95
	v_cvt_pk_f16_f32 v92, v92, v93
	v_cvt_pk_f16_f32 v93, v88, v89
	v_cvt_pk_f16_f32 v91, v90, v91
	v_cvt_pk_f16_f32 v84, v84, v85
	v_cvt_pk_f16_f32 v85, v86, v87
	v_cvt_pk_f16_f32 v86, v76, v77
	v_cvt_pk_f16_f32 v79, v78, v79
	v_pk_max_f16 v88, v94, 0
	v_pk_max_f16 v89, v92, 0
	v_pk_max_f16 v90, v93, 0
	v_pk_max_f16 v91, v91, 0
	v_pk_max_f16 v76, v84, 0
	v_pk_max_f16 v77, v85, 0
	v_pk_max_f16 v78, v86, 0
	v_pk_max_f16 v79, v79, 0
	ds_write_b128 v175, v[88:91]
	ds_write_b128 v175, v[76:79] offset:64
	ds_read_b128 v[76:79], v176
	ds_read_b128 v[84:87], v176 offset:1152
	v_add_u32_e32 v88, s55, v104
	v_add_u32_e32 v105, v104, v171
	v_add_u32_e32 v89, v88, v170
	buffer_store_dwordx4 v[100:103], v105, s[20:23], 0 offen nt
	s_waitcnt lgkmcnt(1)
	buffer_store_dwordx4 v[76:79], v89, s[20:23], 0 offen nt
	v_pk_fma_f32 v[74:75], v[74:75], v[228:229], v[240:241] op_sel:[0,1,0]
	v_pk_fma_f32 v[72:73], v[72:73], v[228:229], v[238:239] op_sel:[0,1,0]
	v_add_u32_e32 v76, v88, v171
	s_waitcnt lgkmcnt(0)
	buffer_store_dwordx4 v[84:87], v76, s[20:23], 0 offen nt
	v_pk_fma_f32 v[76:77], v[82:83], v[228:229], v[236:237] op_sel:[0,1,0]
	v_pk_fma_f32 v[78:79], v[80:81], v[228:229], v[234:235] op_sel:[0,1,0]
	v_pk_fma_f32 v[70:71], v[70:71], v[228:229], v[244:245] op_sel:[0,1,0]
	v_pk_fma_f32 v[68:69], v[68:69], v[228:229], v[242:243] op_sel:[0,1,0]
	v_pk_fma_f32 v[66:67], v[66:67], v[228:229], v[248:249] op_sel:[0,1,0]
	v_pk_fma_f32 v[64:65], v[64:65], v[228:229], v[246:247] op_sel:[0,1,0]
	v_cvt_pk_f16_f32 v78, v78, v79
	v_cvt_pk_f16_f32 v76, v76, v77
	v_cvt_pk_f16_f32 v77, v72, v73
	v_cvt_pk_f16_f32 v75, v74, v75
	v_cvt_pk_f16_f32 v68, v68, v69
	v_cvt_pk_f16_f32 v69, v70, v71
	v_cvt_pk_f16_f32 v70, v64, v65
	v_cvt_pk_f16_f32 v67, v66, v67
	v_pk_fma_f32 v[62:63], v[62:63], v[230:231], v[236:237] op_sel_hi:[1,0,1]
	v_pk_fma_f32 v[60:61], v[60:61], v[230:231], v[234:235] op_sel_hi:[1,0,1]
	v_pk_fma_f32 v[58:59], v[58:59], v[230:231], v[240:241] op_sel_hi:[1,0,1]
	v_pk_fma_f32 v[56:57], v[56:57], v[230:231], v[238:239] op_sel_hi:[1,0,1]
	v_pk_fma_f32 v[54:55], v[54:55], v[230:231], v[244:245] op_sel_hi:[1,0,1]
	v_pk_fma_f32 v[52:53], v[52:53], v[230:231], v[242:243] op_sel_hi:[1,0,1]
	v_pk_fma_f32 v[46:47], v[46:47], v[230:231], v[248:249] op_sel_hi:[1,0,1]
	v_pk_fma_f32 v[44:45], v[44:45], v[230:231], v[246:247] op_sel_hi:[1,0,1]
	v_pk_max_f16 v72, v78, 0
	v_pk_max_f16 v73, v76, 0
	v_pk_max_f16 v74, v77, 0
	v_pk_max_f16 v75, v75, 0
	v_pk_max_f16 v64, v68, 0
	v_pk_max_f16 v65, v69, 0
	v_pk_max_f16 v66, v70, 0
	v_pk_max_f16 v67, v67, 0
	v_cvt_pk_f16_f32 v60, v60, v61
	v_cvt_pk_f16_f32 v61, v62, v63
	v_cvt_pk_f16_f32 v62, v56, v57
	v_cvt_pk_f16_f32 v59, v58, v59
	v_cvt_pk_f16_f32 v52, v52, v53
	v_cvt_pk_f16_f32 v53, v54, v55
	v_cvt_pk_f16_f32 v54, v44, v45
	v_cvt_pk_f16_f32 v47, v46, v47
	ds_write_b128 v175, v[72:75]
	ds_write_b128 v175, v[64:67] offset:64
	v_pk_max_f16 v56, v60, 0
	v_pk_max_f16 v57, v61, 0
	v_pk_max_f16 v58, v62, 0
	v_pk_max_f16 v59, v59, 0
	v_pk_max_f16 v44, v52, 0
	v_pk_max_f16 v45, v53, 0
	v_pk_max_f16 v46, v54, 0
	v_pk_max_f16 v47, v47, 0
	ds_read_b128 v[64:67], v176
	ds_read_b128 v[68:71], v176 offset:1152
	ds_write_b128 v175, v[56:59]
	ds_write_b128 v175, v[44:47] offset:64
	ds_read_b128 v[44:47], v176
	ds_read_b128 v[52:55], v176 offset:1152
	v_add_u32_e32 v72, s56, v120
	v_lshlrev_b32_e32 v73, 1, v72
	v_add_u32_e32 v74, v73, v170
	v_add_u32_e32 v56, s62, v88
	s_waitcnt lgkmcnt(5)
	buffer_store_dwordx4 v[64:67], v74, s[20:23], 0 offen nt
	v_add_u32_e32 v57, v56, v170
	v_pk_fma_f32 v[42:43], v[42:43], v[230:231], v[240:241] op_sel:[0,1,0]
	v_add_u32_e32 v64, v73, v171
	s_waitcnt lgkmcnt(4)
	buffer_store_dwordx4 v[68:71], v64, s[20:23], 0 offen nt
	s_waitcnt lgkmcnt(1)
	buffer_store_dwordx4 v[44:47], v57, s[20:23], 0 offen nt
	v_pk_fma_f32 v[40:41], v[40:41], v[230:231], v[238:239] op_sel:[0,1,0]
	v_pk_fma_f32 v[38:39], v[38:39], v[230:231], v[244:245] op_sel:[0,1,0]
	v_add_u32_e32 v44, v56, v171
	s_waitcnt lgkmcnt(0)
	buffer_store_dwordx4 v[52:55], v44, s[20:23], 0 offen nt
	v_pk_fma_f32 v[44:45], v[50:51], v[230:231], v[236:237] op_sel:[0,1,0]
	v_pk_fma_f32 v[46:47], v[48:49], v[230:231], v[234:235] op_sel:[0,1,0]
	v_pk_fma_f32 v[36:37], v[36:37], v[230:231], v[242:243] op_sel:[0,1,0]
	v_pk_fma_f32 v[30:31], v[30:31], v[230:231], v[248:249] op_sel:[0,1,0]
	v_pk_fma_f32 v[28:29], v[28:29], v[230:231], v[246:247] op_sel:[0,1,0]
	v_cvt_pk_f16_f32 v46, v46, v47
	v_cvt_pk_f16_f32 v44, v44, v45
	v_cvt_pk_f16_f32 v45, v40, v41
	v_cvt_pk_f16_f32 v43, v42, v43
	v_cvt_pk_f16_f32 v36, v36, v37
	v_cvt_pk_f16_f32 v37, v38, v39
	v_cvt_pk_f16_f32 v38, v28, v29
	v_cvt_pk_f16_f32 v31, v30, v31
	v_pk_max_f16 v40, v46, 0
	v_pk_max_f16 v41, v44, 0
	v_pk_max_f16 v42, v45, 0
	v_pk_max_f16 v43, v43, 0
	v_pk_max_f16 v28, v36, 0
	v_pk_max_f16 v29, v37, 0
	v_pk_max_f16 v30, v38, 0
	v_pk_max_f16 v31, v31, 0
	ds_write_b128 v175, v[40:43]
	ds_write_b128 v175, v[28:31] offset:64
	ds_read_b128 v[28:31], v176
	ds_read_b128 v[36:39], v176 offset:1152
	v_add_u32_e32 v40, s63, v72
	v_lshlrev_b32_e32 v41, 1, v40
	v_add_u32_e32 v42, v41, v170
	s_waitcnt lgkmcnt(1)
	buffer_store_dwordx4 v[28:31], v42, s[20:23], 0 offen nt
	v_pk_fma_f32 v[26:27], v[26:27], v[232:233], v[240:241] op_sel_hi:[1,0,1]
	v_pk_fma_f32 v[24:25], v[24:25], v[232:233], v[238:239] op_sel_hi:[1,0,1]
	v_add_u32_e32 v28, v41, v171
	s_waitcnt lgkmcnt(0)
	buffer_store_dwordx4 v[36:39], v28, s[20:23], 0 offen nt
	v_pk_fma_f32 v[28:29], v[34:35], v[232:233], v[236:237] op_sel_hi:[1,0,1]
	v_pk_fma_f32 v[30:31], v[32:33], v[232:233], v[234:235] op_sel_hi:[1,0,1]
	v_pk_fma_f32 v[22:23], v[22:23], v[232:233], v[244:245] op_sel_hi:[1,0,1]
	v_pk_fma_f32 v[20:21], v[20:21], v[232:233], v[242:243] op_sel_hi:[1,0,1]
	v_pk_fma_f32 v[14:15], v[14:15], v[232:233], v[248:249] op_sel_hi:[1,0,1]
	v_pk_fma_f32 v[12:13], v[12:13], v[232:233], v[246:247] op_sel_hi:[1,0,1]
	v_cvt_pk_f16_f32 v30, v30, v31
	v_cvt_pk_f16_f32 v28, v28, v29
	v_cvt_pk_f16_f32 v29, v24, v25
	v_cvt_pk_f16_f32 v27, v26, v27
	v_cvt_pk_f16_f32 v20, v20, v21
	v_cvt_pk_f16_f32 v21, v22, v23
	v_cvt_pk_f16_f32 v22, v12, v13
	v_cvt_pk_f16_f32 v15, v14, v15
	v_pk_max_f16 v24, v30, 0
	v_pk_max_f16 v25, v28, 0
	v_pk_max_f16 v26, v29, 0
	v_pk_max_f16 v27, v27, 0
	v_pk_max_f16 v12, v20, 0
	v_pk_max_f16 v13, v21, 0
	v_pk_max_f16 v14, v22, 0
	v_pk_max_f16 v15, v15, 0
	ds_write_b128 v175, v[24:27]
	ds_write_b128 v175, v[12:15] offset:64
	ds_read_b128 v[12:15], v176
	ds_read_b128 v[20:23], v176 offset:1152
	v_add_u32_e32 v24, s64, v40
	v_lshlrev_b32_e32 v25, 1, v24
	v_add_u32_e32 v26, v25, v170
	s_waitcnt lgkmcnt(1)
	buffer_store_dwordx4 v[12:15], v26, s[20:23], 0 offen nt
	v_pk_fma_f32 v[10:11], v[10:11], v[232:233], v[240:241] op_sel:[0,1,0]
	v_pk_fma_f32 v[8:9], v[8:9], v[232:233], v[238:239] op_sel:[0,1,0]
	v_pk_fma_f32 v[12:13], v[18:19], v[232:233], v[236:237] op_sel:[0,1,0]
	v_pk_fma_f32 v[14:15], v[16:17], v[232:233], v[234:235] op_sel:[0,1,0]
	v_pk_fma_f32 v[6:7], v[6:7], v[232:233], v[244:245] op_sel:[0,1,0]
	v_pk_fma_f32 v[4:5], v[4:5], v[232:233], v[242:243] op_sel:[0,1,0]
	v_pk_fma_f32 v[2:3], v[2:3], v[232:233], v[248:249] op_sel:[0,1,0]
	v_pk_fma_f32 v[0:1], v[0:1], v[232:233], v[246:247] op_sel:[0,1,0]
	v_cvt_pk_f16_f32 v14, v14, v15
	v_cvt_pk_f16_f32 v12, v12, v13
	v_cvt_pk_f16_f32 v13, v8, v9
	v_cvt_pk_f16_f32 v11, v10, v11
	v_cvt_pk_f16_f32 v4, v4, v5
	v_cvt_pk_f16_f32 v5, v6, v7
	v_cvt_pk_f16_f32 v6, v0, v1
	v_cvt_pk_f16_f32 v3, v2, v3
	v_pk_max_f16 v8, v14, 0
	v_pk_max_f16 v9, v12, 0
	v_pk_max_f16 v10, v13, 0
	v_pk_max_f16 v11, v11, 0
	v_pk_max_f16 v0, v4, 0
	v_pk_max_f16 v1, v5, 0
	v_pk_max_f16 v2, v6, 0
	v_pk_max_f16 v3, v3, 0
	ds_write_b128 v175, v[8:11]
	ds_write_b128 v175, v[0:3] offset:64
	ds_read_b128 v[0:3], v176
	ds_read_b128 v[4:7], v176 offset:1152
	v_add_lshl_u32 v8, v24, s64, 1
	v_add_u32_e32 v25, v25, v171
	v_add_u32_e32 v9, v8, v170
	s_waitcnt lgkmcnt(4)
	buffer_store_dwordx4 v[20:23], v25, s[20:23], 0 offen nt
	s_waitcnt lgkmcnt(1)
	buffer_store_dwordx4 v[0:3], v9, s[20:23], 0 offen nt
	s_mov_b32 s68, s67
	s_mov_b32 s70, s69
	v_add_u32_e32 v0, v8, v171
	s_mov_b64 s[30:31], s[0:1]
	s_mov_b64 s[28:29], s[8:9]
	s_mov_b64 vcc, s[6:7]
	s_waitcnt lgkmcnt(0)
	buffer_store_dwordx4 v[4:7], v0, s[20:23], 0 offen nt
	s_cbranch_vccz .LBB9_12
	s_waitcnt vmcnt(0)
	s_cmpk_gt_u32 s36, 0xff
	s_cbranch_scc1 .LBB9_31
	s_barrier

.LBB9_32:
	s_endpgm
	s_endpgm
	s_endpgm
	s_endpgm
	s_endpgm
	s_endpgm
	s_endpgm
	s_endpgm
	s_endpgm
	s_endpgm
	s_endpgm
	s_endpgm
	s_endpgm
	s_endpgm
	s_endpgm
	s_endpgm
	s_endpgm
	s_endpgm
	s_endpgm
	s_endpgm
	s_endpgm
	s_endpgm
	s_endpgm
	s_endpgm
	s_endpgm
	s_endpgm
	s_endpgm
	s_endpgm
	s_endpgm
	s_endpgm
	s_endpgm
	s_endpgm
	s_endpgm
	s_endpgm
	s_endpgm
	s_endpgm
	s_endpgm
	s_endpgm
	s_endpgm

.LBB10_27:
	ds_read_b128 v[72:75], v231
	ds_read_b128 v[80:83], v231 offset:1024
	ds_read_b128 v[88:91], v231 offset:2048
	ds_read_b128 v[92:95], v231 offset:3072
	s_add_u32 s40, s38, 0xfff40080
	s_addc_u32 s41, s39, -1
	s_cmp_eq_u32 s87, 44
	s_cselect_b32 s43, s9, s41
	s_cselect_b32 s42, s8, s40
	s_cselect_b32 s41, s1, s86
	s_cselect_b32 s40, s0, s85
	s_add_i32 m0, s51, 0xc000
	ds_read_b128 v[136:139], v232
	ds_read_b128 v[148:151], v232 offset:1024
	ds_read_b128 v[152:155], v232 offset:2048
	ds_read_b128 v[156:159], v232 offset:3072
	ds_read_b128 v[160:163], v232 offset:4096
	ds_read_b128 v[164:167], v232 offset:5120
	ds_read_b128 v[168:171], v232 offset:6144
	ds_read_b128 v[172:175], v232 offset:7168
	global_load_lds_dwordx4 v184, s[38:39]
	s_add_i32 m0, s51, 0xe000
	s_nop 0
	global_load_lds_dwordx4 v186, s[38:39]
	s_waitcnt lgkmcnt(8)
	s_barrier
	s_waitcnt lgkmcnt(0)
	v_mfma_f32_16x16x32_f16 v[144:147], v[72:75], v[136:139], v[144:147]
	v_mfma_f32_16x16x32_f16 v[140:143], v[88:91], v[136:139], v[140:143]
	v_mfma_f32_16x16x32_f16 v[124:127], v[72:75], v[152:155], v[124:127]
	v_mfma_f32_16x16x32_f16 v[120:123], v[88:91], v[152:155], v[120:123]
	v_mfma_f32_16x16x32_f16 v[108:111], v[72:75], v[160:163], v[108:111]
	v_mfma_f32_16x16x32_f16 v[104:107], v[88:91], v[160:163], v[104:107]
	v_mfma_f32_16x16x32_f16 v[84:87], v[72:75], v[168:171], v[84:87]
	v_mfma_f32_16x16x32_f16 v[76:79], v[88:91], v[168:171], v[76:79]
	v_mfma_f32_16x16x32_f16 v[144:147], v[80:83], v[148:151], v[144:147]
	v_mfma_f32_16x16x32_f16 v[140:143], v[92:95], v[148:151], v[140:143]
	v_mfma_f32_16x16x32_f16 v[124:127], v[80:83], v[156:159], v[124:127]
	v_mfma_f32_16x16x32_f16 v[120:123], v[92:95], v[156:159], v[120:123]
	v_mfma_f32_16x16x32_f16 v[108:111], v[80:83], v[164:167], v[108:111]
	v_mfma_f32_16x16x32_f16 v[104:107], v[92:95], v[164:167], v[104:107]
	v_mfma_f32_16x16x32_f16 v[84:87], v[80:83], v[172:175], v[84:87]
	v_mfma_f32_16x16x32_f16 v[76:79], v[92:95], v[172:175], v[76:79]
	s_barrier
	s_add_i32 s88, s69, s50
	s_add_u32 s92, s40, 0x80
	s_addc_u32 s93, s41, 0
	s_mov_b32 m0, s88
	ds_read_b128 v[190:193], v233
	ds_read_b128 v[194:197], v233 offset:1024
	ds_read_b128 v[198:201], v233 offset:2048
	ds_read_b128 v[202:205], v233 offset:3072
	global_load_lds_dwordx4 v178, s[40:41]
	s_add_i32 m0, s88, 0x2000
	s_nop 0
	global_load_lds_dwordx4 v182, s[40:41]
	s_barrier
	s_waitcnt lgkmcnt(0)
	v_mfma_f32_16x16x32_f16 v[132:135], v[190:193], v[136:139], v[132:135]
	v_mfma_f32_16x16x32_f16 v[128:131], v[198:201], v[136:139], v[128:131]
	v_mfma_f32_16x16x32_f16 v[116:119], v[190:193], v[152:155], v[116:119]
	v_mfma_f32_16x16x32_f16 v[112:115], v[198:201], v[152:155], v[112:115]
	v_mfma_f32_16x16x32_f16 v[100:103], v[190:193], v[160:163], v[100:103]
	v_mfma_f32_16x16x32_f16 v[96:99], v[198:201], v[160:163], v[96:99]
	v_mfma_f32_16x16x32_f16 v[68:71], v[190:193], v[168:171], v[68:71]
	v_mfma_f32_16x16x32_f16 v[64:67], v[198:201], v[168:171], v[64:67]
	v_mfma_f32_16x16x32_f16 v[132:135], v[194:197], v[148:151], v[132:135]
	v_mfma_f32_16x16x32_f16 v[128:131], v[202:205], v[148:151], v[128:131]
	v_mfma_f32_16x16x32_f16 v[116:119], v[194:197], v[156:159], v[116:119]
	v_mfma_f32_16x16x32_f16 v[112:115], v[202:205], v[156:159], v[112:115]
	v_mfma_f32_16x16x32_f16 v[100:103], v[194:197], v[164:167], v[100:103]
	v_mfma_f32_16x16x32_f16 v[96:99], v[202:205], v[164:167], v[96:99]
	v_mfma_f32_16x16x32_f16 v[68:71], v[194:197], v[172:175], v[68:71]
	v_mfma_f32_16x16x32_f16 v[64:67], v[202:205], v[172:175], v[64:67]
	s_barrier
	s_mov_b32 m0, s51
	s_add_u32 s94, s42, 0x80
	s_addc_u32 s95, s43, 0
	ds_read_b128 v[136:139], v232 offset:16384
	ds_read_b128 v[148:151], v232 offset:17408
	ds_read_b128 v[152:155], v232 offset:18432
	ds_read_b128 v[156:159], v232 offset:19456
	ds_read_b128 v[160:163], v232 offset:20480
	ds_read_b128 v[164:167], v232 offset:21504
	ds_read_b128 v[168:171], v232 offset:22528
	ds_read_b128 v[172:175], v232 offset:23552
	global_load_lds_dwordx4 v176, s[42:43]
	s_mov_b32 m0, s52
	s_nop 0
	global_load_lds_dwordx4 v180, s[42:43]
	s_barrier
	s_waitcnt lgkmcnt(0)
	v_mfma_f32_16x16x32_f16 v[60:63], v[72:75], v[136:139], v[60:63]
	v_mfma_f32_16x16x32_f16 v[56:59], v[88:91], v[136:139], v[56:59]
	v_mfma_f32_16x16x32_f16 v[44:47], v[72:75], v[152:155], v[44:47]
	v_mfma_f32_16x16x32_f16 v[40:43], v[88:91], v[152:155], v[40:43]
	v_mfma_f32_16x16x32_f16 v[28:31], v[72:75], v[160:163], v[28:31]
	v_mfma_f32_16x16x32_f16 v[24:27], v[88:91], v[160:163], v[24:27]
	v_mfma_f32_16x16x32_f16 v[12:15], v[72:75], v[168:171], v[12:15]
	v_mfma_f32_16x16x32_f16 v[8:11], v[88:91], v[168:171], v[8:11]
	v_mfma_f32_16x16x32_f16 v[60:63], v[80:83], v[148:151], v[60:63]
	v_mfma_f32_16x16x32_f16 v[56:59], v[92:95], v[148:151], v[56:59]
	v_mfma_f32_16x16x32_f16 v[44:47], v[80:83], v[156:159], v[44:47]
	v_mfma_f32_16x16x32_f16 v[40:43], v[92:95], v[156:159], v[40:43]
	v_mfma_f32_16x16x32_f16 v[28:31], v[80:83], v[164:167], v[28:31]
	v_mfma_f32_16x16x32_f16 v[24:27], v[92:95], v[164:167], v[24:27]
	v_mfma_f32_16x16x32_f16 v[12:15], v[80:83], v[172:175], v[12:15]
	v_mfma_f32_16x16x32_f16 v[8:11], v[92:95], v[172:175], v[8:11]
	s_barrier
	s_add_u32 s88, s40, 0x30000
	s_addc_u32 s89, s41, 0
	s_add_i32 s90, s70, s50
	s_mov_b32 m0, s90
	s_nop 0
	global_load_lds_dwordx4 v178, s[88:89]
	s_add_i32 m0, s90, 0x2000
	s_nop 0
	global_load_lds_dwordx4 v182, s[88:89]
	s_waitcnt vmcnt(6)
	s_barrier
	v_mfma_f32_16x16x32_f16 v[52:55], v[190:193], v[136:139], v[52:55]
	v_mfma_f32_16x16x32_f16 v[48:51], v[198:201], v[136:139], v[48:51]
	v_mfma_f32_16x16x32_f16 v[36:39], v[190:193], v[152:155], v[36:39]
	v_mfma_f32_16x16x32_f16 v[32:35], v[198:201], v[152:155], v[32:35]
	v_mfma_f32_16x16x32_f16 v[20:23], v[190:193], v[160:163], v[20:23]
	v_mfma_f32_16x16x32_f16 v[16:19], v[198:201], v[160:163], v[16:19]
	v_mfma_f32_16x16x32_f16 v[4:7], v[190:193], v[168:171], v[4:7]
	v_mfma_f32_16x16x32_f16 v[0:3], v[198:201], v[168:171], v[0:3]
	v_mfma_f32_16x16x32_f16 v[52:55], v[194:197], v[148:151], v[52:55]
	v_mfma_f32_16x16x32_f16 v[48:51], v[202:205], v[148:151], v[48:51]
	v_mfma_f32_16x16x32_f16 v[36:39], v[194:197], v[156:159], v[36:39]
	v_mfma_f32_16x16x32_f16 v[32:35], v[202:205], v[156:159], v[32:35]
	v_mfma_f32_16x16x32_f16 v[20:23], v[194:197], v[164:167], v[20:23]
	v_mfma_f32_16x16x32_f16 v[16:19], v[202:205], v[164:167], v[16:19]
	v_mfma_f32_16x16x32_f16 v[4:7], v[194:197], v[172:175], v[4:7]
	v_mfma_f32_16x16x32_f16 v[0:3], v[202:205], v[172:175], v[0:3]
	s_barrier
	s_add_i32 s88, 0, 0x18000
	v_add_u32_e32 v92, s88, v228
	ds_read_b128 v[72:75], v92
	ds_read_b128 v[80:83], v92 offset:1024
	ds_read_b128 v[88:91], v92 offset:2048
	ds_read_b128 v[92:95], v92 offset:3072
	s_add_u32 s42, s42, 0xc0000
	s_addc_u32 s43, s43, 0
	s_mov_b32 m0, s53
	ds_read_b128 v[136:139], v232 offset:32768
	ds_read_b128 v[148:151], v232 offset:33792
	ds_read_b128 v[152:155], v232 offset:34816
	ds_read_b128 v[156:159], v232 offset:35840
	ds_read_b128 v[160:163], v232 offset:36864
	ds_read_b128 v[164:167], v232 offset:37888
	ds_read_b128 v[168:171], v232 offset:38912
	ds_read_b128 v[172:175], v232 offset:39936
	global_load_lds_dwordx4 v176, s[42:43]
	s_mov_b32 m0, s54
	s_nop 0
	global_load_lds_dwordx4 v180, s[42:43]
	s_waitcnt lgkmcnt(8)
	s_barrier
	s_waitcnt lgkmcnt(0)
	v_mfma_f32_16x16x32_f16 v[144:147], v[72:75], v[136:139], v[144:147]
	v_mfma_f32_16x16x32_f16 v[140:143], v[88:91], v[136:139], v[140:143]
	v_mfma_f32_16x16x32_f16 v[124:127], v[72:75], v[152:155], v[124:127]
	v_mfma_f32_16x16x32_f16 v[120:123], v[88:91], v[152:155], v[120:123]
	v_mfma_f32_16x16x32_f16 v[108:111], v[72:75], v[160:163], v[108:111]
	v_mfma_f32_16x16x32_f16 v[104:107], v[88:91], v[160:163], v[104:107]
	v_mfma_f32_16x16x32_f16 v[84:87], v[72:75], v[168:171], v[84:87]
	v_mfma_f32_16x16x32_f16 v[76:79], v[88:91], v[168:171], v[76:79]
	v_mfma_f32_16x16x32_f16 v[144:147], v[80:83], v[148:151], v[144:147]
	v_mfma_f32_16x16x32_f16 v[140:143], v[92:95], v[148:151], v[140:143]
	v_mfma_f32_16x16x32_f16 v[124:127], v[80:83], v[156:159], v[124:127]
	v_mfma_f32_16x16x32_f16 v[120:123], v[92:95], v[156:159], v[120:123]
	v_mfma_f32_16x16x32_f16 v[108:111], v[80:83], v[164:167], v[108:111]
	v_mfma_f32_16x16x32_f16 v[104:107], v[92:95], v[164:167], v[104:107]
	v_mfma_f32_16x16x32_f16 v[84:87], v[80:83], v[172:175], v[84:87]
	v_mfma_f32_16x16x32_f16 v[76:79], v[92:95], v[172:175], v[76:79]
	s_barrier
	s_add_i32 s42, 0, 0x1c000
	s_add_i32 s43, s88, s50
	v_add_u32_e32 v202, s42, v228
	s_mov_b32 m0, s43
	ds_read_b128 v[190:193], v202
	ds_read_b128 v[194:197], v202 offset:1024
	ds_read_b128 v[198:201], v202 offset:2048
	ds_read_b128 v[202:205], v202 offset:3072
	global_load_lds_dwordx4 v178, s[92:93]
	s_add_i32 m0, s43, 0x2000
	s_nop 0
	global_load_lds_dwordx4 v182, s[92:93]
	s_barrier
	s_waitcnt lgkmcnt(0)
	v_mfma_f32_16x16x32_f16 v[132:135], v[190:193], v[136:139], v[132:135]
	v_mfma_f32_16x16x32_f16 v[128:131], v[198:201], v[136:139], v[128:131]
	v_mfma_f32_16x16x32_f16 v[116:119], v[190:193], v[152:155], v[116:119]
	v_mfma_f32_16x16x32_f16 v[112:115], v[198:201], v[152:155], v[112:115]
	v_mfma_f32_16x16x32_f16 v[100:103], v[190:193], v[160:163], v[100:103]
	v_mfma_f32_16x16x32_f16 v[96:99], v[198:201], v[160:163], v[96:99]
	v_mfma_f32_16x16x32_f16 v[68:71], v[190:193], v[168:171], v[68:71]
	v_mfma_f32_16x16x32_f16 v[64:67], v[198:201], v[168:171], v[64:67]
	v_mfma_f32_16x16x32_f16 v[132:135], v[194:197], v[148:151], v[132:135]
	v_mfma_f32_16x16x32_f16 v[128:131], v[202:205], v[148:151], v[128:131]
	v_mfma_f32_16x16x32_f16 v[116:119], v[194:197], v[156:159], v[116:119]
	v_mfma_f32_16x16x32_f16 v[112:115], v[202:205], v[156:159], v[112:115]
	v_mfma_f32_16x16x32_f16 v[100:103], v[194:197], v[164:167], v[100:103]
	v_mfma_f32_16x16x32_f16 v[96:99], v[202:205], v[164:167], v[96:99]
	v_mfma_f32_16x16x32_f16 v[68:71], v[194:197], v[172:175], v[68:71]
	v_mfma_f32_16x16x32_f16 v[64:67], v[202:205], v[172:175], v[64:67]
	s_barrier
	s_mov_b32 m0, s58
	ds_read_b128 v[136:139], v232 offset:49152
	ds_read_b128 v[148:151], v232 offset:50176
	ds_read_b128 v[152:155], v232 offset:51200
	ds_read_b128 v[156:159], v232 offset:52224
	ds_read_b128 v[160:163], v232 offset:53248
	ds_read_b128 v[164:167], v232 offset:54272
	ds_read_b128 v[168:171], v232 offset:55296
	ds_read_b128 v[172:175], v232 offset:56320
	global_load_lds_dwordx4 v176, s[94:95]
	s_mov_b32 m0, s59
	s_nop 0
	global_load_lds_dwordx4 v180, s[94:95]
	s_barrier
	s_waitcnt lgkmcnt(0)
	v_mfma_f32_16x16x32_f16 v[60:63], v[72:75], v[136:139], v[60:63]
	v_mfma_f32_16x16x32_f16 v[56:59], v[88:91], v[136:139], v[56:59]
	v_mfma_f32_16x16x32_f16 v[44:47], v[72:75], v[152:155], v[44:47]
	v_mfma_f32_16x16x32_f16 v[40:43], v[88:91], v[152:155], v[40:43]
	v_mfma_f32_16x16x32_f16 v[28:31], v[72:75], v[160:163], v[28:31]
	v_mfma_f32_16x16x32_f16 v[24:27], v[88:91], v[160:163], v[24:27]
	v_mfma_f32_16x16x32_f16 v[12:15], v[72:75], v[168:171], v[12:15]
	v_mfma_f32_16x16x32_f16 v[8:11], v[88:91], v[168:171], v[8:11]
	v_mfma_f32_16x16x32_f16 v[60:63], v[80:83], v[148:151], v[60:63]
	v_mfma_f32_16x16x32_f16 v[56:59], v[92:95], v[148:151], v[56:59]
	v_mfma_f32_16x16x32_f16 v[44:47], v[80:83], v[156:159], v[44:47]
	v_mfma_f32_16x16x32_f16 v[40:43], v[92:95], v[156:159], v[40:43]
	v_mfma_f32_16x16x32_f16 v[28:31], v[80:83], v[164:167], v[28:31]
	v_mfma_f32_16x16x32_f16 v[24:27], v[92:95], v[164:167], v[24:27]
	v_mfma_f32_16x16x32_f16 v[12:15], v[80:83], v[172:175], v[12:15]
	v_mfma_f32_16x16x32_f16 v[8:11], v[92:95], v[172:175], v[8:11]
	s_barrier
	s_add_u32 s40, s40, 0x30080
	s_addc_u32 s41, s41, 0
	s_add_i32 s42, s42, s50
	s_mov_b32 m0, s42
	s_nop 0
	global_load_lds_dwordx4 v178, s[40:41]
	s_add_i32 m0, s42, 0x2000
	s_nop 0
	global_load_lds_dwordx4 v182, s[40:41]
	s_waitcnt vmcnt(6)
	s_barrier
	v_mfma_f32_16x16x32_f16 v[52:55], v[190:193], v[136:139], v[52:55]
	v_mfma_f32_16x16x32_f16 v[48:51], v[198:201], v[136:139], v[48:51]
	v_mfma_f32_16x16x32_f16 v[36:39], v[190:193], v[152:155], v[36:39]
	v_mfma_f32_16x16x32_f16 v[32:35], v[198:201], v[152:155], v[32:35]
	v_mfma_f32_16x16x32_f16 v[20:23], v[190:193], v[160:163], v[20:23]
	v_mfma_f32_16x16x32_f16 v[16:19], v[198:201], v[160:163], v[16:19]
	v_mfma_f32_16x16x32_f16 v[4:7], v[190:193], v[168:171], v[4:7]
	v_mfma_f32_16x16x32_f16 v[0:3], v[198:201], v[168:171], v[0:3]
	v_mfma_f32_16x16x32_f16 v[52:55], v[194:197], v[148:151], v[52:55]
	v_mfma_f32_16x16x32_f16 v[48:51], v[202:205], v[148:151], v[48:51]
	v_mfma_f32_16x16x32_f16 v[36:39], v[194:197], v[156:159], v[36:39]
	v_mfma_f32_16x16x32_f16 v[32:35], v[202:205], v[156:159], v[32:35]
	v_mfma_f32_16x16x32_f16 v[20:23], v[194:197], v[164:167], v[20:23]
	v_mfma_f32_16x16x32_f16 v[16:19], v[202:205], v[164:167], v[16:19]
	v_mfma_f32_16x16x32_f16 v[4:7], v[194:197], v[172:175], v[4:7]
	v_mfma_f32_16x16x32_f16 v[0:3], v[202:205], v[172:175], v[0:3]
	s_barrier
	s_add_i32 s87, s87, 2
	s_add_u32 s38, s38, 0x100
	s_addc_u32 s39, s39, 0
	s_add_u32 s85, s85, 0x100
	s_addc_u32 s86, s86, 0
	s_cmp_gt_u32 s87, 45
	s_cbranch_scc0 .LBB10_27
	s_lshl_b32 s92, s84, 8
	s_add_i32 s92, s92, s57
	s_lshl_b32 s93, s83, 8
	s_or_b32 s93, s93, s60
	v_lshlrev_b32_e32 v237, 2, v226
	s_lshl_b32 s96, s93, 2
	s_add_u32 s94, s16, s96
	s_addc_u32 s95, s17, 0
	global_load_dwordx4 v[72:75], v237, s[94:95] offset:0
	global_load_dwordx4 v[80:83], v237, s[94:95] offset:16
	global_load_dwordx4 v[88:91], v237, s[94:95] offset:128
	global_load_dwordx4 v[92:95], v237, s[94:95] offset:144
	s_add_u32 s94, s18, s96
	s_addc_u32 s95, s19, 0
	global_load_dwordx4 v[136:139], v237, s[94:95] offset:0
	global_load_dwordx4 v[148:151], v237, s[94:95] offset:16
	global_load_dwordx4 v[152:155], v237, s[94:95] offset:128
	global_load_dwordx4 v[156:159], v237, s[94:95] offset:144
	s_add_u32 s94, s14, s96
	s_addc_u32 s95, s15, 0
	global_load_dwordx4 v[160:163], v237, s[94:95] offset:0
	global_load_dwordx4 v[164:167], v237, s[94:95] offset:16
	global_load_dwordx4 v[168:171], v237, s[94:95] offset:128
	global_load_dwordx4 v[172:175], v237, s[94:95] offset:144
	v_lshlrev_b32_e32 v190, 3, v227
	s_lshl_b32 s96, s92, 3
	s_add_u32 s94, s12, s96
	s_addc_u32 s95, s13, 0
	global_load_dwordx2 v[238:239], v190, s[94:95] offset:0
	global_load_dwordx2 v[192:193], v190, s[94:95] offset:128
	global_load_dwordx2 v[194:195], v190, s[94:95] offset:256
	global_load_dwordx2 v[196:197], v190, s[94:95] offset:384
	global_load_dwordx2 v[198:199], v190, s[94:95] offset:1024
	global_load_dwordx2 v[200:201], v190, s[94:95] offset:1152
	global_load_dwordx2 v[202:203], v190, s[94:95] offset:1280
	global_load_dwordx2 v[204:205], v190, s[94:95] offset:1408
	v_mul_u32_u24_e32 v191, 0x600, v227
	v_lshl_add_u32 v191, v226, 1, v191
	s_mul_i32 s96, s92, 0x600
	s_lshl_b32 s97, s93, 1
	s_add_u32 s96, s96, s97
	s_add_u32 s98, s10, s96
	s_addc_u32 s99, s11, 0
	s_add_u32 s94, s98, 0x0
	s_addc_u32 s95, s99, 0
	global_load_dwordx4 v[208:211], v191, s[94:95] offset:0 nt
	global_load_dwordx4 v[212:215], v191, s[94:95] offset:64 nt
	s_add_u32 s94, s98, 0x6000
	s_addc_u32 s95, s99, 0
	global_load_dwordx4 v[216:219], v191, s[94:95] offset:0 nt
	global_load_dwordx4 v[220:223], v191, s[94:95] offset:64 nt
	v_add_u32_e32 v224, s92, v229
	v_mul_u32_u24_e32 v224, 0x600, v224
	s_lshl_b32 s97, s93, 1
	v_add3_u32 v224, v224, v230, s97
	s_lshl_b32 s96, s83, 2
	s_lshr_b32 s97, s60, 6
	s_add_u32 s96, s96, s97
	s_lshl_b32 s96, s96, 19
	s_lshl_b32 s97, s92, 3
	s_add_u32 s96, s96, s97
	s_add_u32 s100, s28, s96
	s_addc_u32 s101, s29, 0
	s_waitcnt vmcnt(19)
	v_pk_add_f32 v[72:73], v[72:73], v[136:137]
	v_pk_add_f32 v[74:75], v[74:75], v[138:139]
	s_waitcnt vmcnt(18)
	v_pk_add_f32 v[80:81], v[80:81], v[148:149]
	v_pk_add_f32 v[82:83], v[82:83], v[150:151]
	s_waitcnt vmcnt(17)
	v_pk_add_f32 v[88:89], v[88:89], v[152:153]
	v_pk_add_f32 v[90:91], v[90:91], v[154:155]
	s_waitcnt vmcnt(16)
	v_pk_add_f32 v[92:93], v[92:93], v[156:157]
	v_pk_add_f32 v[94:95], v[94:95], v[158:159]
	v_pk_add_f32 v[144:145], v[144:145], v[72:73]
	v_pk_add_f32 v[146:147], v[146:147], v[74:75]
	v_pk_add_f32 v[124:125], v[124:125], v[72:73]
	v_pk_add_f32 v[126:127], v[126:127], v[74:75]
	v_pk_add_f32 v[108:109], v[108:109], v[72:73]
	v_pk_add_f32 v[110:111], v[110:111], v[74:75]
	v_pk_add_f32 v[84:85], v[84:85], v[72:73]
	v_pk_add_f32 v[86:87], v[86:87], v[74:75]
	v_pk_add_f32 v[60:61], v[60:61], v[72:73]
	v_pk_add_f32 v[62:63], v[62:63], v[74:75]
	v_pk_add_f32 v[44:45], v[44:45], v[72:73]
	v_pk_add_f32 v[46:47], v[46:47], v[74:75]
	v_pk_add_f32 v[28:29], v[28:29], v[72:73]
	v_pk_add_f32 v[30:31], v[30:31], v[74:75]
	v_pk_add_f32 v[12:13], v[12:13], v[72:73]
	v_pk_add_f32 v[14:15], v[14:15], v[74:75]
	v_pk_add_f32 v[140:141], v[140:141], v[80:81]
	v_pk_add_f32 v[142:143], v[142:143], v[82:83]
	v_pk_add_f32 v[120:121], v[120:121], v[80:81]
	v_pk_add_f32 v[122:123], v[122:123], v[82:83]
	v_pk_add_f32 v[104:105], v[104:105], v[80:81]
	v_pk_add_f32 v[106:107], v[106:107], v[82:83]
	v_pk_add_f32 v[76:77], v[76:77], v[80:81]
	v_pk_add_f32 v[78:79], v[78:79], v[82:83]
	v_pk_add_f32 v[56:57], v[56:57], v[80:81]
	v_pk_add_f32 v[58:59], v[58:59], v[82:83]
	v_pk_add_f32 v[40:41], v[40:41], v[80:81]
	v_pk_add_f32 v[42:43], v[42:43], v[82:83]
	v_pk_add_f32 v[24:25], v[24:25], v[80:81]
	v_pk_add_f32 v[26:27], v[26:27], v[82:83]
	v_pk_add_f32 v[8:9], v[8:9], v[80:81]
	v_pk_add_f32 v[10:11], v[10:11], v[82:83]
	v_pk_add_f32 v[132:133], v[132:133], v[88:89]
	v_pk_add_f32 v[134:135], v[134:135], v[90:91]
	v_pk_add_f32 v[116:117], v[116:117], v[88:89]
	v_pk_add_f32 v[118:119], v[118:119], v[90:91]
	v_pk_add_f32 v[100:101], v[100:101], v[88:89]
	v_pk_add_f32 v[102:103], v[102:103], v[90:91]
	v_pk_add_f32 v[68:69], v[68:69], v[88:89]
	v_pk_add_f32 v[70:71], v[70:71], v[90:91]
	v_pk_add_f32 v[52:53], v[52:53], v[88:89]
	v_pk_add_f32 v[54:55], v[54:55], v[90:91]
	v_pk_add_f32 v[36:37], v[36:37], v[88:89]
	v_pk_add_f32 v[38:39], v[38:39], v[90:91]
	v_pk_add_f32 v[20:21], v[20:21], v[88:89]
	v_pk_add_f32 v[22:23], v[22:23], v[90:91]
	v_pk_add_f32 v[4:5], v[4:5], v[88:89]
	v_pk_add_f32 v[6:7], v[6:7], v[90:91]
	v_pk_add_f32 v[128:129], v[128:129], v[92:93]
	v_pk_add_f32 v[130:131], v[130:131], v[94:95]
	v_pk_add_f32 v[112:113], v[112:113], v[92:93]
	v_pk_add_f32 v[114:115], v[114:115], v[94:95]
	v_pk_add_f32 v[96:97], v[96:97], v[92:93]
	v_pk_add_f32 v[98:99], v[98:99], v[94:95]
	v_pk_add_f32 v[64:65], v[64:65], v[92:93]
	v_pk_add_f32 v[66:67], v[66:67], v[94:95]
	v_pk_add_f32 v[48:49], v[48:49], v[92:93]
	v_pk_add_f32 v[50:51], v[50:51], v[94:95]
	v_pk_add_f32 v[32:33], v[32:33], v[92:93]
	v_pk_add_f32 v[34:35], v[34:35], v[94:95]
	v_pk_add_f32 v[16:17], v[16:17], v[92:93]
	v_pk_add_f32 v[18:19], v[18:19], v[94:95]
	v_pk_add_f32 v[0:1], v[0:1], v[92:93]
	v_pk_add_f32 v[2:3], v[2:3], v[94:95]
	s_add_u32 s94, s98, 0xc000
	s_addc_u32 s95, s99, 0
	global_load_dwordx4 v[240:243], v191, s[94:95] offset:0 nt
	global_load_dwordx4 v[244:247], v191, s[94:95] offset:64 nt
	s_add_u32 s94, s98, 0x12000
	s_addc_u32 s95, s99, 0
	global_load_dwordx4 v[248:251], v191, s[94:95] offset:0 nt
	global_load_dwordx4 v[252:255], v191, s[94:95] offset:64 nt
	s_add_u32 s94, s98, 0x30000
	s_addc_u32 s95, s99, 0
	global_load_dwordx4 v[136:139], v191, s[94:95] offset:0 nt
	global_load_dwordx4 v[148:151], v191, s[94:95] offset:64 nt
	s_add_u32 s94, s98, 0x36000
	s_addc_u32 s95, s99, 0
	global_load_dwordx4 v[152:155], v191, s[94:95] offset:0 nt
	global_load_dwordx4 v[156:159], v191, s[94:95] offset:64 nt
	s_waitcnt vmcnt(19)
	s_waitcnt vmcnt(11)
	v_cvt_f32_f16_e32 v72, v208
	v_cvt_f32_f16_sdwa v73, v208 dst_sel:DWORD dst_unused:UNUSED_PAD src0_sel:WORD_1
	v_cvt_f32_f16_e32 v74, v209
	v_cvt_f32_f16_sdwa v75, v209 dst_sel:DWORD dst_unused:UNUSED_PAD src0_sel:WORD_1
	v_cvt_f32_f16_e32 v80, v210
	v_cvt_f32_f16_sdwa v81, v210 dst_sel:DWORD dst_unused:UNUSED_PAD src0_sel:WORD_1
	v_cvt_f32_f16_e32 v82, v211
	v_cvt_f32_f16_sdwa v83, v211 dst_sel:DWORD dst_unused:UNUSED_PAD src0_sel:WORD_1
	v_sub_f32_e32 v72, v72, v238
	v_sub_f32_e32 v73, v73, v238
	v_sub_f32_e32 v74, v74, v238
	v_sub_f32_e32 v75, v75, v238
	v_sub_f32_e32 v80, v80, v238
	v_sub_f32_e32 v81, v81, v238
	v_sub_f32_e32 v82, v82, v238
	v_sub_f32_e32 v83, v83, v238
	v_pk_mul_f32 v[72:73], v[238:239], v[72:73] op_sel:[1,0]
	v_pk_mul_f32 v[74:75], v[238:239], v[74:75] op_sel:[1,0]
	v_pk_mul_f32 v[80:81], v[238:239], v[80:81] op_sel:[1,0]
	v_pk_mul_f32 v[82:83], v[238:239], v[82:83] op_sel:[1,0]
	v_pk_fma_f32 v[144:145], v[72:73], v[160:161], v[144:145]
	v_pk_fma_f32 v[146:147], v[74:75], v[162:163], v[146:147]
	v_pk_fma_f32 v[140:141], v[80:81], v[164:165], v[140:141]
	v_pk_fma_f32 v[142:143], v[82:83], v[166:167], v[142:143]
	v_cvt_pk_f16_f32 v144, v144, v145
	v_cvt_pk_f16_f32 v145, v146, v147
	v_cvt_pk_f16_f32 v146, v140, v141
	v_cvt_pk_f16_f32 v147, v142, v143
	ds_write_b128 v235, v[144:147]
	v_fma_mix_f32 v206, v144, 1.0, 0 op_sel_hi:[1,0,0]
	v_fma_mix_f32 v207, v144, v144, 0 op_sel_hi:[1,1,0]
	v_fma_mix_f32 v206, v144, 1.0, v206 op_sel:[1,0,0] op_sel_hi:[1,0,0]
	v_fma_mix_f32 v207, v144, v144, v207 op_sel:[1,1,0] op_sel_hi:[1,1,0]
	v_fma_mix_f32 v206, v145, 1.0, v206 op_sel_hi:[1,0,0]
	v_fma_mix_f32 v207, v145, v145, v207 op_sel_hi:[1,1,0]
	v_fma_mix_f32 v206, v145, 1.0, v206 op_sel:[1,0,0] op_sel_hi:[1,0,0]
	v_fma_mix_f32 v207, v145, v145, v207 op_sel:[1,1,0] op_sel_hi:[1,1,0]
	v_fma_mix_f32 v206, v146, 1.0, v206 op_sel_hi:[1,0,0]
	v_fma_mix_f32 v207, v146, v146, v207 op_sel_hi:[1,1,0]
	v_fma_mix_f32 v206, v146, 1.0, v206 op_sel:[1,0,0] op_sel_hi:[1,0,0]
	v_fma_mix_f32 v207, v146, v146, v207 op_sel:[1,1,0] op_sel_hi:[1,1,0]
	v_fma_mix_f32 v206, v147, 1.0, v206 op_sel_hi:[1,0,0]
	v_fma_mix_f32 v207, v147, v147, v207 op_sel_hi:[1,1,0]
	v_fma_mix_f32 v206, v147, 1.0, v206 op_sel:[1,0,0] op_sel_hi:[1,0,0]
	v_fma_mix_f32 v207, v147, v147, v207 op_sel:[1,1,0] op_sel_hi:[1,1,0]
	s_waitcnt vmcnt(10)
	v_cvt_f32_f16_e32 v72, v212
	v_cvt_f32_f16_sdwa v73, v212 dst_sel:DWORD dst_unused:UNUSED_PAD src0_sel:WORD_1
	v_cvt_f32_f16_e32 v74, v213
	v_cvt_f32_f16_sdwa v75, v213 dst_sel:DWORD dst_unused:UNUSED_PAD src0_sel:WORD_1
	v_cvt_f32_f16_e32 v80, v214
	v_cvt_f32_f16_sdwa v81, v214 dst_sel:DWORD dst_unused:UNUSED_PAD src0_sel:WORD_1
	v_cvt_f32_f16_e32 v82, v215
	v_cvt_f32_f16_sdwa v83, v215 dst_sel:DWORD dst_unused:UNUSED_PAD src0_sel:WORD_1
	v_sub_f32_e32 v72, v72, v238
	v_sub_f32_e32 v73, v73, v238
	v_sub_f32_e32 v74, v74, v238
	v_sub_f32_e32 v75, v75, v238
	v_sub_f32_e32 v80, v80, v238
	v_sub_f32_e32 v81, v81, v238
	v_sub_f32_e32 v82, v82, v238
	v_sub_f32_e32 v83, v83, v238
	v_pk_mul_f32 v[72:73], v[238:239], v[72:73] op_sel:[1,0]
	v_pk_mul_f32 v[74:75], v[238:239], v[74:75] op_sel:[1,0]
	v_pk_mul_f32 v[80:81], v[238:239], v[80:81] op_sel:[1,0]
	v_pk_mul_f32 v[82:83], v[238:239], v[82:83] op_sel:[1,0]
	v_pk_fma_f32 v[132:133], v[72:73], v[168:169], v[132:133]
	v_pk_fma_f32 v[134:135], v[74:75], v[170:171], v[134:135]
	v_pk_fma_f32 v[128:129], v[80:81], v[172:173], v[128:129]
	v_pk_fma_f32 v[130:131], v[82:83], v[174:175], v[130:131]
	v_cvt_pk_f16_f32 v132, v132, v133
	v_cvt_pk_f16_f32 v133, v134, v135
	v_cvt_pk_f16_f32 v134, v128, v129
	v_cvt_pk_f16_f32 v135, v130, v131
	ds_write_b128 v235, v[132:135] offset:64
	v_fma_mix_f32 v206, v132, 1.0, v206 op_sel_hi:[1,0,0]
	v_fma_mix_f32 v207, v132, v132, v207 op_sel_hi:[1,1,0]
	v_fma_mix_f32 v206, v132, 1.0, v206 op_sel:[1,0,0] op_sel_hi:[1,0,0]
	v_fma_mix_f32 v207, v132, v132, v207 op_sel:[1,1,0] op_sel_hi:[1,1,0]
	v_fma_mix_f32 v206, v133, 1.0, v206 op_sel_hi:[1,0,0]
	v_fma_mix_f32 v207, v133, v133, v207 op_sel_hi:[1,1,0]
	v_fma_mix_f32 v206, v133, 1.0, v206 op_sel:[1,0,0] op_sel_hi:[1,0,0]
	v_fma_mix_f32 v207, v133, v133, v207 op_sel:[1,1,0] op_sel_hi:[1,1,0]
	v_fma_mix_f32 v206, v134, 1.0, v206 op_sel_hi:[1,0,0]
	v_fma_mix_f32 v207, v134, v134, v207 op_sel_hi:[1,1,0]
	v_fma_mix_f32 v206, v134, 1.0, v206 op_sel:[1,0,0] op_sel_hi:[1,0,0]
	v_fma_mix_f32 v207, v134, v134, v207 op_sel:[1,1,0] op_sel_hi:[1,1,0]
	v_fma_mix_f32 v206, v135, 1.0, v206 op_sel_hi:[1,0,0]
	v_fma_mix_f32 v207, v135, v135, v207 op_sel_hi:[1,1,0]
	v_fma_mix_f32 v206, v135, 1.0, v206 op_sel:[1,0,0] op_sel_hi:[1,0,0]
	v_fma_mix_f32 v207, v135, v135, v207 op_sel:[1,1,0] op_sel_hi:[1,1,0]
	ds_read_b128 v[88:91], v236
	ds_read_b128 v[92:95], v236 offset:1152
	s_waitcnt vmcnt(9)
	v_cvt_f32_f16_e32 v72, v216
	v_cvt_f32_f16_sdwa v73, v216 dst_sel:DWORD dst_unused:UNUSED_PAD src0_sel:WORD_1
	v_cvt_f32_f16_e32 v74, v217
	v_cvt_f32_f16_sdwa v75, v217 dst_sel:DWORD dst_unused:UNUSED_PAD src0_sel:WORD_1
	v_cvt_f32_f16_e32 v80, v218
	v_cvt_f32_f16_sdwa v81, v218 dst_sel:DWORD dst_unused:UNUSED_PAD src0_sel:WORD_1
	v_cvt_f32_f16_e32 v82, v219
	v_cvt_f32_f16_sdwa v83, v219 dst_sel:DWORD dst_unused:UNUSED_PAD src0_sel:WORD_1
	v_sub_f32_e32 v72, v72, v192
	v_sub_f32_e32 v73, v73, v192
	v_sub_f32_e32 v74, v74, v192
	v_sub_f32_e32 v75, v75, v192
	v_sub_f32_e32 v80, v80, v192
	v_sub_f32_e32 v81, v81, v192
	v_sub_f32_e32 v82, v82, v192
	v_sub_f32_e32 v83, v83, v192
	v_pk_mul_f32 v[72:73], v[192:193], v[72:73] op_sel:[1,0]
	v_pk_mul_f32 v[74:75], v[192:193], v[74:75] op_sel:[1,0]
	v_pk_mul_f32 v[80:81], v[192:193], v[80:81] op_sel:[1,0]
	v_pk_mul_f32 v[82:83], v[192:193], v[82:83] op_sel:[1,0]
	v_pk_fma_f32 v[124:125], v[72:73], v[160:161], v[124:125]
	v_pk_fma_f32 v[126:127], v[74:75], v[162:163], v[126:127]
	v_pk_fma_f32 v[120:121], v[80:81], v[164:165], v[120:121]
	v_pk_fma_f32 v[122:123], v[82:83], v[166:167], v[122:123]
	v_cvt_pk_f16_f32 v124, v124, v125
	v_cvt_pk_f16_f32 v125, v126, v127
	v_cvt_pk_f16_f32 v126, v120, v121
	v_cvt_pk_f16_f32 v127, v122, v123
	s_waitcnt lgkmcnt(0)
	buffer_store_dwordx4 v[88:91], v224, s[24:27], 0 offen nt
	v_add_u32_e32 v82, 0x3000, v224
	buffer_store_dwordx4 v[92:95], v82, s[24:27], 0 offen nt
	ds_write_b128 v235, v[124:127]
	v_fma_mix_f32 v140, v124, 1.0, 0 op_sel_hi:[1,0,0]
	v_fma_mix_f32 v141, v124, v124, 0 op_sel_hi:[1,1,0]
	v_fma_mix_f32 v140, v124, 1.0, v140 op_sel:[1,0,0] op_sel_hi:[1,0,0]
	v_fma_mix_f32 v141, v124, v124, v141 op_sel:[1,1,0] op_sel_hi:[1,1,0]
	v_fma_mix_f32 v140, v125, 1.0, v140 op_sel_hi:[1,0,0]
	v_fma_mix_f32 v141, v125, v125, v141 op_sel_hi:[1,1,0]
	v_fma_mix_f32 v140, v125, 1.0, v140 op_sel:[1,0,0] op_sel_hi:[1,0,0]
	v_fma_mix_f32 v141, v125, v125, v141 op_sel:[1,1,0] op_sel_hi:[1,1,0]
	v_fma_mix_f32 v140, v126, 1.0, v140 op_sel_hi:[1,0,0]
	v_fma_mix_f32 v141, v126, v126, v141 op_sel_hi:[1,1,0]
	v_fma_mix_f32 v140, v126, 1.0, v140 op_sel:[1,0,0] op_sel_hi:[1,0,0]
	v_fma_mix_f32 v141, v126, v126, v141 op_sel:[1,1,0] op_sel_hi:[1,1,0]
	v_fma_mix_f32 v140, v127, 1.0, v140 op_sel_hi:[1,0,0]
	v_fma_mix_f32 v141, v127, v127, v141 op_sel_hi:[1,1,0]
	v_fma_mix_f32 v140, v127, 1.0, v140 op_sel:[1,0,0] op_sel_hi:[1,0,0]
	v_fma_mix_f32 v141, v127, v127, v141 op_sel:[1,1,0] op_sel_hi:[1,1,0]
	s_waitcnt vmcnt(10)
	v_cvt_f32_f16_e32 v72, v220
	v_cvt_f32_f16_sdwa v73, v220 dst_sel:DWORD dst_unused:UNUSED_PAD src0_sel:WORD_1
	v_cvt_f32_f16_e32 v74, v221
	v_cvt_f32_f16_sdwa v75, v221 dst_sel:DWORD dst_unused:UNUSED_PAD src0_sel:WORD_1
	v_cvt_f32_f16_e32 v80, v222
	v_cvt_f32_f16_sdwa v81, v222 dst_sel:DWORD dst_unused:UNUSED_PAD src0_sel:WORD_1
	v_cvt_f32_f16_e32 v82, v223
	v_cvt_f32_f16_sdwa v83, v223 dst_sel:DWORD dst_unused:UNUSED_PAD src0_sel:WORD_1
	v_sub_f32_e32 v72, v72, v192
	v_sub_f32_e32 v73, v73, v192
	v_sub_f32_e32 v74, v74, v192
	v_sub_f32_e32 v75, v75, v192
	v_sub_f32_e32 v80, v80, v192
	v_sub_f32_e32 v81, v81, v192
	v_sub_f32_e32 v82, v82, v192
	v_sub_f32_e32 v83, v83, v192
	v_pk_mul_f32 v[72:73], v[192:193], v[72:73] op_sel:[1,0]
	v_pk_mul_f32 v[74:75], v[192:193], v[74:75] op_sel:[1,0]
	v_pk_mul_f32 v[80:81], v[192:193], v[80:81] op_sel:[1,0]
	v_pk_mul_f32 v[82:83], v[192:193], v[82:83] op_sel:[1,0]
	v_pk_fma_f32 v[116:117], v[72:73], v[168:169], v[116:117]
	v_pk_fma_f32 v[118:119], v[74:75], v[170:171], v[118:119]
	v_pk_fma_f32 v[112:113], v[80:81], v[172:173], v[112:113]
	v_pk_fma_f32 v[114:115], v[82:83], v[174:175], v[114:115]
	v_cvt_pk_f16_f32 v116, v116, v117
	v_cvt_pk_f16_f32 v117, v118, v119
	v_cvt_pk_f16_f32 v118, v112, v113
	v_cvt_pk_f16_f32 v119, v114, v115
	ds_write_b128 v235, v[116:119] offset:64
	v_fma_mix_f32 v140, v116, 1.0, v140 op_sel_hi:[1,0,0]
	v_fma_mix_f32 v141, v116, v116, v141 op_sel_hi:[1,1,0]
	v_fma_mix_f32 v140, v116, 1.0, v140 op_sel:[1,0,0] op_sel_hi:[1,0,0]
	v_fma_mix_f32 v141, v116, v116, v141 op_sel:[1,1,0] op_sel_hi:[1,1,0]
	v_fma_mix_f32 v140, v117, 1.0, v140 op_sel_hi:[1,0,0]
	v_fma_mix_f32 v141, v117, v117, v141 op_sel_hi:[1,1,0]
	v_fma_mix_f32 v140, v117, 1.0, v140 op_sel:[1,0,0] op_sel_hi:[1,0,0]
	v_fma_mix_f32 v141, v117, v117, v141 op_sel:[1,1,0] op_sel_hi:[1,1,0]
	v_fma_mix_f32 v140, v118, 1.0, v140 op_sel_hi:[1,0,0]
	v_fma_mix_f32 v141, v118, v118, v141 op_sel_hi:[1,1,0]
	v_fma_mix_f32 v140, v118, 1.0, v140 op_sel:[1,0,0] op_sel_hi:[1,0,0]
	v_fma_mix_f32 v141, v118, v118, v141 op_sel:[1,1,0] op_sel_hi:[1,1,0]
	v_fma_mix_f32 v140, v119, 1.0, v140 op_sel_hi:[1,0,0]
	v_fma_mix_f32 v141, v119, v119, v141 op_sel_hi:[1,1,0]
	v_fma_mix_f32 v140, v119, 1.0, v140 op_sel:[1,0,0] op_sel_hi:[1,0,0]
	v_fma_mix_f32 v141, v119, v119, v141 op_sel:[1,1,0] op_sel_hi:[1,1,0]
	ds_read_b128 v[208:211], v236
	ds_read_b128 v[128:131], v236 offset:1152
	s_add_u32 s94, s98, 0x3c000
	s_addc_u32 s95, s99, 0
	global_load_dwordx4 v[212:215], v191, s[94:95] offset:0 nt
	global_load_dwordx4 v[144:147], v191, s[94:95] offset:64 nt
	s_add_u32 s94, s98, 0x42000
	s_addc_u32 s95, s99, 0
	global_load_dwordx4 v[132:135], v191, s[94:95] offset:0 nt
	global_load_dwordx4 v[88:91], v191, s[94:95] offset:64 nt
	s_waitcnt vmcnt(13)
	v_cvt_f32_f16_e32 v72, v240
	v_cvt_f32_f16_sdwa v73, v240 dst_sel:DWORD dst_unused:UNUSED_PAD src0_sel:WORD_1
	v_cvt_f32_f16_e32 v74, v241
	v_cvt_f32_f16_sdwa v75, v241 dst_sel:DWORD dst_unused:UNUSED_PAD src0_sel:WORD_1
	v_cvt_f32_f16_e32 v80, v242
	v_cvt_f32_f16_sdwa v81, v242 dst_sel:DWORD dst_unused:UNUSED_PAD src0_sel:WORD_1
	v_cvt_f32_f16_e32 v82, v243
	v_cvt_f32_f16_sdwa v83, v243 dst_sel:DWORD dst_unused:UNUSED_PAD src0_sel:WORD_1
	v_sub_f32_e32 v72, v72, v194
	v_sub_f32_e32 v73, v73, v194
	v_sub_f32_e32 v74, v74, v194
	v_sub_f32_e32 v75, v75, v194
	v_sub_f32_e32 v80, v80, v194
	v_sub_f32_e32 v81, v81, v194
	v_sub_f32_e32 v82, v82, v194
	v_sub_f32_e32 v83, v83, v194
	v_pk_mul_f32 v[72:73], v[194:195], v[72:73] op_sel:[1,0]
	v_pk_mul_f32 v[74:75], v[194:195], v[74:75] op_sel:[1,0]
	v_pk_mul_f32 v[80:81], v[194:195], v[80:81] op_sel:[1,0]
	v_pk_mul_f32 v[82:83], v[194:195], v[82:83] op_sel:[1,0]
	v_pk_fma_f32 v[108:109], v[72:73], v[160:161], v[108:109]
	v_pk_fma_f32 v[110:111], v[74:75], v[162:163], v[110:111]
	v_pk_fma_f32 v[104:105], v[80:81], v[164:165], v[104:105]
	v_pk_fma_f32 v[106:107], v[82:83], v[166:167], v[106:107]
	v_cvt_pk_f16_f32 v108, v108, v109
	v_cvt_pk_f16_f32 v109, v110, v111
	v_cvt_pk_f16_f32 v110, v104, v105
	v_cvt_pk_f16_f32 v111, v106, v107
	s_waitcnt lgkmcnt(0)
	v_add_u32_e32 v83, 0x6000, v224
	buffer_store_dwordx4 v[208:211], v83, s[24:27], 0 offen nt
	v_add_u32_e32 v82, 0x9000, v224
	buffer_store_dwordx4 v[128:131], v82, s[24:27], 0 offen nt
	ds_write_b128 v235, v[108:111]
	v_fma_mix_f32 v142, v108, 1.0, 0 op_sel_hi:[1,0,0]
	v_fma_mix_f32 v143, v108, v108, 0 op_sel_hi:[1,1,0]
	v_fma_mix_f32 v142, v108, 1.0, v142 op_sel:[1,0,0] op_sel_hi:[1,0,0]
	v_fma_mix_f32 v143, v108, v108, v143 op_sel:[1,1,0] op_sel_hi:[1,1,0]
	v_fma_mix_f32 v142, v109, 1.0, v142 op_sel_hi:[1,0,0]
	v_fma_mix_f32 v143, v109, v109, v143 op_sel_hi:[1,1,0]
	v_fma_mix_f32 v142, v109, 1.0, v142 op_sel:[1,0,0] op_sel_hi:[1,0,0]
	v_fma_mix_f32 v143, v109, v109, v143 op_sel:[1,1,0] op_sel_hi:[1,1,0]
	v_fma_mix_f32 v142, v110, 1.0, v142 op_sel_hi:[1,0,0]
	v_fma_mix_f32 v143, v110, v110, v143 op_sel_hi:[1,1,0]
	v_fma_mix_f32 v142, v110, 1.0, v142 op_sel:[1,0,0] op_sel_hi:[1,0,0]
	v_fma_mix_f32 v143, v110, v110, v143 op_sel:[1,1,0] op_sel_hi:[1,1,0]
	v_fma_mix_f32 v142, v111, 1.0, v142 op_sel_hi:[1,0,0]
	v_fma_mix_f32 v143, v111, v111, v143 op_sel_hi:[1,1,0]
	v_fma_mix_f32 v142, v111, 1.0, v142 op_sel:[1,0,0] op_sel_hi:[1,0,0]
	v_fma_mix_f32 v143, v111, v111, v143 op_sel:[1,1,0] op_sel_hi:[1,1,0]
	s_waitcnt vmcnt(14)
	v_cvt_f32_f16_e32 v72, v244
	v_cvt_f32_f16_sdwa v73, v244 dst_sel:DWORD dst_unused:UNUSED_PAD src0_sel:WORD_1
	v_cvt_f32_f16_e32 v74, v245
	v_cvt_f32_f16_sdwa v75, v245 dst_sel:DWORD dst_unused:UNUSED_PAD src0_sel:WORD_1
	v_cvt_f32_f16_e32 v80, v246
	v_cvt_f32_f16_sdwa v81, v246 dst_sel:DWORD dst_unused:UNUSED_PAD src0_sel:WORD_1
	v_cvt_f32_f16_e32 v82, v247
	v_cvt_f32_f16_sdwa v83, v247 dst_sel:DWORD dst_unused:UNUSED_PAD src0_sel:WORD_1
	v_sub_f32_e32 v72, v72, v194
	v_sub_f32_e32 v73, v73, v194
	v_sub_f32_e32 v74, v74, v194
	v_sub_f32_e32 v75, v75, v194
	v_sub_f32_e32 v80, v80, v194
	v_sub_f32_e32 v81, v81, v194
	v_sub_f32_e32 v82, v82, v194
	v_sub_f32_e32 v83, v83, v194
	v_pk_mul_f32 v[72:73], v[194:195], v[72:73] op_sel:[1,0]
	v_pk_mul_f32 v[74:75], v[194:195], v[74:75] op_sel:[1,0]
	v_pk_mul_f32 v[80:81], v[194:195], v[80:81] op_sel:[1,0]
	v_pk_mul_f32 v[82:83], v[194:195], v[82:83] op_sel:[1,0]
	v_pk_fma_f32 v[100:101], v[72:73], v[168:169], v[100:101]
	v_pk_fma_f32 v[102:103], v[74:75], v[170:171], v[102:103]
	v_pk_fma_f32 v[96:97], v[80:81], v[172:173], v[96:97]
	v_pk_fma_f32 v[98:99], v[82:83], v[174:175], v[98:99]
	v_cvt_pk_f16_f32 v100, v100, v101
	v_cvt_pk_f16_f32 v101, v102, v103
	v_cvt_pk_f16_f32 v102, v96, v97
	v_cvt_pk_f16_f32 v103, v98, v99
	ds_write_b128 v235, v[100:103] offset:64
	v_fma_mix_f32 v142, v100, 1.0, v142 op_sel_hi:[1,0,0]
	v_fma_mix_f32 v143, v100, v100, v143 op_sel_hi:[1,1,0]
	v_fma_mix_f32 v142, v100, 1.0, v142 op_sel:[1,0,0] op_sel_hi:[1,0,0]
	v_fma_mix_f32 v143, v100, v100, v143 op_sel:[1,1,0] op_sel_hi:[1,1,0]
	v_fma_mix_f32 v142, v101, 1.0, v142 op_sel_hi:[1,0,0]
	v_fma_mix_f32 v143, v101, v101, v143 op_sel_hi:[1,1,0]
	v_fma_mix_f32 v142, v101, 1.0, v142 op_sel:[1,0,0] op_sel_hi:[1,0,0]
	v_fma_mix_f32 v143, v101, v101, v143 op_sel:[1,1,0] op_sel_hi:[1,1,0]
	v_fma_mix_f32 v142, v102, 1.0, v142 op_sel_hi:[1,0,0]
	v_fma_mix_f32 v143, v102, v102, v143 op_sel_hi:[1,1,0]
	v_fma_mix_f32 v142, v102, 1.0, v142 op_sel:[1,0,0] op_sel_hi:[1,0,0]
	v_fma_mix_f32 v143, v102, v102, v143 op_sel:[1,1,0] op_sel_hi:[1,1,0]
	v_fma_mix_f32 v142, v103, 1.0, v142 op_sel_hi:[1,0,0]
	v_fma_mix_f32 v143, v103, v103, v143 op_sel_hi:[1,1,0]
	v_fma_mix_f32 v142, v103, 1.0, v142 op_sel:[1,0,0] op_sel_hi:[1,0,0]
	v_fma_mix_f32 v143, v103, v103, v143 op_sel:[1,1,0] op_sel_hi:[1,1,0]
	ds_read_b128 v[92:95], v236
	ds_read_b128 v[120:123], v236 offset:1152
	s_waitcnt vmcnt(13)
	v_cvt_f32_f16_e32 v72, v248
	v_cvt_f32_f16_sdwa v73, v248 dst_sel:DWORD dst_unused:UNUSED_PAD src0_sel:WORD_1
	v_cvt_f32_f16_e32 v74, v249
	v_cvt_f32_f16_sdwa v75, v249 dst_sel:DWORD dst_unused:UNUSED_PAD src0_sel:WORD_1
	v_cvt_f32_f16_e32 v80, v250
	v_cvt_f32_f16_sdwa v81, v250 dst_sel:DWORD dst_unused:UNUSED_PAD src0_sel:WORD_1
	v_cvt_f32_f16_e32 v82, v251
	v_cvt_f32_f16_sdwa v83, v251 dst_sel:DWORD dst_unused:UNUSED_PAD src0_sel:WORD_1
	v_sub_f32_e32 v72, v72, v196
	v_sub_f32_e32 v73, v73, v196
	v_sub_f32_e32 v74, v74, v196
	v_sub_f32_e32 v75, v75, v196
	v_sub_f32_e32 v80, v80, v196
	v_sub_f32_e32 v81, v81, v196
	v_sub_f32_e32 v82, v82, v196
	v_sub_f32_e32 v83, v83, v196
	v_pk_mul_f32 v[72:73], v[196:197], v[72:73] op_sel:[1,0]
	v_pk_mul_f32 v[74:75], v[196:197], v[74:75] op_sel:[1,0]
	v_pk_mul_f32 v[80:81], v[196:197], v[80:81] op_sel:[1,0]
	v_pk_mul_f32 v[82:83], v[196:197], v[82:83] op_sel:[1,0]
	v_pk_fma_f32 v[84:85], v[72:73], v[160:161], v[84:85]
	v_pk_fma_f32 v[86:87], v[74:75], v[162:163], v[86:87]
	v_pk_fma_f32 v[76:77], v[80:81], v[164:165], v[76:77]
	v_pk_fma_f32 v[78:79], v[82:83], v[166:167], v[78:79]
	v_cvt_pk_f16_f32 v84, v84, v85
	v_cvt_pk_f16_f32 v85, v86, v87
	v_cvt_pk_f16_f32 v86, v76, v77
	v_cvt_pk_f16_f32 v87, v78, v79
	s_waitcnt lgkmcnt(0)
	v_add_u32_e32 v83, 0xc000, v224
	buffer_store_dwordx4 v[92:95], v83, s[24:27], 0 offen nt
	v_add_u32_e32 v82, 0xf000, v224
	buffer_store_dwordx4 v[120:123], v82, s[24:27], 0 offen nt
	ds_write_b128 v235, v[84:87]
	v_fma_mix_f32 v216, v84, 1.0, 0 op_sel_hi:[1,0,0]
	v_fma_mix_f32 v217, v84, v84, 0 op_sel_hi:[1,1,0]
	v_fma_mix_f32 v216, v84, 1.0, v216 op_sel:[1,0,0] op_sel_hi:[1,0,0]
	v_fma_mix_f32 v217, v84, v84, v217 op_sel:[1,1,0] op_sel_hi:[1,1,0]
	v_fma_mix_f32 v216, v85, 1.0, v216 op_sel_hi:[1,0,0]
	v_fma_mix_f32 v217, v85, v85, v217 op_sel_hi:[1,1,0]
	v_fma_mix_f32 v216, v85, 1.0, v216 op_sel:[1,0,0] op_sel_hi:[1,0,0]
	v_fma_mix_f32 v217, v85, v85, v217 op_sel:[1,1,0] op_sel_hi:[1,1,0]
	v_fma_mix_f32 v216, v86, 1.0, v216 op_sel_hi:[1,0,0]
	v_fma_mix_f32 v217, v86, v86, v217 op_sel_hi:[1,1,0]
	v_fma_mix_f32 v216, v86, 1.0, v216 op_sel:[1,0,0] op_sel_hi:[1,0,0]
	v_fma_mix_f32 v217, v86, v86, v217 op_sel:[1,1,0] op_sel_hi:[1,1,0]
	v_fma_mix_f32 v216, v87, 1.0, v216 op_sel_hi:[1,0,0]
	v_fma_mix_f32 v217, v87, v87, v217 op_sel_hi:[1,1,0]
	v_fma_mix_f32 v216, v87, 1.0, v216 op_sel:[1,0,0] op_sel_hi:[1,0,0]
	v_fma_mix_f32 v217, v87, v87, v217 op_sel:[1,1,0] op_sel_hi:[1,1,0]
	s_waitcnt vmcnt(14)
	v_cvt_f32_f16_e32 v72, v252
	v_cvt_f32_f16_sdwa v73, v252 dst_sel:DWORD dst_unused:UNUSED_PAD src0_sel:WORD_1
	v_cvt_f32_f16_e32 v74, v253
	v_cvt_f32_f16_sdwa v75, v253 dst_sel:DWORD dst_unused:UNUSED_PAD src0_sel:WORD_1
	v_cvt_f32_f16_e32 v80, v254
	v_cvt_f32_f16_sdwa v81, v254 dst_sel:DWORD dst_unused:UNUSED_PAD src0_sel:WORD_1
	v_cvt_f32_f16_e32 v82, v255
	v_cvt_f32_f16_sdwa v83, v255 dst_sel:DWORD dst_unused:UNUSED_PAD src0_sel:WORD_1
	v_sub_f32_e32 v72, v72, v196
	v_sub_f32_e32 v73, v73, v196
	v_sub_f32_e32 v74, v74, v196
	v_sub_f32_e32 v75, v75, v196
	v_sub_f32_e32 v80, v80, v196
	v_sub_f32_e32 v81, v81, v196
	v_sub_f32_e32 v82, v82, v196
	v_sub_f32_e32 v83, v83, v196
	v_pk_mul_f32 v[72:73], v[196:197], v[72:73] op_sel:[1,0]
	v_pk_mul_f32 v[74:75], v[196:197], v[74:75] op_sel:[1,0]
	v_pk_mul_f32 v[80:81], v[196:197], v[80:81] op_sel:[1,0]
	v_pk_mul_f32 v[82:83], v[196:197], v[82:83] op_sel:[1,0]
	v_pk_fma_f32 v[68:69], v[72:73], v[168:169], v[68:69]
	v_pk_fma_f32 v[70:71], v[74:75], v[170:171], v[70:71]
	v_pk_fma_f32 v[64:65], v[80:81], v[172:173], v[64:65]
	v_pk_fma_f32 v[66:67], v[82:83], v[174:175], v[66:67]
	v_cvt_pk_f16_f32 v68, v68, v69
	v_cvt_pk_f16_f32 v69, v70, v71
	v_cvt_pk_f16_f32 v70, v64, v65
	v_cvt_pk_f16_f32 v71, v66, v67
	ds_write_b128 v235, v[68:71] offset:64
	v_fma_mix_f32 v216, v68, 1.0, v216 op_sel_hi:[1,0,0]
	v_fma_mix_f32 v217, v68, v68, v217 op_sel_hi:[1,1,0]
	v_fma_mix_f32 v216, v68, 1.0, v216 op_sel:[1,0,0] op_sel_hi:[1,0,0]
	v_fma_mix_f32 v217, v68, v68, v217 op_sel:[1,1,0] op_sel_hi:[1,1,0]
	v_fma_mix_f32 v216, v69, 1.0, v216 op_sel_hi:[1,0,0]
	v_fma_mix_f32 v217, v69, v69, v217 op_sel_hi:[1,1,0]
	v_fma_mix_f32 v216, v69, 1.0, v216 op_sel:[1,0,0] op_sel_hi:[1,0,0]
	v_fma_mix_f32 v217, v69, v69, v217 op_sel:[1,1,0] op_sel_hi:[1,1,0]
	v_fma_mix_f32 v216, v70, 1.0, v216 op_sel_hi:[1,0,0]
	v_fma_mix_f32 v217, v70, v70, v217 op_sel_hi:[1,1,0]
	v_fma_mix_f32 v216, v70, 1.0, v216 op_sel:[1,0,0] op_sel_hi:[1,0,0]
	v_fma_mix_f32 v217, v70, v70, v217 op_sel:[1,1,0] op_sel_hi:[1,1,0]
	v_fma_mix_f32 v216, v71, 1.0, v216 op_sel_hi:[1,0,0]
	v_fma_mix_f32 v217, v71, v71, v217 op_sel_hi:[1,1,0]
	v_fma_mix_f32 v216, v71, 1.0, v216 op_sel:[1,0,0] op_sel_hi:[1,0,0]
	v_fma_mix_f32 v217, v71, v71, v217 op_sel:[1,1,0] op_sel_hi:[1,1,0]
	ds_read_b128 v[112:115], v236
	ds_read_b128 v[220:223], v236 offset:1152
	s_waitcnt vmcnt(13)
	v_cvt_f32_f16_e32 v72, v136
	v_cvt_f32_f16_sdwa v73, v136 dst_sel:DWORD dst_unused:UNUSED_PAD src0_sel:WORD_1
	v_cvt_f32_f16_e32 v74, v137
	v_cvt_f32_f16_sdwa v75, v137 dst_sel:DWORD dst_unused:UNUSED_PAD src0_sel:WORD_1
	v_cvt_f32_f16_e32 v80, v138
	v_cvt_f32_f16_sdwa v81, v138 dst_sel:DWORD dst_unused:UNUSED_PAD src0_sel:WORD_1
	v_cvt_f32_f16_e32 v82, v139
	v_cvt_f32_f16_sdwa v83, v139 dst_sel:DWORD dst_unused:UNUSED_PAD src0_sel:WORD_1
	v_sub_f32_e32 v72, v72, v198
	v_sub_f32_e32 v73, v73, v198
	v_sub_f32_e32 v74, v74, v198
	v_sub_f32_e32 v75, v75, v198
	v_sub_f32_e32 v80, v80, v198
	v_sub_f32_e32 v81, v81, v198
	v_sub_f32_e32 v82, v82, v198
	v_sub_f32_e32 v83, v83, v198
	v_pk_mul_f32 v[72:73], v[198:199], v[72:73] op_sel:[1,0]
	v_pk_mul_f32 v[74:75], v[198:199], v[74:75] op_sel:[1,0]
	v_pk_mul_f32 v[80:81], v[198:199], v[80:81] op_sel:[1,0]
	v_pk_mul_f32 v[82:83], v[198:199], v[82:83] op_sel:[1,0]
	v_pk_fma_f32 v[60:61], v[72:73], v[160:161], v[60:61]
	v_pk_fma_f32 v[62:63], v[74:75], v[162:163], v[62:63]
	v_pk_fma_f32 v[56:57], v[80:81], v[164:165], v[56:57]
	v_pk_fma_f32 v[58:59], v[82:83], v[166:167], v[58:59]
	v_cvt_pk_f16_f32 v60, v60, v61
	v_cvt_pk_f16_f32 v61, v62, v63
	v_cvt_pk_f16_f32 v62, v56, v57
	v_cvt_pk_f16_f32 v63, v58, v59
	s_waitcnt lgkmcnt(0)
	v_add_u32_e32 v83, 0x12000, v224
	buffer_store_dwordx4 v[112:115], v83, s[24:27], 0 offen nt
	v_add_u32_e32 v82, 0x15000, v224
	buffer_store_dwordx4 v[220:223], v82, s[24:27], 0 offen nt
	ds_write_b128 v235, v[60:63]
	v_fma_mix_f32 v218, v60, 1.0, 0 op_sel_hi:[1,0,0]
	v_fma_mix_f32 v219, v60, v60, 0 op_sel_hi:[1,1,0]
	v_fma_mix_f32 v218, v60, 1.0, v218 op_sel:[1,0,0] op_sel_hi:[1,0,0]
	v_fma_mix_f32 v219, v60, v60, v219 op_sel:[1,1,0] op_sel_hi:[1,1,0]
	v_fma_mix_f32 v218, v61, 1.0, v218 op_sel_hi:[1,0,0]
	v_fma_mix_f32 v219, v61, v61, v219 op_sel_hi:[1,1,0]
	v_fma_mix_f32 v218, v61, 1.0, v218 op_sel:[1,0,0] op_sel_hi:[1,0,0]
	v_fma_mix_f32 v219, v61, v61, v219 op_sel:[1,1,0] op_sel_hi:[1,1,0]
	v_fma_mix_f32 v218, v62, 1.0, v218 op_sel_hi:[1,0,0]
	v_fma_mix_f32 v219, v62, v62, v219 op_sel_hi:[1,1,0]
	v_fma_mix_f32 v218, v62, 1.0, v218 op_sel:[1,0,0] op_sel_hi:[1,0,0]
	v_fma_mix_f32 v219, v62, v62, v219 op_sel:[1,1,0] op_sel_hi:[1,1,0]
	v_fma_mix_f32 v218, v63, 1.0, v218 op_sel_hi:[1,0,0]
	v_fma_mix_f32 v219, v63, v63, v219 op_sel_hi:[1,1,0]
	v_fma_mix_f32 v218, v63, 1.0, v218 op_sel:[1,0,0] op_sel_hi:[1,0,0]
	v_fma_mix_f32 v219, v63, v63, v219 op_sel:[1,1,0] op_sel_hi:[1,1,0]
	s_waitcnt vmcnt(14)
	v_cvt_f32_f16_e32 v72, v148
	v_cvt_f32_f16_sdwa v73, v148 dst_sel:DWORD dst_unused:UNUSED_PAD src0_sel:WORD_1
	v_cvt_f32_f16_e32 v74, v149
	v_cvt_f32_f16_sdwa v75, v149 dst_sel:DWORD dst_unused:UNUSED_PAD src0_sel:WORD_1
	v_cvt_f32_f16_e32 v80, v150
	v_cvt_f32_f16_sdwa v81, v150 dst_sel:DWORD dst_unused:UNUSED_PAD src0_sel:WORD_1
	v_cvt_f32_f16_e32 v82, v151
	v_cvt_f32_f16_sdwa v83, v151 dst_sel:DWORD dst_unused:UNUSED_PAD src0_sel:WORD_1
	v_sub_f32_e32 v72, v72, v198
	v_sub_f32_e32 v73, v73, v198
	v_sub_f32_e32 v74, v74, v198
	v_sub_f32_e32 v75, v75, v198
	v_sub_f32_e32 v80, v80, v198
	v_sub_f32_e32 v81, v81, v198
	v_sub_f32_e32 v82, v82, v198
	v_sub_f32_e32 v83, v83, v198
	v_pk_mul_f32 v[72:73], v[198:199], v[72:73] op_sel:[1,0]
	v_pk_mul_f32 v[74:75], v[198:199], v[74:75] op_sel:[1,0]
	v_pk_mul_f32 v[80:81], v[198:199], v[80:81] op_sel:[1,0]
	v_pk_mul_f32 v[82:83], v[198:199], v[82:83] op_sel:[1,0]
	v_pk_fma_f32 v[52:53], v[72:73], v[168:169], v[52:53]
	v_pk_fma_f32 v[54:55], v[74:75], v[170:171], v[54:55]
	v_pk_fma_f32 v[48:49], v[80:81], v[172:173], v[48:49]
	v_pk_fma_f32 v[50:51], v[82:83], v[174:175], v[50:51]
	v_cvt_pk_f16_f32 v52, v52, v53
	v_cvt_pk_f16_f32 v53, v54, v55
	v_cvt_pk_f16_f32 v54, v48, v49
	v_cvt_pk_f16_f32 v55, v50, v51
	ds_write_b128 v235, v[52:55] offset:64
	v_fma_mix_f32 v218, v52, 1.0, v218 op_sel_hi:[1,0,0]
	v_fma_mix_f32 v219, v52, v52, v219 op_sel_hi:[1,1,0]
	v_fma_mix_f32 v218, v52, 1.0, v218 op_sel:[1,0,0] op_sel_hi:[1,0,0]
	v_fma_mix_f32 v219, v52, v52, v219 op_sel:[1,1,0] op_sel_hi:[1,1,0]
	v_fma_mix_f32 v218, v53, 1.0, v218 op_sel_hi:[1,0,0]
	v_fma_mix_f32 v219, v53, v53, v219 op_sel_hi:[1,1,0]
	v_fma_mix_f32 v218, v53, 1.0, v218 op_sel:[1,0,0] op_sel_hi:[1,0,0]
	v_fma_mix_f32 v219, v53, v53, v219 op_sel:[1,1,0] op_sel_hi:[1,1,0]
	v_fma_mix_f32 v218, v54, 1.0, v218 op_sel_hi:[1,0,0]
	v_fma_mix_f32 v219, v54, v54, v219 op_sel_hi:[1,1,0]
	v_fma_mix_f32 v218, v54, 1.0, v218 op_sel:[1,0,0] op_sel_hi:[1,0,0]
	v_fma_mix_f32 v219, v54, v54, v219 op_sel:[1,1,0] op_sel_hi:[1,1,0]
	v_fma_mix_f32 v218, v55, 1.0, v218 op_sel_hi:[1,0,0]
	v_fma_mix_f32 v219, v55, v55, v219 op_sel_hi:[1,1,0]
	v_fma_mix_f32 v218, v55, 1.0, v218 op_sel:[1,0,0] op_sel_hi:[1,0,0]
	v_fma_mix_f32 v219, v55, v55, v219 op_sel:[1,1,0] op_sel_hi:[1,1,0]
	ds_read_b128 v[124:127], v236
	ds_read_b128 v[116:119], v236 offset:1152
	s_waitcnt vmcnt(13)
	v_cvt_f32_f16_e32 v72, v152
	v_cvt_f32_f16_sdwa v73, v152 dst_sel:DWORD dst_unused:UNUSED_PAD src0_sel:WORD_1
	v_cvt_f32_f16_e32 v74, v153
	v_cvt_f32_f16_sdwa v75, v153 dst_sel:DWORD dst_unused:UNUSED_PAD src0_sel:WORD_1
	v_cvt_f32_f16_e32 v80, v154
	v_cvt_f32_f16_sdwa v81, v154 dst_sel:DWORD dst_unused:UNUSED_PAD src0_sel:WORD_1
	v_cvt_f32_f16_e32 v82, v155
	v_cvt_f32_f16_sdwa v83, v155 dst_sel:DWORD dst_unused:UNUSED_PAD src0_sel:WORD_1
	v_sub_f32_e32 v72, v72, v200
	v_sub_f32_e32 v73, v73, v200
	v_sub_f32_e32 v74, v74, v200
	v_sub_f32_e32 v75, v75, v200
	v_sub_f32_e32 v80, v80, v200
	v_sub_f32_e32 v81, v81, v200
	v_sub_f32_e32 v82, v82, v200
	v_sub_f32_e32 v83, v83, v200
	v_pk_mul_f32 v[72:73], v[200:201], v[72:73] op_sel:[1,0]
	v_pk_mul_f32 v[74:75], v[200:201], v[74:75] op_sel:[1,0]
	v_pk_mul_f32 v[80:81], v[200:201], v[80:81] op_sel:[1,0]
	v_pk_mul_f32 v[82:83], v[200:201], v[82:83] op_sel:[1,0]
	v_pk_fma_f32 v[44:45], v[72:73], v[160:161], v[44:45]
	v_pk_fma_f32 v[46:47], v[74:75], v[162:163], v[46:47]
	v_pk_fma_f32 v[40:41], v[80:81], v[164:165], v[40:41]
	v_pk_fma_f32 v[42:43], v[82:83], v[166:167], v[42:43]
	v_cvt_pk_f16_f32 v44, v44, v45
	v_cvt_pk_f16_f32 v45, v46, v47
	v_cvt_pk_f16_f32 v46, v40, v41
	v_cvt_pk_f16_f32 v47, v42, v43
	s_waitcnt lgkmcnt(0)
	v_add_u32_e32 v83, 0x30000, v224
	buffer_store_dwordx4 v[124:127], v83, s[24:27], 0 offen nt
	v_add_u32_e32 v82, 0x33000, v224
	buffer_store_dwordx4 v[116:119], v82, s[24:27], 0 offen nt
	ds_write_b128 v235, v[44:47]
	v_fma_mix_f32 v208, v44, 1.0, 0 op_sel_hi:[1,0,0]
	v_fma_mix_f32 v209, v44, v44, 0 op_sel_hi:[1,1,0]
	v_fma_mix_f32 v208, v44, 1.0, v208 op_sel:[1,0,0] op_sel_hi:[1,0,0]
	v_fma_mix_f32 v209, v44, v44, v209 op_sel:[1,1,0] op_sel_hi:[1,1,0]
	v_fma_mix_f32 v208, v45, 1.0, v208 op_sel_hi:[1,0,0]
	v_fma_mix_f32 v209, v45, v45, v209 op_sel_hi:[1,1,0]
	v_fma_mix_f32 v208, v45, 1.0, v208 op_sel:[1,0,0] op_sel_hi:[1,0,0]
	v_fma_mix_f32 v209, v45, v45, v209 op_sel:[1,1,0] op_sel_hi:[1,1,0]
	v_fma_mix_f32 v208, v46, 1.0, v208 op_sel_hi:[1,0,0]
	v_fma_mix_f32 v209, v46, v46, v209 op_sel_hi:[1,1,0]
	v_fma_mix_f32 v208, v46, 1.0, v208 op_sel:[1,0,0] op_sel_hi:[1,0,0]
	v_fma_mix_f32 v209, v46, v46, v209 op_sel:[1,1,0] op_sel_hi:[1,1,0]
	v_fma_mix_f32 v208, v47, 1.0, v208 op_sel_hi:[1,0,0]
	v_fma_mix_f32 v209, v47, v47, v209 op_sel_hi:[1,1,0]
	v_fma_mix_f32 v208, v47, 1.0, v208 op_sel:[1,0,0] op_sel_hi:[1,0,0]
	v_fma_mix_f32 v209, v47, v47, v209 op_sel:[1,1,0] op_sel_hi:[1,1,0]
	s_waitcnt vmcnt(14)
	v_cvt_f32_f16_e32 v72, v156
	v_cvt_f32_f16_sdwa v73, v156 dst_sel:DWORD dst_unused:UNUSED_PAD src0_sel:WORD_1
	v_cvt_f32_f16_e32 v74, v157
	v_cvt_f32_f16_sdwa v75, v157 dst_sel:DWORD dst_unused:UNUSED_PAD src0_sel:WORD_1
	v_cvt_f32_f16_e32 v80, v158
	v_cvt_f32_f16_sdwa v81, v158 dst_sel:DWORD dst_unused:UNUSED_PAD src0_sel:WORD_1
	v_cvt_f32_f16_e32 v82, v159
	v_cvt_f32_f16_sdwa v83, v159 dst_sel:DWORD dst_unused:UNUSED_PAD src0_sel:WORD_1
	v_sub_f32_e32 v72, v72, v200
	v_sub_f32_e32 v73, v73, v200
	v_sub_f32_e32 v74, v74, v200
	v_sub_f32_e32 v75, v75, v200
	v_sub_f32_e32 v80, v80, v200
	v_sub_f32_e32 v81, v81, v200
	v_sub_f32_e32 v82, v82, v200
	v_sub_f32_e32 v83, v83, v200
	v_pk_mul_f32 v[72:73], v[200:201], v[72:73] op_sel:[1,0]
	v_pk_mul_f32 v[74:75], v[200:201], v[74:75] op_sel:[1,0]
	v_pk_mul_f32 v[80:81], v[200:201], v[80:81] op_sel:[1,0]
	v_pk_mul_f32 v[82:83], v[200:201], v[82:83] op_sel:[1,0]
	v_pk_fma_f32 v[36:37], v[72:73], v[168:169], v[36:37]
	v_pk_fma_f32 v[38:39], v[74:75], v[170:171], v[38:39]
	v_pk_fma_f32 v[32:33], v[80:81], v[172:173], v[32:33]
	v_pk_fma_f32 v[34:35], v[82:83], v[174:175], v[34:35]
	v_cvt_pk_f16_f32 v36, v36, v37
	v_cvt_pk_f16_f32 v37, v38, v39
	v_cvt_pk_f16_f32 v38, v32, v33
	v_cvt_pk_f16_f32 v39, v34, v35
	ds_write_b128 v235, v[36:39] offset:64
	v_fma_mix_f32 v208, v36, 1.0, v208 op_sel_hi:[1,0,0]
	v_fma_mix_f32 v209, v36, v36, v209 op_sel_hi:[1,1,0]
	v_fma_mix_f32 v208, v36, 1.0, v208 op_sel:[1,0,0] op_sel_hi:[1,0,0]
	v_fma_mix_f32 v209, v36, v36, v209 op_sel:[1,1,0] op_sel_hi:[1,1,0]
	v_fma_mix_f32 v208, v37, 1.0, v208 op_sel_hi:[1,0,0]
	v_fma_mix_f32 v209, v37, v37, v209 op_sel_hi:[1,1,0]
	v_fma_mix_f32 v208, v37, 1.0, v208 op_sel:[1,0,0] op_sel_hi:[1,0,0]
	v_fma_mix_f32 v209, v37, v37, v209 op_sel:[1,1,0] op_sel_hi:[1,1,0]
	v_fma_mix_f32 v208, v38, 1.0, v208 op_sel_hi:[1,0,0]
	v_fma_mix_f32 v209, v38, v38, v209 op_sel_hi:[1,1,0]
	v_fma_mix_f32 v208, v38, 1.0, v208 op_sel:[1,0,0] op_sel_hi:[1,0,0]
	v_fma_mix_f32 v209, v38, v38, v209 op_sel:[1,1,0] op_sel_hi:[1,1,0]
	v_fma_mix_f32 v208, v39, 1.0, v208 op_sel_hi:[1,0,0]
	v_fma_mix_f32 v209, v39, v39, v209 op_sel_hi:[1,1,0]
	v_fma_mix_f32 v208, v39, 1.0, v208 op_sel:[1,0,0] op_sel_hi:[1,0,0]
	v_fma_mix_f32 v209, v39, v39, v209 op_sel:[1,1,0] op_sel_hi:[1,1,0]
	ds_read_b128 v[128:131], v236
	ds_read_b128 v[104:107], v236 offset:1152
	s_waitcnt vmcnt(11)
	v_cvt_f32_f16_e32 v72, v212
	v_cvt_f32_f16_sdwa v73, v212 dst_sel:DWORD dst_unused:UNUSED_PAD src0_sel:WORD_1
	v_cvt_f32_f16_e32 v74, v213
	v_cvt_f32_f16_sdwa v75, v213 dst_sel:DWORD dst_unused:UNUSED_PAD src0_sel:WORD_1
	v_cvt_f32_f16_e32 v80, v214
	v_cvt_f32_f16_sdwa v81, v214 dst_sel:DWORD dst_unused:UNUSED_PAD src0_sel:WORD_1
	v_cvt_f32_f16_e32 v82, v215
	v_cvt_f32_f16_sdwa v83, v215 dst_sel:DWORD dst_unused:UNUSED_PAD src0_sel:WORD_1
	v_sub_f32_e32 v72, v72, v202
	v_sub_f32_e32 v73, v73, v202
	v_sub_f32_e32 v74, v74, v202
	v_sub_f32_e32 v75, v75, v202
	v_sub_f32_e32 v80, v80, v202
	v_sub_f32_e32 v81, v81, v202
	v_sub_f32_e32 v82, v82, v202
	v_sub_f32_e32 v83, v83, v202
	v_pk_mul_f32 v[72:73], v[202:203], v[72:73] op_sel:[1,0]
	v_pk_mul_f32 v[74:75], v[202:203], v[74:75] op_sel:[1,0]
	v_pk_mul_f32 v[80:81], v[202:203], v[80:81] op_sel:[1,0]
	v_pk_mul_f32 v[82:83], v[202:203], v[82:83] op_sel:[1,0]
	v_pk_fma_f32 v[28:29], v[72:73], v[160:161], v[28:29]
	v_pk_fma_f32 v[30:31], v[74:75], v[162:163], v[30:31]
	v_pk_fma_f32 v[24:25], v[80:81], v[164:165], v[24:25]
	v_pk_fma_f32 v[26:27], v[82:83], v[166:167], v[26:27]
	v_cvt_pk_f16_f32 v28, v28, v29
	v_cvt_pk_f16_f32 v29, v30, v31
	v_cvt_pk_f16_f32 v30, v24, v25
	v_cvt_pk_f16_f32 v31, v26, v27
	s_waitcnt lgkmcnt(0)
	v_add_u32_e32 v83, 0x36000, v224
	buffer_store_dwordx4 v[128:131], v83, s[24:27], 0 offen nt
	v_add_u32_e32 v82, 0x39000, v224
	buffer_store_dwordx4 v[104:107], v82, s[24:27], 0 offen nt
	ds_write_b128 v235, v[28:31]
	v_fma_mix_f32 v210, v28, 1.0, 0 op_sel_hi:[1,0,0]
	v_fma_mix_f32 v211, v28, v28, 0 op_sel_hi:[1,1,0]
	v_fma_mix_f32 v210, v28, 1.0, v210 op_sel:[1,0,0] op_sel_hi:[1,0,0]
	v_fma_mix_f32 v211, v28, v28, v211 op_sel:[1,1,0] op_sel_hi:[1,1,0]
	v_fma_mix_f32 v210, v29, 1.0, v210 op_sel_hi:[1,0,0]
	v_fma_mix_f32 v211, v29, v29, v211 op_sel_hi:[1,1,0]
	v_fma_mix_f32 v210, v29, 1.0, v210 op_sel:[1,0,0] op_sel_hi:[1,0,0]
	v_fma_mix_f32 v211, v29, v29, v211 op_sel:[1,1,0] op_sel_hi:[1,1,0]
	v_fma_mix_f32 v210, v30, 1.0, v210 op_sel_hi:[1,0,0]
	v_fma_mix_f32 v211, v30, v30, v211 op_sel_hi:[1,1,0]
	v_fma_mix_f32 v210, v30, 1.0, v210 op_sel:[1,0,0] op_sel_hi:[1,0,0]
	v_fma_mix_f32 v211, v30, v30, v211 op_sel:[1,1,0] op_sel_hi:[1,1,0]
	v_fma_mix_f32 v210, v31, 1.0, v210 op_sel_hi:[1,0,0]
	v_fma_mix_f32 v211, v31, v31, v211 op_sel_hi:[1,1,0]
	v_fma_mix_f32 v210, v31, 1.0, v210 op_sel:[1,0,0] op_sel_hi:[1,0,0]
	v_fma_mix_f32 v211, v31, v31, v211 op_sel:[1,1,0] op_sel_hi:[1,1,0]
	s_waitcnt vmcnt(12)
	v_cvt_f32_f16_e32 v72, v144
	v_cvt_f32_f16_sdwa v73, v144 dst_sel:DWORD dst_unused:UNUSED_PAD src0_sel:WORD_1
	v_cvt_f32_f16_e32 v74, v145
	v_cvt_f32_f16_sdwa v75, v145 dst_sel:DWORD dst_unused:UNUSED_PAD src0_sel:WORD_1
	v_cvt_f32_f16_e32 v80, v146
	v_cvt_f32_f16_sdwa v81, v146 dst_sel:DWORD dst_unused:UNUSED_PAD src0_sel:WORD_1
	v_cvt_f32_f16_e32 v82, v147
	v_cvt_f32_f16_sdwa v83, v147 dst_sel:DWORD dst_unused:UNUSED_PAD src0_sel:WORD_1
	v_sub_f32_e32 v72, v72, v202
	v_sub_f32_e32 v73, v73, v202
	v_sub_f32_e32 v74, v74, v202
	v_sub_f32_e32 v75, v75, v202
	v_sub_f32_e32 v80, v80, v202
	v_sub_f32_e32 v81, v81, v202
	v_sub_f32_e32 v82, v82, v202
	v_sub_f32_e32 v83, v83, v202
	v_pk_mul_f32 v[72:73], v[202:203], v[72:73] op_sel:[1,0]
	v_pk_mul_f32 v[74:75], v[202:203], v[74:75] op_sel:[1,0]
	v_pk_mul_f32 v[80:81], v[202:203], v[80:81] op_sel:[1,0]
	v_pk_mul_f32 v[82:83], v[202:203], v[82:83] op_sel:[1,0]
	v_pk_fma_f32 v[20:21], v[72:73], v[168:169], v[20:21]
	v_pk_fma_f32 v[22:23], v[74:75], v[170:171], v[22:23]
	v_pk_fma_f32 v[16:17], v[80:81], v[172:173], v[16:17]
	v_pk_fma_f32 v[18:19], v[82:83], v[174:175], v[18:19]
	v_cvt_pk_f16_f32 v20, v20, v21
	v_cvt_pk_f16_f32 v21, v22, v23
	v_cvt_pk_f16_f32 v22, v16, v17
	v_cvt_pk_f16_f32 v23, v18, v19
	ds_write_b128 v235, v[20:23] offset:64
	v_fma_mix_f32 v210, v20, 1.0, v210 op_sel_hi:[1,0,0]
	v_fma_mix_f32 v211, v20, v20, v211 op_sel_hi:[1,1,0]
	v_fma_mix_f32 v210, v20, 1.0, v210 op_sel:[1,0,0] op_sel_hi:[1,0,0]
	v_fma_mix_f32 v211, v20, v20, v211 op_sel:[1,1,0] op_sel_hi:[1,1,0]
	v_fma_mix_f32 v210, v21, 1.0, v210 op_sel_hi:[1,0,0]
	v_fma_mix_f32 v211, v21, v21, v211 op_sel_hi:[1,1,0]
	v_fma_mix_f32 v210, v21, 1.0, v210 op_sel:[1,0,0] op_sel_hi:[1,0,0]
	v_fma_mix_f32 v211, v21, v21, v211 op_sel:[1,1,0] op_sel_hi:[1,1,0]
	v_fma_mix_f32 v210, v22, 1.0, v210 op_sel_hi:[1,0,0]
	v_fma_mix_f32 v211, v22, v22, v211 op_sel_hi:[1,1,0]
	v_fma_mix_f32 v210, v22, 1.0, v210 op_sel:[1,0,0] op_sel_hi:[1,0,0]
	v_fma_mix_f32 v211, v22, v22, v211 op_sel:[1,1,0] op_sel_hi:[1,1,0]
	v_fma_mix_f32 v210, v23, 1.0, v210 op_sel_hi:[1,0,0]
	v_fma_mix_f32 v211, v23, v23, v211 op_sel_hi:[1,1,0]
	v_fma_mix_f32 v210, v23, 1.0, v210 op_sel:[1,0,0] op_sel_hi:[1,0,0]
	v_fma_mix_f32 v211, v23, v23, v211 op_sel:[1,1,0] op_sel_hi:[1,1,0]
	ds_read_b128 v[240:243], v236
	ds_read_b128 v[96:99], v236 offset:1152
	s_waitcnt vmcnt(11)
	v_cvt_f32_f16_e32 v72, v132
	v_cvt_f32_f16_sdwa v73, v132 dst_sel:DWORD dst_unused:UNUSED_PAD src0_sel:WORD_1
	v_cvt_f32_f16_e32 v74, v133
	v_cvt_f32_f16_sdwa v75, v133 dst_sel:DWORD dst_unused:UNUSED_PAD src0_sel:WORD_1
	v_cvt_f32_f16_e32 v80, v134
	v_cvt_f32_f16_sdwa v81, v134 dst_sel:DWORD dst_unused:UNUSED_PAD src0_sel:WORD_1
	v_cvt_f32_f16_e32 v82, v135
	v_cvt_f32_f16_sdwa v83, v135 dst_sel:DWORD dst_unused:UNUSED_PAD src0_sel:WORD_1
	v_sub_f32_e32 v72, v72, v204
	v_sub_f32_e32 v73, v73, v204
	v_sub_f32_e32 v74, v74, v204
	v_sub_f32_e32 v75, v75, v204
	v_sub_f32_e32 v80, v80, v204
	v_sub_f32_e32 v81, v81, v204
	v_sub_f32_e32 v82, v82, v204
	v_sub_f32_e32 v83, v83, v204
	v_pk_mul_f32 v[72:73], v[204:205], v[72:73] op_sel:[1,0]
	v_pk_mul_f32 v[74:75], v[204:205], v[74:75] op_sel:[1,0]
	v_pk_mul_f32 v[80:81], v[204:205], v[80:81] op_sel:[1,0]
	v_pk_mul_f32 v[82:83], v[204:205], v[82:83] op_sel:[1,0]
	v_pk_fma_f32 v[12:13], v[72:73], v[160:161], v[12:13]
	v_pk_fma_f32 v[14:15], v[74:75], v[162:163], v[14:15]
	v_pk_fma_f32 v[8:9], v[80:81], v[164:165], v[8:9]
	v_pk_fma_f32 v[10:11], v[82:83], v[166:167], v[10:11]
	v_cvt_pk_f16_f32 v12, v12, v13
	v_cvt_pk_f16_f32 v13, v14, v15
	v_cvt_pk_f16_f32 v14, v8, v9
	v_cvt_pk_f16_f32 v15, v10, v11
	s_waitcnt lgkmcnt(0)
	v_add_u32_e32 v83, 0x3c000, v224
	buffer_store_dwordx4 v[240:243], v83, s[24:27], 0 offen nt
	v_add_u32_e32 v82, 0x3f000, v224
	buffer_store_dwordx4 v[96:99], v82, s[24:27], 0 offen nt
	ds_write_b128 v235, v[12:15]
	v_fma_mix_f32 v244, v12, 1.0, 0 op_sel_hi:[1,0,0]
	v_fma_mix_f32 v245, v12, v12, 0 op_sel_hi:[1,1,0]
	v_fma_mix_f32 v244, v12, 1.0, v244 op_sel:[1,0,0] op_sel_hi:[1,0,0]
	v_fma_mix_f32 v245, v12, v12, v245 op_sel:[1,1,0] op_sel_hi:[1,1,0]
	v_fma_mix_f32 v244, v13, 1.0, v244 op_sel_hi:[1,0,0]
	v_fma_mix_f32 v245, v13, v13, v245 op_sel_hi:[1,1,0]
	v_fma_mix_f32 v244, v13, 1.0, v244 op_sel:[1,0,0] op_sel_hi:[1,0,0]
	v_fma_mix_f32 v245, v13, v13, v245 op_sel:[1,1,0] op_sel_hi:[1,1,0]
	v_fma_mix_f32 v244, v14, 1.0, v244 op_sel_hi:[1,0,0]
	v_fma_mix_f32 v245, v14, v14, v245 op_sel_hi:[1,1,0]
	v_fma_mix_f32 v244, v14, 1.0, v244 op_sel:[1,0,0] op_sel_hi:[1,0,0]
	v_fma_mix_f32 v245, v14, v14, v245 op_sel:[1,1,0] op_sel_hi:[1,1,0]
	v_fma_mix_f32 v244, v15, 1.0, v244 op_sel_hi:[1,0,0]
	v_fma_mix_f32 v245, v15, v15, v245 op_sel_hi:[1,1,0]
	v_fma_mix_f32 v244, v15, 1.0, v244 op_sel:[1,0,0] op_sel_hi:[1,0,0]
	v_fma_mix_f32 v245, v15, v15, v245 op_sel:[1,1,0] op_sel_hi:[1,1,0]
	s_waitcnt vmcnt(12)
	v_cvt_f32_f16_e32 v72, v88
	v_cvt_f32_f16_sdwa v73, v88 dst_sel:DWORD dst_unused:UNUSED_PAD src0_sel:WORD_1
	v_cvt_f32_f16_e32 v74, v89
	v_cvt_f32_f16_sdwa v75, v89 dst_sel:DWORD dst_unused:UNUSED_PAD src0_sel:WORD_1
	v_cvt_f32_f16_e32 v80, v90
	v_cvt_f32_f16_sdwa v81, v90 dst_sel:DWORD dst_unused:UNUSED_PAD src0_sel:WORD_1
	v_cvt_f32_f16_e32 v82, v91
	v_cvt_f32_f16_sdwa v83, v91 dst_sel:DWORD dst_unused:UNUSED_PAD src0_sel:WORD_1
	v_sub_f32_e32 v72, v72, v204
	v_sub_f32_e32 v73, v73, v204
	v_sub_f32_e32 v74, v74, v204
	v_sub_f32_e32 v75, v75, v204
	v_sub_f32_e32 v80, v80, v204
	v_sub_f32_e32 v81, v81, v204
	v_sub_f32_e32 v82, v82, v204
	v_sub_f32_e32 v83, v83, v204
	v_pk_mul_f32 v[72:73], v[204:205], v[72:73] op_sel:[1,0]
	v_pk_mul_f32 v[74:75], v[204:205], v[74:75] op_sel:[1,0]
	v_pk_mul_f32 v[80:81], v[204:205], v[80:81] op_sel:[1,0]
	v_pk_mul_f32 v[82:83], v[204:205], v[82:83] op_sel:[1,0]
	v_pk_fma_f32 v[4:5], v[72:73], v[168:169], v[4:5]
	v_pk_fma_f32 v[6:7], v[74:75], v[170:171], v[6:7]
	v_pk_fma_f32 v[0:1], v[80:81], v[172:173], v[0:1]
	v_pk_fma_f32 v[2:3], v[82:83], v[174:175], v[2:3]
	v_cvt_pk_f16_f32 v4, v4, v5
	v_cvt_pk_f16_f32 v5, v6, v7
	v_cvt_pk_f16_f32 v6, v0, v1
	v_cvt_pk_f16_f32 v7, v2, v3
	ds_write_b128 v235, v[4:7] offset:64
	v_fma_mix_f32 v244, v4, 1.0, v244 op_sel_hi:[1,0,0]
	v_fma_mix_f32 v245, v4, v4, v245 op_sel_hi:[1,1,0]
	v_fma_mix_f32 v244, v4, 1.0, v244 op_sel:[1,0,0] op_sel_hi:[1,0,0]
	v_fma_mix_f32 v245, v4, v4, v245 op_sel:[1,1,0] op_sel_hi:[1,1,0]
	v_fma_mix_f32 v244, v5, 1.0, v244 op_sel_hi:[1,0,0]
	v_fma_mix_f32 v245, v5, v5, v245 op_sel_hi:[1,1,0]
	v_fma_mix_f32 v244, v5, 1.0, v244 op_sel:[1,0,0] op_sel_hi:[1,0,0]
	v_fma_mix_f32 v245, v5, v5, v245 op_sel:[1,1,0] op_sel_hi:[1,1,0]
	v_fma_mix_f32 v244, v6, 1.0, v244 op_sel_hi:[1,0,0]
	v_fma_mix_f32 v245, v6, v6, v245 op_sel_hi:[1,1,0]
	v_fma_mix_f32 v244, v6, 1.0, v244 op_sel:[1,0,0] op_sel_hi:[1,0,0]
	v_fma_mix_f32 v245, v6, v6, v245 op_sel:[1,1,0] op_sel_hi:[1,1,0]
	v_fma_mix_f32 v244, v7, 1.0, v244 op_sel_hi:[1,0,0]
	v_fma_mix_f32 v245, v7, v7, v245 op_sel_hi:[1,1,0]
	v_fma_mix_f32 v244, v7, 1.0, v244 op_sel:[1,0,0] op_sel_hi:[1,0,0]
	v_fma_mix_f32 v245, v7, v7, v245 op_sel:[1,1,0] op_sel_hi:[1,1,0]
	ds_read_b128 v[108:111], v236
	ds_read_b128 v[100:103], v236 offset:1152
	s_waitcnt lgkmcnt(0)
	v_add_u32_e32 v83, 0x42000, v224
	buffer_store_dwordx4 v[108:111], v83, s[24:27], 0 offen nt
	v_add_u32_e32 v82, 0x45000, v224
	buffer_store_dwordx4 v[100:103], v82, s[24:27], 0 offen nt
	v_xor_b32_e32 v225, 16, v234
	v_lshlrev_b32_e32 v225, 2, v225
	v_xor_b32_e32 v246, 32, v234
	v_lshlrev_b32_e32 v246, 2, v246
	ds_bpermute_b32 v92, v225, v206
	ds_bpermute_b32 v93, v225, v207
	ds_bpermute_b32 v94, v225, v140
	ds_bpermute_b32 v95, v225, v141
	ds_bpermute_b32 v120, v225, v142
	ds_bpermute_b32 v121, v225, v143
	ds_bpermute_b32 v122, v225, v216
	ds_bpermute_b32 v123, v225, v217
	s_waitcnt lgkmcnt(0)
	v_pk_add_f32 v[206:207], v[206:207], v[92:93]
	v_pk_add_f32 v[140:141], v[140:141], v[94:95]
	v_pk_add_f32 v[142:143], v[142:143], v[120:121]
	v_pk_add_f32 v[216:217], v[216:217], v[122:123]
	ds_bpermute_b32 v92, v225, v218
	ds_bpermute_b32 v93, v225, v219
	ds_bpermute_b32 v94, v225, v208
	ds_bpermute_b32 v95, v225, v209
	ds_bpermute_b32 v120, v225, v210
	ds_bpermute_b32 v121, v225, v211
	ds_bpermute_b32 v122, v225, v244
	ds_bpermute_b32 v123, v225, v245
	s_waitcnt lgkmcnt(0)
	v_pk_add_f32 v[218:219], v[218:219], v[92:93]
	v_pk_add_f32 v[208:209], v[208:209], v[94:95]
	v_pk_add_f32 v[210:211], v[210:211], v[120:121]
	v_pk_add_f32 v[244:245], v[244:245], v[122:123]
	ds_bpermute_b32 v92, v246, v206
	ds_bpermute_b32 v93, v246, v207
	ds_bpermute_b32 v94, v246, v140
	ds_bpermute_b32 v95, v246, v141
	ds_bpermute_b32 v120, v246, v142
	ds_bpermute_b32 v121, v246, v143
	ds_bpermute_b32 v122, v246, v216
	ds_bpermute_b32 v123, v246, v217
	s_waitcnt lgkmcnt(0)
	v_pk_add_f32 v[206:207], v[206:207], v[92:93]
	v_pk_add_f32 v[140:141], v[140:141], v[94:95]
	v_pk_add_f32 v[142:143], v[142:143], v[120:121]
	v_pk_add_f32 v[216:217], v[216:217], v[122:123]
	ds_bpermute_b32 v92, v246, v218
	ds_bpermute_b32 v93, v246, v219
	ds_bpermute_b32 v94, v246, v208
	ds_bpermute_b32 v95, v246, v209
	ds_bpermute_b32 v120, v246, v210
	ds_bpermute_b32 v121, v246, v211
	ds_bpermute_b32 v122, v246, v244
	ds_bpermute_b32 v123, v246, v245
	s_waitcnt lgkmcnt(0)
	v_pk_add_f32 v[218:219], v[218:219], v[92:93]
	v_pk_add_f32 v[208:209], v[208:209], v[94:95]
	v_pk_add_f32 v[210:211], v[210:211], v[120:121]
	v_pk_add_f32 v[244:245], v[244:245], v[122:123]
	s_mov_b64 exec, 0xffff
	global_store_dwordx2 v190, v[206:207], s[100:101] offset:0
	global_store_dwordx2 v190, v[140:141], s[100:101] offset:128
	global_store_dwordx2 v190, v[142:143], s[100:101] offset:256
	global_store_dwordx2 v190, v[216:217], s[100:101] offset:384
	global_store_dwordx2 v190, v[218:219], s[100:101] offset:1024
	global_store_dwordx2 v190, v[208:209], s[100:101] offset:1152
	global_store_dwordx2 v190, v[210:211], s[100:101] offset:1280
	global_store_dwordx2 v190, v[244:245], s[100:101] offset:1408
	s_mov_b64 exec, -1
	s_mov_b32 s83, s81
	s_mov_b32 s84, s82
	s_mov_b64 s[40:41], s[0:1]
	s_mov_b64 s[38:39], s[8:9]
	s_mov_b64 vcc, s[6:7]
	s_cbranch_vccz .LBB10_12
	s_waitcnt vmcnt(0)
	s_cmpk_gt_u32 s44, 0xff
	s_cbranch_scc1 .LBB10_31
	s_barrier
